# v14 + first K-iteration peeled with C=0 in down/in-proj/out GEMMs + prologue weight transposes software-pipelined (32 loads in flight per wave)
# baseline (speedup 1.0000x reference)
.LBB0_26:
	v_lshl_add_u64 v[38:39], v[2:3], 0, s[38:39]
	v_add_co_u32_e32 v40, vcc, 0x1000, v38
	global_load_dword v100, v[38:39], off nt
	s_nop 0
	v_addc_co_u32_e32 v41, vcc, 0, v39, vcc
	v_add_co_u32_e32 v54, vcc, 0x2000, v38
	global_load_dword v101, v[40:41], off nt
	s_nop 0
	v_addc_co_u32_e32 v55, vcc, 0, v39, vcc
	v_add_co_u32_e32 v40, vcc, 0x3000, v38
	s_add_u32 s38, s38, 0x10000
	s_nop 0
	v_addc_co_u32_e32 v41, vcc, 0, v39, vcc
	v_add_co_u32_e32 v56, vcc, 0x4000, v38
	global_load_dword v102, v[54:55], off nt
	global_load_dword v103, v[40:41], off nt
	v_addc_co_u32_e32 v57, vcc, 0, v39, vcc
	v_add_co_u32_e32 v40, vcc, 0x5000, v38
	s_addc_u32 s39, s39, 0
	s_nop 0
	v_addc_co_u32_e32 v41, vcc, 0, v39, vcc
	v_add_co_u32_e32 v54, vcc, 0x6000, v38
	global_load_dword v104, v[56:57], off nt
	global_load_dword v105, v[40:41], off nt
	v_addc_co_u32_e32 v55, vcc, 0, v39, vcc
	v_add_co_u32_e32 v40, vcc, 0x7000, v38
	s_nop 0
	v_addc_co_u32_e32 v41, vcc, 0, v39, vcc
	v_add_co_u32_e32 v56, vcc, 0x8000, v38
	global_load_dword v106, v[54:55], off nt
	global_load_dword v107, v[40:41], off nt
	v_addc_co_u32_e32 v57, vcc, 0, v39, vcc
	v_add_co_u32_e32 v40, vcc, 0x9000, v38
	s_nop 1
	v_addc_co_u32_e32 v41, vcc, 0, v39, vcc
	v_add_co_u32_e32 v54, vcc, 0xa000, v38
	global_load_dword v108, v[56:57], off nt
	global_load_dword v109, v[40:41], off nt
	v_addc_co_u32_e32 v55, vcc, 0, v39, vcc
	v_add_co_u32_e32 v40, vcc, 0xb000, v38
	s_nop 1
	v_addc_co_u32_e32 v41, vcc, 0, v39, vcc
	v_add_co_u32_e32 v56, vcc, 0xc000, v38
	global_load_dword v110, v[54:55], off nt
	global_load_dword v111, v[40:41], off nt
	v_addc_co_u32_e32 v57, vcc, 0, v39, vcc
	v_add_co_u32_e32 v40, vcc, 0xd000, v38
	s_nop 1
	v_addc_co_u32_e32 v41, vcc, 0, v39, vcc
	v_add_co_u32_e32 v54, vcc, 0xe000, v38
	global_load_dword v112, v[56:57], off nt
	s_nop 0
	global_load_dword v113, v[40:41], off nt
	v_addc_co_u32_e32 v55, vcc, 0, v39, vcc
	v_add_co_u32_e32 v38, vcc, 0xf000, v38
	s_nop 1
	v_addc_co_u32_e32 v39, vcc, 0, v39, vcc
	global_load_dword v114, v[54:55], off nt
	s_nop 0
	global_load_dword v115, v[38:39], off nt
	v_lshl_add_u64 v[38:39], v[2:3], 0, s[38:39]
	v_add_co_u32_e32 v40, vcc, 0x1000, v38
	global_load_dword v116, v[38:39], off nt
	s_nop 0
	v_addc_co_u32_e32 v41, vcc, 0, v39, vcc
	v_add_co_u32_e32 v54, vcc, 0x2000, v38
	global_load_dword v117, v[40:41], off nt
	s_nop 0
	v_addc_co_u32_e32 v55, vcc, 0, v39, vcc
	v_add_co_u32_e32 v40, vcc, 0x3000, v38
	s_add_u32 s38, s38, 0x10000
	s_nop 0
	v_addc_co_u32_e32 v41, vcc, 0, v39, vcc
	v_add_co_u32_e32 v56, vcc, 0x4000, v38
	global_load_dword v118, v[54:55], off nt
	global_load_dword v119, v[40:41], off nt
	v_addc_co_u32_e32 v57, vcc, 0, v39, vcc
	v_add_co_u32_e32 v40, vcc, 0x5000, v38
	s_addc_u32 s39, s39, 0
	s_nop 0
	v_addc_co_u32_e32 v41, vcc, 0, v39, vcc
	v_add_co_u32_e32 v54, vcc, 0x6000, v38
	global_load_dword v120, v[56:57], off nt
	global_load_dword v121, v[40:41], off nt
	v_addc_co_u32_e32 v55, vcc, 0, v39, vcc
	v_add_co_u32_e32 v40, vcc, 0x7000, v38
	s_nop 0
	v_addc_co_u32_e32 v41, vcc, 0, v39, vcc
	v_add_co_u32_e32 v56, vcc, 0x8000, v38
	global_load_dword v122, v[54:55], off nt
	global_load_dword v123, v[40:41], off nt
	v_addc_co_u32_e32 v57, vcc, 0, v39, vcc
	v_add_co_u32_e32 v40, vcc, 0x9000, v38
	s_nop 1
	v_addc_co_u32_e32 v41, vcc, 0, v39, vcc
	v_add_co_u32_e32 v54, vcc, 0xa000, v38
	global_load_dword v124, v[56:57], off nt
	global_load_dword v125, v[40:41], off nt
	v_addc_co_u32_e32 v55, vcc, 0, v39, vcc
	v_add_co_u32_e32 v40, vcc, 0xb000, v38
	s_nop 1
	v_addc_co_u32_e32 v41, vcc, 0, v39, vcc
	v_add_co_u32_e32 v56, vcc, 0xc000, v38
	global_load_dword v126, v[54:55], off nt
	global_load_dword v127, v[40:41], off nt
	v_addc_co_u32_e32 v57, vcc, 0, v39, vcc
	v_add_co_u32_e32 v40, vcc, 0xd000, v38
	s_nop 1
	v_addc_co_u32_e32 v41, vcc, 0, v39, vcc
	v_add_co_u32_e32 v54, vcc, 0xe000, v38
	global_load_dword v128, v[56:57], off nt
	s_nop 0
	global_load_dword v129, v[40:41], off nt
	v_addc_co_u32_e32 v55, vcc, 0, v39, vcc
	v_add_co_u32_e32 v38, vcc, 0xf000, v38
	s_nop 1
	v_addc_co_u32_e32 v39, vcc, 0, v39, vcc
	global_load_dword v130, v[54:55], off nt
	s_nop 0
	global_load_dword v131, v[38:39], off nt
	v_add_u32_e32 v39, 0x400, v4
	v_add_u32_e32 v54, 0x800, v4
	v_add_u32_e32 v55, 0xc00, v4
	s_waitcnt vmcnt(30)
	ds_write2_b32 v4, v100, v101 offset1:65
	s_waitcnt vmcnt(28)
	ds_write2_b32 v4, v102, v103 offset0:130 offset1:195
	v_add_u32_e32 v4, 0x1040, v4
	s_waitcnt vmcnt(26)
	ds_write2_b32 v39, v104, v105 offset0:4 offset1:69
	s_waitcnt vmcnt(24)
	ds_write2_b32 v39, v106, v107 offset0:134 offset1:199
	s_waitcnt vmcnt(22)
	ds_write2_b32 v54, v108, v109 offset0:8 offset1:73
	s_waitcnt vmcnt(20)
	ds_write2_b32 v54, v110, v111 offset0:138 offset1:203
	s_waitcnt vmcnt(18)
	ds_write2_b32 v55, v112, v113 offset0:12 offset1:77
	s_waitcnt vmcnt(16)
	ds_write2_b32 v55, v114, v115 offset0:142 offset1:207
	v_lshl_add_u64 v[38:39], v[2:3], 0, s[38:39]
	v_add_co_u32_e32 v40, vcc, 0x1000, v38
	global_load_dword v100, v[38:39], off nt
	s_nop 0
	v_addc_co_u32_e32 v41, vcc, 0, v39, vcc
	v_add_co_u32_e32 v54, vcc, 0x2000, v38
	global_load_dword v101, v[40:41], off nt
	s_nop 0
	v_addc_co_u32_e32 v55, vcc, 0, v39, vcc
	v_add_co_u32_e32 v40, vcc, 0x3000, v38
	s_add_u32 s38, s38, 0x10000
	s_nop 0
	v_addc_co_u32_e32 v41, vcc, 0, v39, vcc
	v_add_co_u32_e32 v56, vcc, 0x4000, v38
	global_load_dword v102, v[54:55], off nt
	global_load_dword v103, v[40:41], off nt
	v_addc_co_u32_e32 v57, vcc, 0, v39, vcc
	v_add_co_u32_e32 v40, vcc, 0x5000, v38
	s_addc_u32 s39, s39, 0
	s_nop 0
	v_addc_co_u32_e32 v41, vcc, 0, v39, vcc
	v_add_co_u32_e32 v54, vcc, 0x6000, v38
	global_load_dword v104, v[56:57], off nt
	global_load_dword v105, v[40:41], off nt
	v_addc_co_u32_e32 v55, vcc, 0, v39, vcc
	v_add_co_u32_e32 v40, vcc, 0x7000, v38
	s_nop 0
	v_addc_co_u32_e32 v41, vcc, 0, v39, vcc
	v_add_co_u32_e32 v56, vcc, 0x8000, v38
	global_load_dword v106, v[54:55], off nt
	global_load_dword v107, v[40:41], off nt
	v_addc_co_u32_e32 v57, vcc, 0, v39, vcc
	v_add_co_u32_e32 v40, vcc, 0x9000, v38
	s_nop 1
	v_addc_co_u32_e32 v41, vcc, 0, v39, vcc
	v_add_co_u32_e32 v54, vcc, 0xa000, v38
	global_load_dword v108, v[56:57], off nt
	global_load_dword v109, v[40:41], off nt
	v_addc_co_u32_e32 v55, vcc, 0, v39, vcc
	v_add_co_u32_e32 v40, vcc, 0xb000, v38
	s_nop 1
	v_addc_co_u32_e32 v41, vcc, 0, v39, vcc
	v_add_co_u32_e32 v56, vcc, 0xc000, v38
	global_load_dword v110, v[54:55], off nt
	global_load_dword v111, v[40:41], off nt
	v_addc_co_u32_e32 v57, vcc, 0, v39, vcc
	v_add_co_u32_e32 v40, vcc, 0xd000, v38
	s_nop 1
	v_addc_co_u32_e32 v41, vcc, 0, v39, vcc
	v_add_co_u32_e32 v54, vcc, 0xe000, v38
	global_load_dword v112, v[56:57], off nt
	s_nop 0
	global_load_dword v113, v[40:41], off nt
	v_addc_co_u32_e32 v55, vcc, 0, v39, vcc
	v_add_co_u32_e32 v38, vcc, 0xf000, v38
	s_nop 1
	v_addc_co_u32_e32 v39, vcc, 0, v39, vcc
	global_load_dword v114, v[54:55], off nt
	s_nop 0
	global_load_dword v115, v[38:39], off nt
	v_add_u32_e32 v39, 0x400, v4
	v_add_u32_e32 v54, 0x800, v4
	v_add_u32_e32 v55, 0xc00, v4
	s_waitcnt vmcnt(30)
	ds_write2_b32 v4, v116, v117 offset1:65
	s_waitcnt vmcnt(28)
	ds_write2_b32 v4, v118, v119 offset0:130 offset1:195
	v_add_u32_e32 v4, 0x1040, v4
	s_waitcnt vmcnt(26)
	ds_write2_b32 v39, v120, v121 offset0:4 offset1:69
	s_waitcnt vmcnt(24)
	ds_write2_b32 v39, v122, v123 offset0:134 offset1:199
	s_waitcnt vmcnt(22)
	ds_write2_b32 v54, v124, v125 offset0:8 offset1:73
	s_waitcnt vmcnt(20)
	ds_write2_b32 v54, v126, v127 offset0:138 offset1:203
	s_waitcnt vmcnt(18)
	ds_write2_b32 v55, v128, v129 offset0:12 offset1:77
	s_waitcnt vmcnt(16)
	ds_write2_b32 v55, v130, v131 offset0:142 offset1:207
	v_lshl_add_u64 v[38:39], v[2:3], 0, s[38:39]
	v_add_co_u32_e32 v40, vcc, 0x1000, v38
	global_load_dword v116, v[38:39], off nt
	s_nop 0
	v_addc_co_u32_e32 v41, vcc, 0, v39, vcc
	v_add_co_u32_e32 v54, vcc, 0x2000, v38
	global_load_dword v117, v[40:41], off nt
	s_nop 0
	v_addc_co_u32_e32 v55, vcc, 0, v39, vcc
	v_add_co_u32_e32 v40, vcc, 0x3000, v38
	s_add_u32 s38, s38, 0x10000
	s_nop 0
	v_addc_co_u32_e32 v41, vcc, 0, v39, vcc
	v_add_co_u32_e32 v56, vcc, 0x4000, v38
	global_load_dword v118, v[54:55], off nt
	global_load_dword v119, v[40:41], off nt
	v_addc_co_u32_e32 v57, vcc, 0, v39, vcc
	v_add_co_u32_e32 v40, vcc, 0x5000, v38
	s_addc_u32 s39, s39, 0
	s_nop 0
	v_addc_co_u32_e32 v41, vcc, 0, v39, vcc
	v_add_co_u32_e32 v54, vcc, 0x6000, v38
	global_load_dword v120, v[56:57], off nt
	global_load_dword v121, v[40:41], off nt
	v_addc_co_u32_e32 v55, vcc, 0, v39, vcc
	v_add_co_u32_e32 v40, vcc, 0x7000, v38
	s_nop 0
	v_addc_co_u32_e32 v41, vcc, 0, v39, vcc
	v_add_co_u32_e32 v56, vcc, 0x8000, v38
	global_load_dword v122, v[54:55], off nt
	global_load_dword v123, v[40:41], off nt
	v_addc_co_u32_e32 v57, vcc, 0, v39, vcc
	v_add_co_u32_e32 v40, vcc, 0x9000, v38
	s_nop 1
	v_addc_co_u32_e32 v41, vcc, 0, v39, vcc
	v_add_co_u32_e32 v54, vcc, 0xa000, v38
	global_load_dword v124, v[56:57], off nt
	global_load_dword v125, v[40:41], off nt
	v_addc_co_u32_e32 v55, vcc, 0, v39, vcc
	v_add_co_u32_e32 v40, vcc, 0xb000, v38
	s_nop 1
	v_addc_co_u32_e32 v41, vcc, 0, v39, vcc
	v_add_co_u32_e32 v56, vcc, 0xc000, v38
	global_load_dword v126, v[54:55], off nt
	global_load_dword v127, v[40:41], off nt
	v_addc_co_u32_e32 v57, vcc, 0, v39, vcc
	v_add_co_u32_e32 v40, vcc, 0xd000, v38
	s_nop 1
	v_addc_co_u32_e32 v41, vcc, 0, v39, vcc
	v_add_co_u32_e32 v54, vcc, 0xe000, v38
	global_load_dword v128, v[56:57], off nt
	s_nop 0
	global_load_dword v129, v[40:41], off nt
	v_addc_co_u32_e32 v55, vcc, 0, v39, vcc
	v_add_co_u32_e32 v38, vcc, 0xf000, v38
	s_nop 1
	v_addc_co_u32_e32 v39, vcc, 0, v39, vcc
	global_load_dword v130, v[54:55], off nt
	s_nop 0
	global_load_dword v131, v[38:39], off nt
	v_add_u32_e32 v39, 0x400, v4
	v_add_u32_e32 v54, 0x800, v4
	v_add_u32_e32 v55, 0xc00, v4
	s_waitcnt vmcnt(30)
	ds_write2_b32 v4, v100, v101 offset1:65
	s_waitcnt vmcnt(28)
	ds_write2_b32 v4, v102, v103 offset0:130 offset1:195
	v_add_u32_e32 v4, 0x1040, v4
	s_waitcnt vmcnt(26)
	ds_write2_b32 v39, v104, v105 offset0:4 offset1:69
	s_waitcnt vmcnt(24)
	ds_write2_b32 v39, v106, v107 offset0:134 offset1:199
	s_waitcnt vmcnt(22)
	ds_write2_b32 v54, v108, v109 offset0:8 offset1:73
	s_waitcnt vmcnt(20)
	ds_write2_b32 v54, v110, v111 offset0:138 offset1:203
	s_waitcnt vmcnt(18)
	ds_write2_b32 v55, v112, v113 offset0:12 offset1:77
	s_waitcnt vmcnt(16)
	ds_write2_b32 v55, v114, v115 offset0:142 offset1:207
	v_add_u32_e32 v39, 0x400, v4
	v_add_u32_e32 v54, 0x800, v4
	v_add_u32_e32 v55, 0xc00, v4
	s_waitcnt vmcnt(14)
	ds_write2_b32 v4, v116, v117 offset1:65
	s_waitcnt vmcnt(12)
	ds_write2_b32 v4, v118, v119 offset0:130 offset1:195
	v_add_u32_e32 v4, 0x1040, v4
	s_waitcnt vmcnt(10)
	ds_write2_b32 v39, v120, v121 offset0:4 offset1:69
	s_waitcnt vmcnt(8)
	ds_write2_b32 v39, v122, v123 offset0:134 offset1:199
	s_waitcnt vmcnt(6)
	ds_write2_b32 v54, v124, v125 offset0:8 offset1:73
	s_waitcnt vmcnt(4)
	ds_write2_b32 v54, v126, v127 offset0:138 offset1:203
	s_waitcnt vmcnt(2)
	ds_write2_b32 v55, v128, v129 offset0:12 offset1:77
	s_waitcnt vmcnt(0)
	ds_write2_b32 v55, v130, v131 offset0:142 offset1:207
	s_add_u32 s38, s34, 0xfffe67c0
	s_addc_u32 s39, s35, -1
	s_and_b32 s78, s36, 0x3c0
	s_lshl_b32 s5, s38, 2
	s_lshl_b64 s[36:37], s[38:39], 13
	s_and_b32 s5, s5, 0x3c0
	s_and_b32 s37, s37, 0x1fffff
	s_and_b32 s36, s36, 0xffe00000
	s_add_u32 s36, s33, s36
	s_waitcnt lgkmcnt(0)
	s_addc_u32 s37, s40, s37
	s_lshl_b32 s38, s78, 1
	ds_read2_b32 v[38:39], v19 offset0:65 offset1:73
	ds_read2_b32 v[40:41], v19 offset1:8
	ds_read2_b32 v[54:55], v19 offset0:130 offset1:138
	ds_read2_b32 v[56:57], v19 offset0:195 offset1:203
	ds_read2_b32 v[58:59], v52 offset0:4 offset1:12
	ds_read2_b32 v[60:61], v52 offset0:69 offset1:77
	ds_read2_b32 v[62:63], v52 offset0:134 offset1:142
	ds_read2_b32 v[64:65], v52 offset0:199 offset1:207
	s_add_u32 s36, s36, s38
	s_addc_u32 s37, s37, 0
	s_waitcnt lgkmcnt(6)
	v_cvt_pk_bf16_f32 v2, v40, v38
	v_or_b32_e32 v38, s5, v42
	v_lshl_add_u64 v[66:67], s[36:37], 0, v[6:7]
	v_lshlrev_b32_e32 v68, 11, v38
	v_mov_b32_e32 v69, v7
	v_lshl_add_u64 v[68:69], v[66:67], 0, v[68:69]
	s_waitcnt lgkmcnt(4)
	v_cvt_pk_bf16_f32 v3, v54, v56
	s_waitcnt lgkmcnt(2)
	v_cvt_pk_bf16_f32 v4, v58, v60
	s_waitcnt lgkmcnt(0)
	v_cvt_pk_bf16_f32 v5, v62, v64
	global_store_dwordx4 v[68:69], v[2:5], off nt
	v_or_b32_e32 v38, s5, v43
	v_lshlrev_b32_e32 v38, 11, v38
	v_cvt_pk_bf16_f32 v2, v41, v39
	v_cvt_pk_bf16_f32 v3, v55, v57
	v_cvt_pk_bf16_f32 v4, v59, v61
	v_cvt_pk_bf16_f32 v5, v63, v65
	v_mov_b32_e32 v39, v7
	ds_read2_b32 v[40:41], v19 offset0:16 offset1:24
	ds_read2_b32 v[54:55], v19 offset0:81 offset1:89
	ds_read2_b32 v[56:57], v19 offset0:146 offset1:154
	ds_read2_b32 v[58:59], v19 offset0:211 offset1:219
	ds_read2_b32 v[60:61], v52 offset0:20 offset1:28
	ds_read2_b32 v[62:63], v52 offset0:85 offset1:93
	ds_read2_b32 v[64:65], v52 offset0:150 offset1:158
	ds_read2_b32 v[68:69], v52 offset0:215 offset1:223
	v_lshl_add_u64 v[38:39], v[66:67], 0, v[38:39]
	global_store_dwordx4 v[38:39], v[2:5], off nt
	v_or_b32_e32 v38, s5, v44
	v_lshlrev_b32_e32 v38, 11, v38
	v_mov_b32_e32 v39, v7
	v_lshl_add_u64 v[38:39], v[66:67], 0, v[38:39]
	s_waitcnt lgkmcnt(6)
	v_cvt_pk_bf16_f32 v2, v40, v54
	s_waitcnt lgkmcnt(4)
	v_cvt_pk_bf16_f32 v3, v56, v58
	s_waitcnt lgkmcnt(2)
	v_cvt_pk_bf16_f32 v4, v60, v62
	s_waitcnt lgkmcnt(0)
	v_cvt_pk_bf16_f32 v5, v64, v68
	global_store_dwordx4 v[38:39], v[2:5], off nt
	v_or_b32_e32 v38, s5, v45
	v_lshlrev_b32_e32 v38, 11, v38
	v_cvt_pk_bf16_f32 v2, v41, v55
	v_cvt_pk_bf16_f32 v3, v57, v59
	v_cvt_pk_bf16_f32 v4, v61, v63
	v_cvt_pk_bf16_f32 v5, v65, v69
	v_mov_b32_e32 v39, v7
	ds_read2_b32 v[40:41], v19 offset0:32 offset1:40
	ds_read2_b32 v[54:55], v19 offset0:97 offset1:105
	ds_read2_b32 v[56:57], v19 offset0:162 offset1:170
	ds_read2_b32 v[58:59], v19 offset0:227 offset1:235
	ds_read2_b32 v[60:61], v52 offset0:36 offset1:44
	ds_read2_b32 v[62:63], v52 offset0:101 offset1:109
	ds_read2_b32 v[64:65], v52 offset0:166 offset1:174
	ds_read2_b32 v[68:69], v52 offset0:231 offset1:239
	v_lshl_add_u64 v[38:39], v[66:67], 0, v[38:39]
	global_store_dwordx4 v[38:39], v[2:5], off nt
	v_or_b32_e32 v38, s5, v46
	v_lshlrev_b32_e32 v38, 11, v38
	v_mov_b32_e32 v39, v7
	v_lshl_add_u64 v[38:39], v[66:67], 0, v[38:39]
	s_waitcnt lgkmcnt(6)
	v_cvt_pk_bf16_f32 v2, v40, v54
	s_waitcnt lgkmcnt(4)
	v_cvt_pk_bf16_f32 v3, v56, v58
	s_waitcnt lgkmcnt(2)
	v_cvt_pk_bf16_f32 v4, v60, v62
	s_waitcnt lgkmcnt(0)
	v_cvt_pk_bf16_f32 v5, v64, v68
	global_store_dwordx4 v[38:39], v[2:5], off nt
	v_or_b32_e32 v38, s5, v47
	v_lshlrev_b32_e32 v38, 11, v38
	v_cvt_pk_bf16_f32 v2, v41, v55
	v_cvt_pk_bf16_f32 v3, v57, v59
	v_cvt_pk_bf16_f32 v4, v61, v63
	v_cvt_pk_bf16_f32 v5, v65, v69
	v_mov_b32_e32 v39, v7
	ds_read2_b32 v[40:41], v19 offset0:48 offset1:56
	ds_read2_b32 v[54:55], v19 offset0:113 offset1:121
	ds_read2_b32 v[56:57], v19 offset0:178 offset1:186
	ds_read2_b32 v[58:59], v19 offset0:243 offset1:251
	ds_read2_b32 v[60:61], v52 offset0:52 offset1:60
	ds_read2_b32 v[62:63], v52 offset0:117 offset1:125
	ds_read2_b32 v[64:65], v52 offset0:182 offset1:190
	ds_read2_b32 v[68:69], v52 offset0:247 offset1:255
	v_lshl_add_u64 v[38:39], v[66:67], 0, v[38:39]
	global_store_dwordx4 v[38:39], v[2:5], off nt
	v_or_b32_e32 v38, s5, v48
	v_lshlrev_b32_e32 v38, 11, v38
	v_mov_b32_e32 v39, v7
	v_lshl_add_u64 v[38:39], v[66:67], 0, v[38:39]
	s_waitcnt lgkmcnt(6)
	v_cvt_pk_bf16_f32 v2, v40, v54
	s_waitcnt lgkmcnt(4)
	v_cvt_pk_bf16_f32 v3, v56, v58
	s_waitcnt lgkmcnt(2)
	v_cvt_pk_bf16_f32 v4, v60, v62
	s_waitcnt lgkmcnt(0)
	v_cvt_pk_bf16_f32 v5, v64, v68
	global_store_dwordx4 v[38:39], v[2:5], off nt
	v_or_b32_e32 v38, s5, v49
	v_lshlrev_b32_e32 v38, 11, v38
	v_mov_b32_e32 v39, v7
	v_lshl_add_u64 v[38:39], v[66:67], 0, v[38:39]
	v_cvt_pk_bf16_f32 v2, v41, v55
	v_cvt_pk_bf16_f32 v3, v57, v59
	v_cvt_pk_bf16_f32 v4, v61, v63
	v_cvt_pk_bf16_f32 v5, v65, v69
	global_store_dwordx4 v[38:39], v[2:5], off nt
	s_waitcnt lgkmcnt(0)

.LBB0_31:
	v_lshl_add_u64 v[38:39], v[2:3], 0, s[36:37]
	v_add_co_u32_e32 v40, vcc, 0x1000, v38
	global_load_dword v100, v[38:39], off nt
	s_nop 0
	v_addc_co_u32_e32 v41, vcc, 0, v39, vcc
	v_add_co_u32_e32 v54, vcc, 0x2000, v38
	global_load_dword v101, v[40:41], off nt
	s_nop 0
	v_addc_co_u32_e32 v55, vcc, 0, v39, vcc
	v_add_co_u32_e32 v40, vcc, 0x3000, v38
	s_add_u32 s36, s36, 0x10000
	s_nop 0
	v_addc_co_u32_e32 v41, vcc, 0, v39, vcc
	v_add_co_u32_e32 v56, vcc, 0x4000, v38
	global_load_dword v102, v[54:55], off nt
	global_load_dword v103, v[40:41], off nt
	v_addc_co_u32_e32 v57, vcc, 0, v39, vcc
	v_add_co_u32_e32 v40, vcc, 0x5000, v38
	s_addc_u32 s37, s37, 0
	s_nop 0
	v_addc_co_u32_e32 v41, vcc, 0, v39, vcc
	v_add_co_u32_e32 v54, vcc, 0x6000, v38
	global_load_dword v104, v[56:57], off nt
	global_load_dword v105, v[40:41], off nt
	v_addc_co_u32_e32 v55, vcc, 0, v39, vcc
	v_add_co_u32_e32 v40, vcc, 0x7000, v38
	s_nop 0
	v_addc_co_u32_e32 v41, vcc, 0, v39, vcc
	v_add_co_u32_e32 v56, vcc, 0x8000, v38
	global_load_dword v106, v[54:55], off nt
	global_load_dword v107, v[40:41], off nt
	v_addc_co_u32_e32 v57, vcc, 0, v39, vcc
	v_add_co_u32_e32 v40, vcc, 0x9000, v38
	s_nop 1
	v_addc_co_u32_e32 v41, vcc, 0, v39, vcc
	v_add_co_u32_e32 v54, vcc, 0xa000, v38
	global_load_dword v108, v[56:57], off nt
	global_load_dword v109, v[40:41], off nt
	v_addc_co_u32_e32 v55, vcc, 0, v39, vcc
	v_add_co_u32_e32 v40, vcc, 0xb000, v38
	s_nop 1
	v_addc_co_u32_e32 v41, vcc, 0, v39, vcc
	v_add_co_u32_e32 v56, vcc, 0xc000, v38
	global_load_dword v110, v[54:55], off nt
	global_load_dword v111, v[40:41], off nt
	v_addc_co_u32_e32 v57, vcc, 0, v39, vcc
	v_add_co_u32_e32 v40, vcc, 0xd000, v38
	s_nop 1
	v_addc_co_u32_e32 v41, vcc, 0, v39, vcc
	v_add_co_u32_e32 v54, vcc, 0xe000, v38
	global_load_dword v112, v[56:57], off nt
	s_nop 0
	global_load_dword v113, v[40:41], off nt
	v_addc_co_u32_e32 v55, vcc, 0, v39, vcc
	v_add_co_u32_e32 v38, vcc, 0xf000, v38
	s_nop 1
	v_addc_co_u32_e32 v39, vcc, 0, v39, vcc
	global_load_dword v114, v[54:55], off nt
	s_nop 0
	global_load_dword v115, v[38:39], off nt
	v_lshl_add_u64 v[38:39], v[2:3], 0, s[36:37]
	v_add_co_u32_e32 v40, vcc, 0x1000, v38
	global_load_dword v116, v[38:39], off nt
	s_nop 0
	v_addc_co_u32_e32 v41, vcc, 0, v39, vcc
	v_add_co_u32_e32 v54, vcc, 0x2000, v38
	global_load_dword v117, v[40:41], off nt
	s_nop 0
	v_addc_co_u32_e32 v55, vcc, 0, v39, vcc
	v_add_co_u32_e32 v40, vcc, 0x3000, v38
	s_add_u32 s36, s36, 0x10000
	s_nop 0
	v_addc_co_u32_e32 v41, vcc, 0, v39, vcc
	v_add_co_u32_e32 v56, vcc, 0x4000, v38
	global_load_dword v118, v[54:55], off nt
	global_load_dword v119, v[40:41], off nt
	v_addc_co_u32_e32 v57, vcc, 0, v39, vcc
	v_add_co_u32_e32 v40, vcc, 0x5000, v38
	s_addc_u32 s37, s37, 0
	s_nop 0
	v_addc_co_u32_e32 v41, vcc, 0, v39, vcc
	v_add_co_u32_e32 v54, vcc, 0x6000, v38
	global_load_dword v120, v[56:57], off nt
	global_load_dword v121, v[40:41], off nt
	v_addc_co_u32_e32 v55, vcc, 0, v39, vcc
	v_add_co_u32_e32 v40, vcc, 0x7000, v38
	s_nop 0
	v_addc_co_u32_e32 v41, vcc, 0, v39, vcc
	v_add_co_u32_e32 v56, vcc, 0x8000, v38
	global_load_dword v122, v[54:55], off nt
	global_load_dword v123, v[40:41], off nt
	v_addc_co_u32_e32 v57, vcc, 0, v39, vcc
	v_add_co_u32_e32 v40, vcc, 0x9000, v38
	s_nop 1
	v_addc_co_u32_e32 v41, vcc, 0, v39, vcc
	v_add_co_u32_e32 v54, vcc, 0xa000, v38
	global_load_dword v124, v[56:57], off nt
	global_load_dword v125, v[40:41], off nt
	v_addc_co_u32_e32 v55, vcc, 0, v39, vcc
	v_add_co_u32_e32 v40, vcc, 0xb000, v38
	s_nop 1
	v_addc_co_u32_e32 v41, vcc, 0, v39, vcc
	v_add_co_u32_e32 v56, vcc, 0xc000, v38
	global_load_dword v126, v[54:55], off nt
	global_load_dword v127, v[40:41], off nt
	v_addc_co_u32_e32 v57, vcc, 0, v39, vcc
	v_add_co_u32_e32 v40, vcc, 0xd000, v38
	s_nop 1
	v_addc_co_u32_e32 v41, vcc, 0, v39, vcc
	v_add_co_u32_e32 v54, vcc, 0xe000, v38
	global_load_dword v128, v[56:57], off nt
	s_nop 0
	global_load_dword v129, v[40:41], off nt
	v_addc_co_u32_e32 v55, vcc, 0, v39, vcc
	v_add_co_u32_e32 v38, vcc, 0xf000, v38
	s_nop 1
	v_addc_co_u32_e32 v39, vcc, 0, v39, vcc
	global_load_dword v130, v[54:55], off nt
	s_nop 0
	global_load_dword v131, v[38:39], off nt
	v_add_u32_e32 v39, 0x400, v4
	v_add_u32_e32 v54, 0x800, v4
	v_add_u32_e32 v55, 0xc00, v4
	s_waitcnt vmcnt(30)
	ds_write2_b32 v4, v100, v101 offset1:65
	s_waitcnt vmcnt(28)
	ds_write2_b32 v4, v102, v103 offset0:130 offset1:195
	v_add_u32_e32 v4, 0x1040, v4
	s_waitcnt vmcnt(26)
	ds_write2_b32 v39, v104, v105 offset0:4 offset1:69
	s_waitcnt vmcnt(24)
	ds_write2_b32 v39, v106, v107 offset0:134 offset1:199
	s_waitcnt vmcnt(22)
	ds_write2_b32 v54, v108, v109 offset0:8 offset1:73
	s_waitcnt vmcnt(20)
	ds_write2_b32 v54, v110, v111 offset0:138 offset1:203
	s_waitcnt vmcnt(18)
	ds_write2_b32 v55, v112, v113 offset0:12 offset1:77
	s_waitcnt vmcnt(16)
	ds_write2_b32 v55, v114, v115 offset0:142 offset1:207
	v_lshl_add_u64 v[38:39], v[2:3], 0, s[36:37]
	v_add_co_u32_e32 v40, vcc, 0x1000, v38
	global_load_dword v100, v[38:39], off nt
	s_nop 0
	v_addc_co_u32_e32 v41, vcc, 0, v39, vcc
	v_add_co_u32_e32 v54, vcc, 0x2000, v38
	global_load_dword v101, v[40:41], off nt
	s_nop 0
	v_addc_co_u32_e32 v55, vcc, 0, v39, vcc
	v_add_co_u32_e32 v40, vcc, 0x3000, v38
	s_add_u32 s36, s36, 0x10000
	s_nop 0
	v_addc_co_u32_e32 v41, vcc, 0, v39, vcc
	v_add_co_u32_e32 v56, vcc, 0x4000, v38
	global_load_dword v102, v[54:55], off nt
	global_load_dword v103, v[40:41], off nt
	v_addc_co_u32_e32 v57, vcc, 0, v39, vcc
	v_add_co_u32_e32 v40, vcc, 0x5000, v38
	s_addc_u32 s37, s37, 0
	s_nop 0
	v_addc_co_u32_e32 v41, vcc, 0, v39, vcc
	v_add_co_u32_e32 v54, vcc, 0x6000, v38
	global_load_dword v104, v[56:57], off nt
	global_load_dword v105, v[40:41], off nt
	v_addc_co_u32_e32 v55, vcc, 0, v39, vcc
	v_add_co_u32_e32 v40, vcc, 0x7000, v38
	s_nop 0
	v_addc_co_u32_e32 v41, vcc, 0, v39, vcc
	v_add_co_u32_e32 v56, vcc, 0x8000, v38
	global_load_dword v106, v[54:55], off nt
	global_load_dword v107, v[40:41], off nt
	v_addc_co_u32_e32 v57, vcc, 0, v39, vcc
	v_add_co_u32_e32 v40, vcc, 0x9000, v38
	s_nop 1
	v_addc_co_u32_e32 v41, vcc, 0, v39, vcc
	v_add_co_u32_e32 v54, vcc, 0xa000, v38
	global_load_dword v108, v[56:57], off nt
	global_load_dword v109, v[40:41], off nt
	v_addc_co_u32_e32 v55, vcc, 0, v39, vcc
	v_add_co_u32_e32 v40, vcc, 0xb000, v38
	s_nop 1
	v_addc_co_u32_e32 v41, vcc, 0, v39, vcc
	v_add_co_u32_e32 v56, vcc, 0xc000, v38
	global_load_dword v110, v[54:55], off nt
	global_load_dword v111, v[40:41], off nt
	v_addc_co_u32_e32 v57, vcc, 0, v39, vcc
	v_add_co_u32_e32 v40, vcc, 0xd000, v38
	s_nop 1
	v_addc_co_u32_e32 v41, vcc, 0, v39, vcc
	v_add_co_u32_e32 v54, vcc, 0xe000, v38
	global_load_dword v112, v[56:57], off nt
	s_nop 0
	global_load_dword v113, v[40:41], off nt
	v_addc_co_u32_e32 v55, vcc, 0, v39, vcc
	v_add_co_u32_e32 v38, vcc, 0xf000, v38
	s_nop 1
	v_addc_co_u32_e32 v39, vcc, 0, v39, vcc
	global_load_dword v114, v[54:55], off nt
	s_nop 0
	global_load_dword v115, v[38:39], off nt
	v_add_u32_e32 v39, 0x400, v4
	v_add_u32_e32 v54, 0x800, v4
	v_add_u32_e32 v55, 0xc00, v4
	s_waitcnt vmcnt(30)
	ds_write2_b32 v4, v116, v117 offset1:65
	s_waitcnt vmcnt(28)
	ds_write2_b32 v4, v118, v119 offset0:130 offset1:195
	v_add_u32_e32 v4, 0x1040, v4
	s_waitcnt vmcnt(26)
	ds_write2_b32 v39, v120, v121 offset0:4 offset1:69
	s_waitcnt vmcnt(24)
	ds_write2_b32 v39, v122, v123 offset0:134 offset1:199
	s_waitcnt vmcnt(22)
	ds_write2_b32 v54, v124, v125 offset0:8 offset1:73
	s_waitcnt vmcnt(20)
	ds_write2_b32 v54, v126, v127 offset0:138 offset1:203
	s_waitcnt vmcnt(18)
	ds_write2_b32 v55, v128, v129 offset0:12 offset1:77
	s_waitcnt vmcnt(16)
	ds_write2_b32 v55, v130, v131 offset0:142 offset1:207
	v_lshl_add_u64 v[38:39], v[2:3], 0, s[36:37]
	v_add_co_u32_e32 v40, vcc, 0x1000, v38
	global_load_dword v116, v[38:39], off nt
	s_nop 0
	v_addc_co_u32_e32 v41, vcc, 0, v39, vcc
	v_add_co_u32_e32 v54, vcc, 0x2000, v38
	global_load_dword v117, v[40:41], off nt
	s_nop 0
	v_addc_co_u32_e32 v55, vcc, 0, v39, vcc
	v_add_co_u32_e32 v40, vcc, 0x3000, v38
	s_add_u32 s36, s36, 0x10000
	s_nop 0
	v_addc_co_u32_e32 v41, vcc, 0, v39, vcc
	v_add_co_u32_e32 v56, vcc, 0x4000, v38
	global_load_dword v118, v[54:55], off nt
	global_load_dword v119, v[40:41], off nt
	v_addc_co_u32_e32 v57, vcc, 0, v39, vcc
	v_add_co_u32_e32 v40, vcc, 0x5000, v38
	s_addc_u32 s37, s37, 0
	s_nop 0
	v_addc_co_u32_e32 v41, vcc, 0, v39, vcc
	v_add_co_u32_e32 v54, vcc, 0x6000, v38
	global_load_dword v120, v[56:57], off nt
	global_load_dword v121, v[40:41], off nt
	v_addc_co_u32_e32 v55, vcc, 0, v39, vcc
	v_add_co_u32_e32 v40, vcc, 0x7000, v38
	s_nop 0
	v_addc_co_u32_e32 v41, vcc, 0, v39, vcc
	v_add_co_u32_e32 v56, vcc, 0x8000, v38
	global_load_dword v122, v[54:55], off nt
	global_load_dword v123, v[40:41], off nt
	v_addc_co_u32_e32 v57, vcc, 0, v39, vcc
	v_add_co_u32_e32 v40, vcc, 0x9000, v38
	s_nop 1
	v_addc_co_u32_e32 v41, vcc, 0, v39, vcc
	v_add_co_u32_e32 v54, vcc, 0xa000, v38
	global_load_dword v124, v[56:57], off nt
	global_load_dword v125, v[40:41], off nt
	v_addc_co_u32_e32 v55, vcc, 0, v39, vcc
	v_add_co_u32_e32 v40, vcc, 0xb000, v38
	s_nop 1
	v_addc_co_u32_e32 v41, vcc, 0, v39, vcc
	v_add_co_u32_e32 v56, vcc, 0xc000, v38
	global_load_dword v126, v[54:55], off nt
	global_load_dword v127, v[40:41], off nt
	v_addc_co_u32_e32 v57, vcc, 0, v39, vcc
	v_add_co_u32_e32 v40, vcc, 0xd000, v38
	s_nop 1
	v_addc_co_u32_e32 v41, vcc, 0, v39, vcc
	v_add_co_u32_e32 v54, vcc, 0xe000, v38
	global_load_dword v128, v[56:57], off nt
	s_nop 0
	global_load_dword v129, v[40:41], off nt
	v_addc_co_u32_e32 v55, vcc, 0, v39, vcc
	v_add_co_u32_e32 v38, vcc, 0xf000, v38
	s_nop 1
	v_addc_co_u32_e32 v39, vcc, 0, v39, vcc
	global_load_dword v130, v[54:55], off nt
	s_nop 0
	global_load_dword v131, v[38:39], off nt
	v_add_u32_e32 v39, 0x400, v4
	v_add_u32_e32 v54, 0x800, v4
	v_add_u32_e32 v55, 0xc00, v4
	s_waitcnt vmcnt(30)
	ds_write2_b32 v4, v100, v101 offset1:65
	s_waitcnt vmcnt(28)
	ds_write2_b32 v4, v102, v103 offset0:130 offset1:195
	v_add_u32_e32 v4, 0x1040, v4
	s_waitcnt vmcnt(26)
	ds_write2_b32 v39, v104, v105 offset0:4 offset1:69
	s_waitcnt vmcnt(24)
	ds_write2_b32 v39, v106, v107 offset0:134 offset1:199
	s_waitcnt vmcnt(22)
	ds_write2_b32 v54, v108, v109 offset0:8 offset1:73
	s_waitcnt vmcnt(20)
	ds_write2_b32 v54, v110, v111 offset0:138 offset1:203
	s_waitcnt vmcnt(18)
	ds_write2_b32 v55, v112, v113 offset0:12 offset1:77
	s_waitcnt vmcnt(16)
	ds_write2_b32 v55, v114, v115 offset0:142 offset1:207
	v_add_u32_e32 v39, 0x400, v4
	v_add_u32_e32 v54, 0x800, v4
	v_add_u32_e32 v55, 0xc00, v4
	s_waitcnt vmcnt(14)
	ds_write2_b32 v4, v116, v117 offset1:65
	s_waitcnt vmcnt(12)
	ds_write2_b32 v4, v118, v119 offset0:130 offset1:195
	v_add_u32_e32 v4, 0x1040, v4
	s_waitcnt vmcnt(10)
	ds_write2_b32 v39, v120, v121 offset0:4 offset1:69
	s_waitcnt vmcnt(8)
	ds_write2_b32 v39, v122, v123 offset0:134 offset1:199
	s_waitcnt vmcnt(6)
	ds_write2_b32 v54, v124, v125 offset0:8 offset1:73
	s_waitcnt vmcnt(4)
	ds_write2_b32 v54, v126, v127 offset0:138 offset1:203
	s_waitcnt vmcnt(2)
	ds_write2_b32 v55, v128, v129 offset0:12 offset1:77
	s_waitcnt vmcnt(0)
	ds_write2_b32 v55, v130, v131 offset0:142 offset1:207
	s_lshl_b32 s5, s34, 4
	s_lshl_b64 s[36:37], s[34:35], 13
	s_and_b32 s5, s5, 0x3c0
	s_add_u32 s36, s36, 0xcd180000
	s_addc_u32 s37, s37, 0x7ffff
	s_and_b32 s37, s37, 0x7ffff
	s_and_b32 s36, s36, 0xfff80000
	s_add_u32 s36, s41, s36
	s_addc_u32 s37, s42, s37
	s_waitcnt lgkmcnt(0)
	s_lshl_b32 s38, s34, 7
	s_and_b32 s38, s38, 0x180
	ds_read2_b32 v[38:39], v19 offset0:65 offset1:73
	ds_read2_b32 v[40:41], v19 offset1:8
	ds_read2_b32 v[54:55], v19 offset0:130 offset1:138
	ds_read2_b32 v[56:57], v19 offset0:195 offset1:203
	ds_read2_b32 v[58:59], v52 offset0:4 offset1:12
	ds_read2_b32 v[60:61], v52 offset0:69 offset1:77
	ds_read2_b32 v[62:63], v52 offset0:134 offset1:142
	ds_read2_b32 v[64:65], v52 offset0:199 offset1:207
	s_add_u32 s36, s36, s38
	s_addc_u32 s37, s37, 0
	s_waitcnt lgkmcnt(6)
	v_cvt_pk_bf16_f32 v2, v40, v38
	v_or_b32_e32 v38, s5, v42
	v_lshl_add_u64 v[66:67], s[36:37], 0, v[6:7]
	v_lshlrev_b32_e32 v68, 9, v38
	v_mov_b32_e32 v69, v7
	v_lshl_add_u64 v[68:69], v[66:67], 0, v[68:69]
	s_waitcnt lgkmcnt(4)
	v_cvt_pk_bf16_f32 v3, v54, v56
	s_waitcnt lgkmcnt(2)
	v_cvt_pk_bf16_f32 v4, v58, v60
	s_waitcnt lgkmcnt(0)
	v_cvt_pk_bf16_f32 v5, v62, v64
	global_store_dwordx4 v[68:69], v[2:5], off nt
	v_or_b32_e32 v38, s5, v43
	v_lshlrev_b32_e32 v38, 9, v38
	v_cvt_pk_bf16_f32 v2, v41, v39
	v_cvt_pk_bf16_f32 v3, v55, v57
	v_cvt_pk_bf16_f32 v4, v59, v61
	v_cvt_pk_bf16_f32 v5, v63, v65
	v_mov_b32_e32 v39, v7
	ds_read2_b32 v[40:41], v19 offset0:16 offset1:24
	ds_read2_b32 v[54:55], v19 offset0:81 offset1:89
	ds_read2_b32 v[56:57], v19 offset0:146 offset1:154
	ds_read2_b32 v[58:59], v19 offset0:211 offset1:219
	ds_read2_b32 v[60:61], v52 offset0:20 offset1:28
	ds_read2_b32 v[62:63], v52 offset0:85 offset1:93
	ds_read2_b32 v[64:65], v52 offset0:150 offset1:158
	ds_read2_b32 v[68:69], v52 offset0:215 offset1:223
	v_lshl_add_u64 v[38:39], v[66:67], 0, v[38:39]
	global_store_dwordx4 v[38:39], v[2:5], off nt
	v_or_b32_e32 v38, s5, v44
	v_lshlrev_b32_e32 v38, 9, v38
	v_mov_b32_e32 v39, v7
	v_lshl_add_u64 v[38:39], v[66:67], 0, v[38:39]
	s_waitcnt lgkmcnt(6)
	v_cvt_pk_bf16_f32 v2, v40, v54
	s_waitcnt lgkmcnt(4)
	v_cvt_pk_bf16_f32 v3, v56, v58
	s_waitcnt lgkmcnt(2)
	v_cvt_pk_bf16_f32 v4, v60, v62
	s_waitcnt lgkmcnt(0)
	v_cvt_pk_bf16_f32 v5, v64, v68
	global_store_dwordx4 v[38:39], v[2:5], off nt
	v_or_b32_e32 v38, s5, v45
	v_lshlrev_b32_e32 v38, 9, v38
	v_cvt_pk_bf16_f32 v2, v41, v55
	v_cvt_pk_bf16_f32 v3, v57, v59
	v_cvt_pk_bf16_f32 v4, v61, v63
	v_cvt_pk_bf16_f32 v5, v65, v69
	v_mov_b32_e32 v39, v7
	ds_read2_b32 v[40:41], v19 offset0:32 offset1:40
	ds_read2_b32 v[54:55], v19 offset0:97 offset1:105
	ds_read2_b32 v[56:57], v19 offset0:162 offset1:170
	ds_read2_b32 v[58:59], v19 offset0:227 offset1:235
	ds_read2_b32 v[60:61], v52 offset0:36 offset1:44
	ds_read2_b32 v[62:63], v52 offset0:101 offset1:109
	ds_read2_b32 v[64:65], v52 offset0:166 offset1:174
	ds_read2_b32 v[68:69], v52 offset0:231 offset1:239
	v_lshl_add_u64 v[38:39], v[66:67], 0, v[38:39]
	global_store_dwordx4 v[38:39], v[2:5], off nt
	v_or_b32_e32 v38, s5, v46
	v_lshlrev_b32_e32 v38, 9, v38
	v_mov_b32_e32 v39, v7
	v_lshl_add_u64 v[38:39], v[66:67], 0, v[38:39]
	s_waitcnt lgkmcnt(6)
	v_cvt_pk_bf16_f32 v2, v40, v54
	s_waitcnt lgkmcnt(4)
	v_cvt_pk_bf16_f32 v3, v56, v58
	s_waitcnt lgkmcnt(2)
	v_cvt_pk_bf16_f32 v4, v60, v62
	s_waitcnt lgkmcnt(0)
	v_cvt_pk_bf16_f32 v5, v64, v68
	global_store_dwordx4 v[38:39], v[2:5], off nt
	v_or_b32_e32 v38, s5, v47
	v_lshlrev_b32_e32 v38, 9, v38
	v_cvt_pk_bf16_f32 v2, v41, v55
	v_cvt_pk_bf16_f32 v3, v57, v59
	v_cvt_pk_bf16_f32 v4, v61, v63
	v_cvt_pk_bf16_f32 v5, v65, v69
	v_mov_b32_e32 v39, v7
	ds_read2_b32 v[40:41], v19 offset0:48 offset1:56
	ds_read2_b32 v[54:55], v19 offset0:113 offset1:121
	ds_read2_b32 v[56:57], v19 offset0:178 offset1:186
	ds_read2_b32 v[58:59], v19 offset0:243 offset1:251
	ds_read2_b32 v[60:61], v52 offset0:52 offset1:60
	ds_read2_b32 v[62:63], v52 offset0:117 offset1:125
	ds_read2_b32 v[64:65], v52 offset0:182 offset1:190
	ds_read2_b32 v[68:69], v52 offset0:247 offset1:255
	v_lshl_add_u64 v[38:39], v[66:67], 0, v[38:39]
	global_store_dwordx4 v[38:39], v[2:5], off nt
	v_or_b32_e32 v38, s5, v48
	v_lshlrev_b32_e32 v38, 9, v38
	v_mov_b32_e32 v39, v7
	v_lshl_add_u64 v[38:39], v[66:67], 0, v[38:39]
	s_waitcnt lgkmcnt(6)
	v_cvt_pk_bf16_f32 v2, v40, v54
	s_waitcnt lgkmcnt(4)
	v_cvt_pk_bf16_f32 v3, v56, v58
	s_waitcnt lgkmcnt(2)
	v_cvt_pk_bf16_f32 v4, v60, v62
	s_waitcnt lgkmcnt(0)
	v_cvt_pk_bf16_f32 v5, v64, v68
	global_store_dwordx4 v[38:39], v[2:5], off nt
	v_or_b32_e32 v38, s5, v49
	v_lshlrev_b32_e32 v38, 9, v38
	v_mov_b32_e32 v39, v7
	v_lshl_add_u64 v[38:39], v[66:67], 0, v[38:39]
	v_cvt_pk_bf16_f32 v2, v41, v55
	v_cvt_pk_bf16_f32 v3, v57, v59
	v_cvt_pk_bf16_f32 v4, v61, v63
	v_cvt_pk_bf16_f32 v5, v65, v69
	global_store_dwordx4 v[38:39], v[2:5], off nt
	s_waitcnt lgkmcnt(0)

.LBB0_36:
	v_lshl_add_u64 v[38:39], v[2:3], 0, s[6:7]
	v_add_co_u32_e32 v40, vcc, 0x1000, v38
	global_load_dword v100, v[38:39], off nt
	s_nop 0
	v_addc_co_u32_e32 v41, vcc, 0, v39, vcc
	v_add_co_u32_e32 v54, vcc, 0x2000, v38
	global_load_dword v101, v[40:41], off nt
	s_nop 0
	v_addc_co_u32_e32 v55, vcc, 0, v39, vcc
	v_add_co_u32_e32 v40, vcc, 0x3000, v38
	s_add_u32 s6, s6, 0x10000
	s_nop 0
	v_addc_co_u32_e32 v41, vcc, 0, v39, vcc
	v_add_co_u32_e32 v56, vcc, 0x4000, v38
	global_load_dword v102, v[54:55], off nt
	global_load_dword v103, v[40:41], off nt
	v_addc_co_u32_e32 v57, vcc, 0, v39, vcc
	v_add_co_u32_e32 v40, vcc, 0x5000, v38
	s_addc_u32 s7, s7, 0
	s_nop 0
	v_addc_co_u32_e32 v41, vcc, 0, v39, vcc
	v_add_co_u32_e32 v54, vcc, 0x6000, v38
	global_load_dword v104, v[56:57], off nt
	global_load_dword v105, v[40:41], off nt
	v_addc_co_u32_e32 v55, vcc, 0, v39, vcc
	v_add_co_u32_e32 v40, vcc, 0x7000, v38
	s_nop 0
	v_addc_co_u32_e32 v41, vcc, 0, v39, vcc
	v_add_co_u32_e32 v56, vcc, 0x8000, v38
	global_load_dword v106, v[54:55], off nt
	global_load_dword v107, v[40:41], off nt
	v_addc_co_u32_e32 v57, vcc, 0, v39, vcc
	v_add_co_u32_e32 v40, vcc, 0x9000, v38
	s_nop 1
	v_addc_co_u32_e32 v41, vcc, 0, v39, vcc
	v_add_co_u32_e32 v54, vcc, 0xa000, v38
	global_load_dword v108, v[56:57], off nt
	global_load_dword v109, v[40:41], off nt
	v_addc_co_u32_e32 v55, vcc, 0, v39, vcc
	v_add_co_u32_e32 v40, vcc, 0xb000, v38
	s_nop 1
	v_addc_co_u32_e32 v41, vcc, 0, v39, vcc
	v_add_co_u32_e32 v56, vcc, 0xc000, v38
	global_load_dword v110, v[54:55], off nt
	global_load_dword v111, v[40:41], off nt
	v_addc_co_u32_e32 v57, vcc, 0, v39, vcc
	v_add_co_u32_e32 v40, vcc, 0xd000, v38
	s_nop 1
	v_addc_co_u32_e32 v41, vcc, 0, v39, vcc
	v_add_co_u32_e32 v54, vcc, 0xe000, v38
	global_load_dword v112, v[56:57], off nt
	s_nop 0
	global_load_dword v113, v[40:41], off nt
	v_addc_co_u32_e32 v55, vcc, 0, v39, vcc
	v_add_co_u32_e32 v38, vcc, 0xf000, v38
	s_nop 1
	v_addc_co_u32_e32 v39, vcc, 0, v39, vcc
	global_load_dword v114, v[54:55], off nt
	s_nop 0
	global_load_dword v115, v[38:39], off nt
	v_lshl_add_u64 v[38:39], v[2:3], 0, s[6:7]
	v_add_co_u32_e32 v40, vcc, 0x1000, v38
	global_load_dword v116, v[38:39], off nt
	s_nop 0
	v_addc_co_u32_e32 v41, vcc, 0, v39, vcc
	v_add_co_u32_e32 v54, vcc, 0x2000, v38
	global_load_dword v117, v[40:41], off nt
	s_nop 0
	v_addc_co_u32_e32 v55, vcc, 0, v39, vcc
	v_add_co_u32_e32 v40, vcc, 0x3000, v38
	s_add_u32 s6, s6, 0x10000
	s_nop 0
	v_addc_co_u32_e32 v41, vcc, 0, v39, vcc
	v_add_co_u32_e32 v56, vcc, 0x4000, v38
	global_load_dword v118, v[54:55], off nt
	global_load_dword v119, v[40:41], off nt
	v_addc_co_u32_e32 v57, vcc, 0, v39, vcc
	v_add_co_u32_e32 v40, vcc, 0x5000, v38
	s_addc_u32 s7, s7, 0
	s_nop 0
	v_addc_co_u32_e32 v41, vcc, 0, v39, vcc
	v_add_co_u32_e32 v54, vcc, 0x6000, v38
	global_load_dword v120, v[56:57], off nt
	global_load_dword v121, v[40:41], off nt
	v_addc_co_u32_e32 v55, vcc, 0, v39, vcc
	v_add_co_u32_e32 v40, vcc, 0x7000, v38
	s_nop 0
	v_addc_co_u32_e32 v41, vcc, 0, v39, vcc
	v_add_co_u32_e32 v56, vcc, 0x8000, v38
	global_load_dword v122, v[54:55], off nt
	global_load_dword v123, v[40:41], off nt
	v_addc_co_u32_e32 v57, vcc, 0, v39, vcc
	v_add_co_u32_e32 v40, vcc, 0x9000, v38
	s_nop 1
	v_addc_co_u32_e32 v41, vcc, 0, v39, vcc
	v_add_co_u32_e32 v54, vcc, 0xa000, v38
	global_load_dword v124, v[56:57], off nt
	global_load_dword v125, v[40:41], off nt
	v_addc_co_u32_e32 v55, vcc, 0, v39, vcc
	v_add_co_u32_e32 v40, vcc, 0xb000, v38
	s_nop 1
	v_addc_co_u32_e32 v41, vcc, 0, v39, vcc
	v_add_co_u32_e32 v56, vcc, 0xc000, v38
	global_load_dword v126, v[54:55], off nt
	global_load_dword v127, v[40:41], off nt
	v_addc_co_u32_e32 v57, vcc, 0, v39, vcc
	v_add_co_u32_e32 v40, vcc, 0xd000, v38
	s_nop 1
	v_addc_co_u32_e32 v41, vcc, 0, v39, vcc
	v_add_co_u32_e32 v54, vcc, 0xe000, v38
	global_load_dword v128, v[56:57], off nt
	s_nop 0
	global_load_dword v129, v[40:41], off nt
	v_addc_co_u32_e32 v55, vcc, 0, v39, vcc
	v_add_co_u32_e32 v38, vcc, 0xf000, v38
	s_nop 1
	v_addc_co_u32_e32 v39, vcc, 0, v39, vcc
	global_load_dword v130, v[54:55], off nt
	s_nop 0
	global_load_dword v131, v[38:39], off nt
	v_add_u32_e32 v39, 0x400, v4
	v_add_u32_e32 v54, 0x800, v4
	v_add_u32_e32 v55, 0xc00, v4
	s_waitcnt vmcnt(30)
	ds_write2_b32 v4, v100, v101 offset1:65
	s_waitcnt vmcnt(28)
	ds_write2_b32 v4, v102, v103 offset0:130 offset1:195
	v_add_u32_e32 v4, 0x1040, v4
	s_waitcnt vmcnt(26)
	ds_write2_b32 v39, v104, v105 offset0:4 offset1:69
	s_waitcnt vmcnt(24)
	ds_write2_b32 v39, v106, v107 offset0:134 offset1:199
	s_waitcnt vmcnt(22)
	ds_write2_b32 v54, v108, v109 offset0:8 offset1:73
	s_waitcnt vmcnt(20)
	ds_write2_b32 v54, v110, v111 offset0:138 offset1:203
	s_waitcnt vmcnt(18)
	ds_write2_b32 v55, v112, v113 offset0:12 offset1:77
	s_waitcnt vmcnt(16)
	ds_write2_b32 v55, v114, v115 offset0:142 offset1:207
	v_lshl_add_u64 v[38:39], v[2:3], 0, s[6:7]
	v_add_co_u32_e32 v40, vcc, 0x1000, v38
	global_load_dword v100, v[38:39], off nt
	s_nop 0
	v_addc_co_u32_e32 v41, vcc, 0, v39, vcc
	v_add_co_u32_e32 v54, vcc, 0x2000, v38
	global_load_dword v101, v[40:41], off nt
	s_nop 0
	v_addc_co_u32_e32 v55, vcc, 0, v39, vcc
	v_add_co_u32_e32 v40, vcc, 0x3000, v38
	s_add_u32 s6, s6, 0x10000
	s_nop 0
	v_addc_co_u32_e32 v41, vcc, 0, v39, vcc
	v_add_co_u32_e32 v56, vcc, 0x4000, v38
	global_load_dword v102, v[54:55], off nt
	global_load_dword v103, v[40:41], off nt
	v_addc_co_u32_e32 v57, vcc, 0, v39, vcc
	v_add_co_u32_e32 v40, vcc, 0x5000, v38
	s_addc_u32 s7, s7, 0
	s_nop 0
	v_addc_co_u32_e32 v41, vcc, 0, v39, vcc
	v_add_co_u32_e32 v54, vcc, 0x6000, v38
	global_load_dword v104, v[56:57], off nt
	global_load_dword v105, v[40:41], off nt
	v_addc_co_u32_e32 v55, vcc, 0, v39, vcc
	v_add_co_u32_e32 v40, vcc, 0x7000, v38
	s_nop 0
	v_addc_co_u32_e32 v41, vcc, 0, v39, vcc
	v_add_co_u32_e32 v56, vcc, 0x8000, v38
	global_load_dword v106, v[54:55], off nt
	global_load_dword v107, v[40:41], off nt
	v_addc_co_u32_e32 v57, vcc, 0, v39, vcc
	v_add_co_u32_e32 v40, vcc, 0x9000, v38
	s_nop 1
	v_addc_co_u32_e32 v41, vcc, 0, v39, vcc
	v_add_co_u32_e32 v54, vcc, 0xa000, v38
	global_load_dword v108, v[56:57], off nt
	global_load_dword v109, v[40:41], off nt
	v_addc_co_u32_e32 v55, vcc, 0, v39, vcc
	v_add_co_u32_e32 v40, vcc, 0xb000, v38
	s_nop 1
	v_addc_co_u32_e32 v41, vcc, 0, v39, vcc
	v_add_co_u32_e32 v56, vcc, 0xc000, v38
	global_load_dword v110, v[54:55], off nt
	global_load_dword v111, v[40:41], off nt
	v_addc_co_u32_e32 v57, vcc, 0, v39, vcc
	v_add_co_u32_e32 v40, vcc, 0xd000, v38
	s_nop 1
	v_addc_co_u32_e32 v41, vcc, 0, v39, vcc
	v_add_co_u32_e32 v54, vcc, 0xe000, v38
	global_load_dword v112, v[56:57], off nt
	s_nop 0
	global_load_dword v113, v[40:41], off nt
	v_addc_co_u32_e32 v55, vcc, 0, v39, vcc
	v_add_co_u32_e32 v38, vcc, 0xf000, v38
	s_nop 1
	v_addc_co_u32_e32 v39, vcc, 0, v39, vcc
	global_load_dword v114, v[54:55], off nt
	s_nop 0
	global_load_dword v115, v[38:39], off nt
	v_add_u32_e32 v39, 0x400, v4
	v_add_u32_e32 v54, 0x800, v4
	v_add_u32_e32 v55, 0xc00, v4
	s_waitcnt vmcnt(30)
	ds_write2_b32 v4, v116, v117 offset1:65
	s_waitcnt vmcnt(28)
	ds_write2_b32 v4, v118, v119 offset0:130 offset1:195
	v_add_u32_e32 v4, 0x1040, v4
	s_waitcnt vmcnt(26)
	ds_write2_b32 v39, v120, v121 offset0:4 offset1:69
	s_waitcnt vmcnt(24)
	ds_write2_b32 v39, v122, v123 offset0:134 offset1:199
	s_waitcnt vmcnt(22)
	ds_write2_b32 v54, v124, v125 offset0:8 offset1:73
	s_waitcnt vmcnt(20)
	ds_write2_b32 v54, v126, v127 offset0:138 offset1:203
	s_waitcnt vmcnt(18)
	ds_write2_b32 v55, v128, v129 offset0:12 offset1:77
	s_waitcnt vmcnt(16)
	ds_write2_b32 v55, v130, v131 offset0:142 offset1:207
	v_lshl_add_u64 v[38:39], v[2:3], 0, s[6:7]
	v_add_co_u32_e32 v40, vcc, 0x1000, v38
	global_load_dword v116, v[38:39], off nt
	s_nop 0
	v_addc_co_u32_e32 v41, vcc, 0, v39, vcc
	v_add_co_u32_e32 v54, vcc, 0x2000, v38
	global_load_dword v117, v[40:41], off nt
	s_nop 0
	v_addc_co_u32_e32 v55, vcc, 0, v39, vcc
	v_add_co_u32_e32 v40, vcc, 0x3000, v38
	s_add_u32 s6, s6, 0x10000
	s_nop 0
	v_addc_co_u32_e32 v41, vcc, 0, v39, vcc
	v_add_co_u32_e32 v56, vcc, 0x4000, v38
	global_load_dword v118, v[54:55], off nt
	global_load_dword v119, v[40:41], off nt
	v_addc_co_u32_e32 v57, vcc, 0, v39, vcc
	v_add_co_u32_e32 v40, vcc, 0x5000, v38
	s_addc_u32 s7, s7, 0
	s_nop 0
	v_addc_co_u32_e32 v41, vcc, 0, v39, vcc
	v_add_co_u32_e32 v54, vcc, 0x6000, v38
	global_load_dword v120, v[56:57], off nt
	global_load_dword v121, v[40:41], off nt
	v_addc_co_u32_e32 v55, vcc, 0, v39, vcc
	v_add_co_u32_e32 v40, vcc, 0x7000, v38
	s_nop 0
	v_addc_co_u32_e32 v41, vcc, 0, v39, vcc
	v_add_co_u32_e32 v56, vcc, 0x8000, v38
	global_load_dword v122, v[54:55], off nt
	global_load_dword v123, v[40:41], off nt
	v_addc_co_u32_e32 v57, vcc, 0, v39, vcc
	v_add_co_u32_e32 v40, vcc, 0x9000, v38
	s_nop 1
	v_addc_co_u32_e32 v41, vcc, 0, v39, vcc
	v_add_co_u32_e32 v54, vcc, 0xa000, v38
	global_load_dword v124, v[56:57], off nt
	global_load_dword v125, v[40:41], off nt
	v_addc_co_u32_e32 v55, vcc, 0, v39, vcc
	v_add_co_u32_e32 v40, vcc, 0xb000, v38
	s_nop 1
	v_addc_co_u32_e32 v41, vcc, 0, v39, vcc
	v_add_co_u32_e32 v56, vcc, 0xc000, v38
	global_load_dword v126, v[54:55], off nt
	global_load_dword v127, v[40:41], off nt
	v_addc_co_u32_e32 v57, vcc, 0, v39, vcc
	v_add_co_u32_e32 v40, vcc, 0xd000, v38
	s_nop 1
	v_addc_co_u32_e32 v41, vcc, 0, v39, vcc
	v_add_co_u32_e32 v54, vcc, 0xe000, v38
	global_load_dword v128, v[56:57], off nt
	s_nop 0
	global_load_dword v129, v[40:41], off nt
	v_addc_co_u32_e32 v55, vcc, 0, v39, vcc
	v_add_co_u32_e32 v38, vcc, 0xf000, v38
	s_nop 1
	v_addc_co_u32_e32 v39, vcc, 0, v39, vcc
	global_load_dword v130, v[54:55], off nt
	s_nop 0
	global_load_dword v131, v[38:39], off nt
	v_add_u32_e32 v39, 0x400, v4
	v_add_u32_e32 v54, 0x800, v4
	v_add_u32_e32 v55, 0xc00, v4
	s_waitcnt vmcnt(30)
	ds_write2_b32 v4, v100, v101 offset1:65
	s_waitcnt vmcnt(28)
	ds_write2_b32 v4, v102, v103 offset0:130 offset1:195
	v_add_u32_e32 v4, 0x1040, v4
	s_waitcnt vmcnt(26)
	ds_write2_b32 v39, v104, v105 offset0:4 offset1:69
	s_waitcnt vmcnt(24)
	ds_write2_b32 v39, v106, v107 offset0:134 offset1:199
	s_waitcnt vmcnt(22)
	ds_write2_b32 v54, v108, v109 offset0:8 offset1:73
	s_waitcnt vmcnt(20)
	ds_write2_b32 v54, v110, v111 offset0:138 offset1:203
	s_waitcnt vmcnt(18)
	ds_write2_b32 v55, v112, v113 offset0:12 offset1:77
	s_waitcnt vmcnt(16)
	ds_write2_b32 v55, v114, v115 offset0:142 offset1:207
	v_add_u32_e32 v39, 0x400, v4
	v_add_u32_e32 v54, 0x800, v4
	v_add_u32_e32 v55, 0xc00, v4
	s_waitcnt vmcnt(14)
	ds_write2_b32 v4, v116, v117 offset1:65
	s_waitcnt vmcnt(12)
	ds_write2_b32 v4, v118, v119 offset0:130 offset1:195
	v_add_u32_e32 v4, 0x1040, v4
	s_waitcnt vmcnt(10)
	ds_write2_b32 v39, v120, v121 offset0:4 offset1:69
	s_waitcnt vmcnt(8)
	ds_write2_b32 v39, v122, v123 offset0:134 offset1:199
	s_waitcnt vmcnt(6)
	ds_write2_b32 v54, v124, v125 offset0:8 offset1:73
	s_waitcnt vmcnt(4)
	ds_write2_b32 v54, v126, v127 offset0:138 offset1:203
	s_waitcnt vmcnt(2)
	ds_write2_b32 v55, v128, v129 offset0:12 offset1:77
	s_waitcnt vmcnt(0)
	ds_write2_b32 v55, v130, v131 offset0:142 offset1:207
	s_lshl_b32 s3, s34, 4
	s_lshl_b64 s[6:7], s[34:35], 13
	s_and_b32 s3, s3, 0x3c0
	s_add_u32 s5, s6, 0xcd380000
	s_addc_u32 s6, s7, 0x7ffff
	s_and_b32 s6, s6, 0x7ffff
	s_and_b32 s5, s5, 0xfff80000
	s_add_u32 s5, s43, s5
	s_addc_u32 s7, s44, s6
	s_waitcnt lgkmcnt(0)
	s_lshl_b32 s6, s34, 7
	s_and_b32 s6, s6, 0x180
	ds_read2_b32 v[38:39], v19 offset0:65 offset1:73
	ds_read2_b32 v[40:41], v19 offset1:8
	ds_read2_b32 v[54:55], v19 offset0:130 offset1:138
	ds_read2_b32 v[56:57], v19 offset0:195 offset1:203
	ds_read2_b32 v[58:59], v52 offset0:4 offset1:12
	ds_read2_b32 v[60:61], v52 offset0:69 offset1:77
	ds_read2_b32 v[62:63], v52 offset0:134 offset1:142
	ds_read2_b32 v[64:65], v52 offset0:199 offset1:207
	s_add_u32 s6, s5, s6
	s_addc_u32 s7, s7, 0
	s_waitcnt lgkmcnt(6)
	v_cvt_pk_bf16_f32 v2, v40, v38
	v_or_b32_e32 v38, s3, v42
	v_lshl_add_u64 v[66:67], s[6:7], 0, v[6:7]
	v_lshlrev_b32_e32 v68, 9, v38
	v_mov_b32_e32 v69, v7
	v_lshl_add_u64 v[68:69], v[66:67], 0, v[68:69]
	s_waitcnt lgkmcnt(4)
	v_cvt_pk_bf16_f32 v3, v54, v56
	s_waitcnt lgkmcnt(2)
	v_cvt_pk_bf16_f32 v4, v58, v60
	s_waitcnt lgkmcnt(0)
	v_cvt_pk_bf16_f32 v5, v62, v64
	global_store_dwordx4 v[68:69], v[2:5], off nt
	v_or_b32_e32 v38, s3, v43
	v_lshlrev_b32_e32 v38, 9, v38
	v_cvt_pk_bf16_f32 v2, v41, v39
	v_cvt_pk_bf16_f32 v3, v55, v57
	v_cvt_pk_bf16_f32 v4, v59, v61
	v_cvt_pk_bf16_f32 v5, v63, v65
	v_mov_b32_e32 v39, v7
	ds_read2_b32 v[40:41], v19 offset0:16 offset1:24
	ds_read2_b32 v[54:55], v19 offset0:81 offset1:89
	ds_read2_b32 v[56:57], v19 offset0:146 offset1:154
	ds_read2_b32 v[58:59], v19 offset0:211 offset1:219
	ds_read2_b32 v[60:61], v52 offset0:20 offset1:28
	ds_read2_b32 v[62:63], v52 offset0:85 offset1:93
	ds_read2_b32 v[64:65], v52 offset0:150 offset1:158
	ds_read2_b32 v[68:69], v52 offset0:215 offset1:223
	v_lshl_add_u64 v[38:39], v[66:67], 0, v[38:39]
	global_store_dwordx4 v[38:39], v[2:5], off nt
	v_or_b32_e32 v38, s3, v44
	v_lshlrev_b32_e32 v38, 9, v38
	v_mov_b32_e32 v39, v7
	v_lshl_add_u64 v[38:39], v[66:67], 0, v[38:39]
	s_waitcnt lgkmcnt(6)
	v_cvt_pk_bf16_f32 v2, v40, v54
	s_waitcnt lgkmcnt(4)
	v_cvt_pk_bf16_f32 v3, v56, v58
	s_waitcnt lgkmcnt(2)
	v_cvt_pk_bf16_f32 v4, v60, v62
	s_waitcnt lgkmcnt(0)
	v_cvt_pk_bf16_f32 v5, v64, v68
	global_store_dwordx4 v[38:39], v[2:5], off nt
	v_or_b32_e32 v38, s3, v45
	v_lshlrev_b32_e32 v38, 9, v38
	v_cvt_pk_bf16_f32 v2, v41, v55
	v_cvt_pk_bf16_f32 v3, v57, v59
	v_cvt_pk_bf16_f32 v4, v61, v63
	v_cvt_pk_bf16_f32 v5, v65, v69
	v_mov_b32_e32 v39, v7
	ds_read2_b32 v[40:41], v19 offset0:32 offset1:40
	ds_read2_b32 v[54:55], v19 offset0:97 offset1:105
	ds_read2_b32 v[56:57], v19 offset0:162 offset1:170
	ds_read2_b32 v[58:59], v19 offset0:227 offset1:235
	ds_read2_b32 v[60:61], v52 offset0:36 offset1:44
	ds_read2_b32 v[62:63], v52 offset0:101 offset1:109
	ds_read2_b32 v[64:65], v52 offset0:166 offset1:174
	ds_read2_b32 v[68:69], v52 offset0:231 offset1:239
	v_lshl_add_u64 v[38:39], v[66:67], 0, v[38:39]
	global_store_dwordx4 v[38:39], v[2:5], off nt
	v_or_b32_e32 v38, s3, v46
	v_lshlrev_b32_e32 v38, 9, v38
	v_mov_b32_e32 v39, v7
	v_lshl_add_u64 v[38:39], v[66:67], 0, v[38:39]
	s_waitcnt lgkmcnt(6)
	v_cvt_pk_bf16_f32 v2, v40, v54
	s_waitcnt lgkmcnt(4)
	v_cvt_pk_bf16_f32 v3, v56, v58
	s_waitcnt lgkmcnt(2)
	v_cvt_pk_bf16_f32 v4, v60, v62
	s_waitcnt lgkmcnt(0)
	v_cvt_pk_bf16_f32 v5, v64, v68
	global_store_dwordx4 v[38:39], v[2:5], off nt
	v_or_b32_e32 v38, s3, v47
	v_lshlrev_b32_e32 v38, 9, v38
	v_cvt_pk_bf16_f32 v2, v41, v55
	v_cvt_pk_bf16_f32 v3, v57, v59
	v_cvt_pk_bf16_f32 v4, v61, v63
	v_cvt_pk_bf16_f32 v5, v65, v69
	v_mov_b32_e32 v39, v7
	ds_read2_b32 v[40:41], v19 offset0:48 offset1:56
	ds_read2_b32 v[54:55], v19 offset0:113 offset1:121
	ds_read2_b32 v[56:57], v19 offset0:178 offset1:186
	ds_read2_b32 v[58:59], v19 offset0:243 offset1:251
	ds_read2_b32 v[60:61], v52 offset0:52 offset1:60
	ds_read2_b32 v[62:63], v52 offset0:117 offset1:125
	ds_read2_b32 v[64:65], v52 offset0:182 offset1:190
	ds_read2_b32 v[68:69], v52 offset0:247 offset1:255
	v_lshl_add_u64 v[38:39], v[66:67], 0, v[38:39]
	global_store_dwordx4 v[38:39], v[2:5], off nt
	v_or_b32_e32 v38, s3, v48
	v_lshlrev_b32_e32 v38, 9, v38
	v_mov_b32_e32 v39, v7
	v_lshl_add_u64 v[38:39], v[66:67], 0, v[38:39]
	s_waitcnt lgkmcnt(6)
	v_cvt_pk_bf16_f32 v2, v40, v54
	s_waitcnt lgkmcnt(4)
	v_cvt_pk_bf16_f32 v3, v56, v58
	s_waitcnt lgkmcnt(2)
	v_cvt_pk_bf16_f32 v4, v60, v62
	s_waitcnt lgkmcnt(0)
	v_cvt_pk_bf16_f32 v5, v64, v68
	global_store_dwordx4 v[38:39], v[2:5], off nt
	v_or_b32_e32 v38, s3, v49
	v_lshlrev_b32_e32 v38, 9, v38
	v_mov_b32_e32 v39, v7
	v_lshl_add_u64 v[38:39], v[66:67], 0, v[38:39]
	v_cvt_pk_bf16_f32 v2, v41, v55
	v_cvt_pk_bf16_f32 v3, v57, v59
	v_cvt_pk_bf16_f32 v4, v61, v63
	v_cvt_pk_bf16_f32 v5, v65, v69
	global_store_dwordx4 v[38:39], v[2:5], off nt
	s_waitcnt lgkmcnt(0)

.LBB0_41:
	v_lshl_add_u64 v[38:39], v[2:3], 0, s[4:5]
	v_add_co_u32_e32 v40, vcc, 0x1000, v38
	global_load_dword v100, v[38:39], off nt
	s_nop 0
	v_addc_co_u32_e32 v41, vcc, 0, v39, vcc
	v_add_co_u32_e32 v54, vcc, 0x2000, v38
	global_load_dword v101, v[40:41], off nt
	s_nop 0
	v_addc_co_u32_e32 v55, vcc, 0, v39, vcc
	v_add_co_u32_e32 v40, vcc, 0x3000, v38
	s_add_u32 s4, s4, 0x10000
	s_nop 0
	v_addc_co_u32_e32 v41, vcc, 0, v39, vcc
	v_add_co_u32_e32 v56, vcc, 0x4000, v38
	global_load_dword v102, v[54:55], off nt
	global_load_dword v103, v[40:41], off nt
	v_addc_co_u32_e32 v57, vcc, 0, v39, vcc
	v_add_co_u32_e32 v40, vcc, 0x5000, v38
	s_addc_u32 s5, s5, 0
	s_nop 0
	v_addc_co_u32_e32 v41, vcc, 0, v39, vcc
	v_add_co_u32_e32 v54, vcc, 0x6000, v38
	global_load_dword v104, v[56:57], off nt
	global_load_dword v105, v[40:41], off nt
	v_addc_co_u32_e32 v55, vcc, 0, v39, vcc
	v_add_co_u32_e32 v40, vcc, 0x7000, v38
	s_nop 0
	v_addc_co_u32_e32 v41, vcc, 0, v39, vcc
	v_add_co_u32_e32 v56, vcc, 0x8000, v38
	global_load_dword v106, v[54:55], off nt
	global_load_dword v107, v[40:41], off nt
	v_addc_co_u32_e32 v57, vcc, 0, v39, vcc
	v_add_co_u32_e32 v40, vcc, 0x9000, v38
	s_nop 1
	v_addc_co_u32_e32 v41, vcc, 0, v39, vcc
	v_add_co_u32_e32 v54, vcc, 0xa000, v38
	global_load_dword v108, v[56:57], off nt
	global_load_dword v109, v[40:41], off nt
	v_addc_co_u32_e32 v55, vcc, 0, v39, vcc
	v_add_co_u32_e32 v40, vcc, 0xb000, v38
	s_nop 1
	v_addc_co_u32_e32 v41, vcc, 0, v39, vcc
	v_add_co_u32_e32 v56, vcc, 0xc000, v38
	global_load_dword v110, v[54:55], off nt
	global_load_dword v111, v[40:41], off nt
	v_addc_co_u32_e32 v57, vcc, 0, v39, vcc
	v_add_co_u32_e32 v40, vcc, 0xd000, v38
	s_nop 1
	v_addc_co_u32_e32 v41, vcc, 0, v39, vcc
	v_add_co_u32_e32 v54, vcc, 0xe000, v38
	global_load_dword v112, v[56:57], off nt
	s_nop 0
	global_load_dword v113, v[40:41], off nt
	v_addc_co_u32_e32 v55, vcc, 0, v39, vcc
	v_add_co_u32_e32 v38, vcc, 0xf000, v38
	s_nop 1
	v_addc_co_u32_e32 v39, vcc, 0, v39, vcc
	global_load_dword v114, v[54:55], off nt
	s_nop 0
	global_load_dword v115, v[38:39], off nt
	v_lshl_add_u64 v[38:39], v[2:3], 0, s[4:5]
	v_add_co_u32_e32 v40, vcc, 0x1000, v38
	global_load_dword v116, v[38:39], off nt
	s_nop 0
	v_addc_co_u32_e32 v41, vcc, 0, v39, vcc
	v_add_co_u32_e32 v54, vcc, 0x2000, v38
	global_load_dword v117, v[40:41], off nt
	s_nop 0
	v_addc_co_u32_e32 v55, vcc, 0, v39, vcc
	v_add_co_u32_e32 v40, vcc, 0x3000, v38
	s_add_u32 s4, s4, 0x10000
	s_nop 0
	v_addc_co_u32_e32 v41, vcc, 0, v39, vcc
	v_add_co_u32_e32 v56, vcc, 0x4000, v38
	global_load_dword v118, v[54:55], off nt
	global_load_dword v119, v[40:41], off nt
	v_addc_co_u32_e32 v57, vcc, 0, v39, vcc
	v_add_co_u32_e32 v40, vcc, 0x5000, v38
	s_addc_u32 s5, s5, 0
	s_nop 0
	v_addc_co_u32_e32 v41, vcc, 0, v39, vcc
	v_add_co_u32_e32 v54, vcc, 0x6000, v38
	global_load_dword v120, v[56:57], off nt
	global_load_dword v121, v[40:41], off nt
	v_addc_co_u32_e32 v55, vcc, 0, v39, vcc
	v_add_co_u32_e32 v40, vcc, 0x7000, v38
	s_nop 0
	v_addc_co_u32_e32 v41, vcc, 0, v39, vcc
	v_add_co_u32_e32 v56, vcc, 0x8000, v38
	global_load_dword v122, v[54:55], off nt
	global_load_dword v123, v[40:41], off nt
	v_addc_co_u32_e32 v57, vcc, 0, v39, vcc
	v_add_co_u32_e32 v40, vcc, 0x9000, v38
	s_nop 1
	v_addc_co_u32_e32 v41, vcc, 0, v39, vcc
	v_add_co_u32_e32 v54, vcc, 0xa000, v38
	global_load_dword v124, v[56:57], off nt
	global_load_dword v125, v[40:41], off nt
	v_addc_co_u32_e32 v55, vcc, 0, v39, vcc
	v_add_co_u32_e32 v40, vcc, 0xb000, v38
	s_nop 1
	v_addc_co_u32_e32 v41, vcc, 0, v39, vcc
	v_add_co_u32_e32 v56, vcc, 0xc000, v38
	global_load_dword v126, v[54:55], off nt
	global_load_dword v127, v[40:41], off nt
	v_addc_co_u32_e32 v57, vcc, 0, v39, vcc
	v_add_co_u32_e32 v40, vcc, 0xd000, v38
	s_nop 1
	v_addc_co_u32_e32 v41, vcc, 0, v39, vcc
	v_add_co_u32_e32 v54, vcc, 0xe000, v38
	global_load_dword v128, v[56:57], off nt
	s_nop 0
	global_load_dword v129, v[40:41], off nt
	v_addc_co_u32_e32 v55, vcc, 0, v39, vcc
	v_add_co_u32_e32 v38, vcc, 0xf000, v38
	s_nop 1
	v_addc_co_u32_e32 v39, vcc, 0, v39, vcc
	global_load_dword v130, v[54:55], off nt
	s_nop 0
	global_load_dword v131, v[38:39], off nt
	v_add_u32_e32 v39, 0x400, v4
	v_add_u32_e32 v54, 0x800, v4
	v_add_u32_e32 v55, 0xc00, v4
	s_waitcnt vmcnt(30)
	ds_write2_b32 v4, v100, v101 offset1:65
	s_waitcnt vmcnt(28)
	ds_write2_b32 v4, v102, v103 offset0:130 offset1:195
	v_add_u32_e32 v4, 0x1040, v4
	s_waitcnt vmcnt(26)
	ds_write2_b32 v39, v104, v105 offset0:4 offset1:69
	s_waitcnt vmcnt(24)
	ds_write2_b32 v39, v106, v107 offset0:134 offset1:199
	s_waitcnt vmcnt(22)
	ds_write2_b32 v54, v108, v109 offset0:8 offset1:73
	s_waitcnt vmcnt(20)
	ds_write2_b32 v54, v110, v111 offset0:138 offset1:203
	s_waitcnt vmcnt(18)
	ds_write2_b32 v55, v112, v113 offset0:12 offset1:77
	s_waitcnt vmcnt(16)
	ds_write2_b32 v55, v114, v115 offset0:142 offset1:207
	v_lshl_add_u64 v[38:39], v[2:3], 0, s[4:5]
	v_add_co_u32_e32 v40, vcc, 0x1000, v38
	global_load_dword v100, v[38:39], off nt
	s_nop 0
	v_addc_co_u32_e32 v41, vcc, 0, v39, vcc
	v_add_co_u32_e32 v54, vcc, 0x2000, v38
	global_load_dword v101, v[40:41], off nt
	s_nop 0
	v_addc_co_u32_e32 v55, vcc, 0, v39, vcc
	v_add_co_u32_e32 v40, vcc, 0x3000, v38
	s_add_u32 s4, s4, 0x10000
	s_nop 0
	v_addc_co_u32_e32 v41, vcc, 0, v39, vcc
	v_add_co_u32_e32 v56, vcc, 0x4000, v38
	global_load_dword v102, v[54:55], off nt
	global_load_dword v103, v[40:41], off nt
	v_addc_co_u32_e32 v57, vcc, 0, v39, vcc
	v_add_co_u32_e32 v40, vcc, 0x5000, v38
	s_addc_u32 s5, s5, 0
	s_nop 0
	v_addc_co_u32_e32 v41, vcc, 0, v39, vcc
	v_add_co_u32_e32 v54, vcc, 0x6000, v38
	global_load_dword v104, v[56:57], off nt
	global_load_dword v105, v[40:41], off nt
	v_addc_co_u32_e32 v55, vcc, 0, v39, vcc
	v_add_co_u32_e32 v40, vcc, 0x7000, v38
	s_nop 0
	v_addc_co_u32_e32 v41, vcc, 0, v39, vcc
	v_add_co_u32_e32 v56, vcc, 0x8000, v38
	global_load_dword v106, v[54:55], off nt
	global_load_dword v107, v[40:41], off nt
	v_addc_co_u32_e32 v57, vcc, 0, v39, vcc
	v_add_co_u32_e32 v40, vcc, 0x9000, v38
	s_nop 1
	v_addc_co_u32_e32 v41, vcc, 0, v39, vcc
	v_add_co_u32_e32 v54, vcc, 0xa000, v38
	global_load_dword v108, v[56:57], off nt
	global_load_dword v109, v[40:41], off nt
	v_addc_co_u32_e32 v55, vcc, 0, v39, vcc
	v_add_co_u32_e32 v40, vcc, 0xb000, v38
	s_nop 1
	v_addc_co_u32_e32 v41, vcc, 0, v39, vcc
	v_add_co_u32_e32 v56, vcc, 0xc000, v38
	global_load_dword v110, v[54:55], off nt
	global_load_dword v111, v[40:41], off nt
	v_addc_co_u32_e32 v57, vcc, 0, v39, vcc
	v_add_co_u32_e32 v40, vcc, 0xd000, v38
	s_nop 1
	v_addc_co_u32_e32 v41, vcc, 0, v39, vcc
	v_add_co_u32_e32 v54, vcc, 0xe000, v38
	global_load_dword v112, v[56:57], off nt
	s_nop 0
	global_load_dword v113, v[40:41], off nt
	v_addc_co_u32_e32 v55, vcc, 0, v39, vcc
	v_add_co_u32_e32 v38, vcc, 0xf000, v38
	s_nop 1
	v_addc_co_u32_e32 v39, vcc, 0, v39, vcc
	global_load_dword v114, v[54:55], off nt
	s_nop 0
	global_load_dword v115, v[38:39], off nt
	v_add_u32_e32 v39, 0x400, v4
	v_add_u32_e32 v54, 0x800, v4
	v_add_u32_e32 v55, 0xc00, v4
	s_waitcnt vmcnt(30)
	ds_write2_b32 v4, v116, v117 offset1:65
	s_waitcnt vmcnt(28)
	ds_write2_b32 v4, v118, v119 offset0:130 offset1:195
	v_add_u32_e32 v4, 0x1040, v4
	s_waitcnt vmcnt(26)
	ds_write2_b32 v39, v120, v121 offset0:4 offset1:69
	s_waitcnt vmcnt(24)
	ds_write2_b32 v39, v122, v123 offset0:134 offset1:199
	s_waitcnt vmcnt(22)
	ds_write2_b32 v54, v124, v125 offset0:8 offset1:73
	s_waitcnt vmcnt(20)
	ds_write2_b32 v54, v126, v127 offset0:138 offset1:203
	s_waitcnt vmcnt(18)
	ds_write2_b32 v55, v128, v129 offset0:12 offset1:77
	s_waitcnt vmcnt(16)
	ds_write2_b32 v55, v130, v131 offset0:142 offset1:207
	v_lshl_add_u64 v[38:39], v[2:3], 0, s[4:5]
	v_add_co_u32_e32 v40, vcc, 0x1000, v38
	global_load_dword v116, v[38:39], off nt
	s_nop 0
	v_addc_co_u32_e32 v41, vcc, 0, v39, vcc
	v_add_co_u32_e32 v54, vcc, 0x2000, v38
	global_load_dword v117, v[40:41], off nt
	s_nop 0
	v_addc_co_u32_e32 v55, vcc, 0, v39, vcc
	v_add_co_u32_e32 v40, vcc, 0x3000, v38
	s_add_u32 s4, s4, 0x10000
	s_nop 0
	v_addc_co_u32_e32 v41, vcc, 0, v39, vcc
	v_add_co_u32_e32 v56, vcc, 0x4000, v38
	global_load_dword v118, v[54:55], off nt
	global_load_dword v119, v[40:41], off nt
	v_addc_co_u32_e32 v57, vcc, 0, v39, vcc
	v_add_co_u32_e32 v40, vcc, 0x5000, v38
	s_addc_u32 s5, s5, 0
	s_nop 0
	v_addc_co_u32_e32 v41, vcc, 0, v39, vcc
	v_add_co_u32_e32 v54, vcc, 0x6000, v38
	global_load_dword v120, v[56:57], off nt
	global_load_dword v121, v[40:41], off nt
	v_addc_co_u32_e32 v55, vcc, 0, v39, vcc
	v_add_co_u32_e32 v40, vcc, 0x7000, v38
	s_nop 0
	v_addc_co_u32_e32 v41, vcc, 0, v39, vcc
	v_add_co_u32_e32 v56, vcc, 0x8000, v38
	global_load_dword v122, v[54:55], off nt
	global_load_dword v123, v[40:41], off nt
	v_addc_co_u32_e32 v57, vcc, 0, v39, vcc
	v_add_co_u32_e32 v40, vcc, 0x9000, v38
	s_nop 1
	v_addc_co_u32_e32 v41, vcc, 0, v39, vcc
	v_add_co_u32_e32 v54, vcc, 0xa000, v38
	global_load_dword v124, v[56:57], off nt
	global_load_dword v125, v[40:41], off nt
	v_addc_co_u32_e32 v55, vcc, 0, v39, vcc
	v_add_co_u32_e32 v40, vcc, 0xb000, v38
	s_nop 1
	v_addc_co_u32_e32 v41, vcc, 0, v39, vcc
	v_add_co_u32_e32 v56, vcc, 0xc000, v38
	global_load_dword v126, v[54:55], off nt
	global_load_dword v127, v[40:41], off nt
	v_addc_co_u32_e32 v57, vcc, 0, v39, vcc
	v_add_co_u32_e32 v40, vcc, 0xd000, v38
	s_nop 1
	v_addc_co_u32_e32 v41, vcc, 0, v39, vcc
	v_add_co_u32_e32 v54, vcc, 0xe000, v38
	global_load_dword v128, v[56:57], off nt
	s_nop 0
	global_load_dword v129, v[40:41], off nt
	v_addc_co_u32_e32 v55, vcc, 0, v39, vcc
	v_add_co_u32_e32 v38, vcc, 0xf000, v38
	s_nop 1
	v_addc_co_u32_e32 v39, vcc, 0, v39, vcc
	global_load_dword v130, v[54:55], off nt
	s_nop 0
	global_load_dword v131, v[38:39], off nt
	v_add_u32_e32 v39, 0x400, v4
	v_add_u32_e32 v54, 0x800, v4
	v_add_u32_e32 v55, 0xc00, v4
	s_waitcnt vmcnt(30)
	ds_write2_b32 v4, v100, v101 offset1:65
	s_waitcnt vmcnt(28)
	ds_write2_b32 v4, v102, v103 offset0:130 offset1:195
	v_add_u32_e32 v4, 0x1040, v4
	s_waitcnt vmcnt(26)
	ds_write2_b32 v39, v104, v105 offset0:4 offset1:69
	s_waitcnt vmcnt(24)
	ds_write2_b32 v39, v106, v107 offset0:134 offset1:199
	s_waitcnt vmcnt(22)
	ds_write2_b32 v54, v108, v109 offset0:8 offset1:73
	s_waitcnt vmcnt(20)
	ds_write2_b32 v54, v110, v111 offset0:138 offset1:203
	s_waitcnt vmcnt(18)
	ds_write2_b32 v55, v112, v113 offset0:12 offset1:77
	s_waitcnt vmcnt(16)
	ds_write2_b32 v55, v114, v115 offset0:142 offset1:207
	v_add_u32_e32 v39, 0x400, v4
	v_add_u32_e32 v54, 0x800, v4
	v_add_u32_e32 v55, 0xc00, v4
	s_waitcnt vmcnt(14)
	ds_write2_b32 v4, v116, v117 offset1:65
	s_waitcnt vmcnt(12)
	ds_write2_b32 v4, v118, v119 offset0:130 offset1:195
	v_add_u32_e32 v4, 0x1040, v4
	s_waitcnt vmcnt(10)
	ds_write2_b32 v39, v120, v121 offset0:4 offset1:69
	s_waitcnt vmcnt(8)
	ds_write2_b32 v39, v122, v123 offset0:134 offset1:199
	s_waitcnt vmcnt(6)
	ds_write2_b32 v54, v124, v125 offset0:8 offset1:73
	s_waitcnt vmcnt(4)
	ds_write2_b32 v54, v126, v127 offset0:138 offset1:203
	s_waitcnt vmcnt(2)
	ds_write2_b32 v55, v128, v129 offset0:12 offset1:77
	s_waitcnt vmcnt(0)
	ds_write2_b32 v55, v130, v131 offset0:142 offset1:207
	s_add_u32 s4, s34, 0xfffe6bc0
	s_addc_u32 s5, s35, -1
	s_lshl_b32 s3, s4, 3
	s_lshl_b64 s[4:5], s[4:5], 13
	s_and_b32 s3, s3, 0x3c0
	s_and_b32 s4, s4, 0xfff00000
	s_add_u32 s4, s45, s4
	s_addc_u32 s5, s46, s5
	s_waitcnt lgkmcnt(0)
	s_lshl_b32 s6, s34, 7
	s_and_b32 s6, s6, 0x380
	ds_read2_b32 v[38:39], v19 offset0:65 offset1:73
	ds_read2_b32 v[40:41], v19 offset1:8
	ds_read2_b32 v[54:55], v19 offset0:130 offset1:138
	ds_read2_b32 v[56:57], v19 offset0:195 offset1:203
	ds_read2_b32 v[58:59], v52 offset0:4 offset1:12
	ds_read2_b32 v[60:61], v52 offset0:69 offset1:77
	ds_read2_b32 v[62:63], v52 offset0:134 offset1:142
	ds_read2_b32 v[64:65], v52 offset0:199 offset1:207
	s_add_u32 s4, s4, s6
	s_addc_u32 s5, s5, 0
	s_waitcnt lgkmcnt(6)
	v_cvt_pk_bf16_f32 v2, v40, v38
	v_or_b32_e32 v38, s3, v42
	v_lshl_add_u64 v[66:67], s[4:5], 0, v[6:7]
	v_lshlrev_b32_e32 v68, 10, v38
	v_mov_b32_e32 v69, v7
	v_lshl_add_u64 v[68:69], v[66:67], 0, v[68:69]
	s_waitcnt lgkmcnt(4)
	v_cvt_pk_bf16_f32 v3, v54, v56
	s_waitcnt lgkmcnt(2)
	v_cvt_pk_bf16_f32 v4, v58, v60
	s_waitcnt lgkmcnt(0)
	v_cvt_pk_bf16_f32 v5, v62, v64
	global_store_dwordx4 v[68:69], v[2:5], off nt
	v_or_b32_e32 v38, s3, v43
	v_lshlrev_b32_e32 v38, 10, v38
	v_cvt_pk_bf16_f32 v2, v41, v39
	v_cvt_pk_bf16_f32 v3, v55, v57
	v_cvt_pk_bf16_f32 v4, v59, v61
	v_cvt_pk_bf16_f32 v5, v63, v65
	v_mov_b32_e32 v39, v7
	ds_read2_b32 v[40:41], v19 offset0:16 offset1:24
	ds_read2_b32 v[54:55], v19 offset0:81 offset1:89
	ds_read2_b32 v[56:57], v19 offset0:146 offset1:154
	ds_read2_b32 v[58:59], v19 offset0:211 offset1:219
	ds_read2_b32 v[60:61], v52 offset0:20 offset1:28
	ds_read2_b32 v[62:63], v52 offset0:85 offset1:93
	ds_read2_b32 v[64:65], v52 offset0:150 offset1:158
	ds_read2_b32 v[68:69], v52 offset0:215 offset1:223
	v_lshl_add_u64 v[38:39], v[66:67], 0, v[38:39]
	global_store_dwordx4 v[38:39], v[2:5], off nt
	v_or_b32_e32 v38, s3, v44
	v_lshlrev_b32_e32 v38, 10, v38
	v_mov_b32_e32 v39, v7
	v_lshl_add_u64 v[38:39], v[66:67], 0, v[38:39]
	s_waitcnt lgkmcnt(6)
	v_cvt_pk_bf16_f32 v2, v40, v54
	s_waitcnt lgkmcnt(4)
	v_cvt_pk_bf16_f32 v3, v56, v58
	s_waitcnt lgkmcnt(2)
	v_cvt_pk_bf16_f32 v4, v60, v62
	s_waitcnt lgkmcnt(0)
	v_cvt_pk_bf16_f32 v5, v64, v68
	global_store_dwordx4 v[38:39], v[2:5], off nt
	v_or_b32_e32 v38, s3, v45
	v_lshlrev_b32_e32 v38, 10, v38
	v_cvt_pk_bf16_f32 v2, v41, v55
	v_cvt_pk_bf16_f32 v3, v57, v59
	v_cvt_pk_bf16_f32 v4, v61, v63
	v_cvt_pk_bf16_f32 v5, v65, v69
	v_mov_b32_e32 v39, v7
	ds_read2_b32 v[40:41], v19 offset0:32 offset1:40
	ds_read2_b32 v[54:55], v19 offset0:97 offset1:105
	ds_read2_b32 v[56:57], v19 offset0:162 offset1:170
	ds_read2_b32 v[58:59], v19 offset0:227 offset1:235
	ds_read2_b32 v[60:61], v52 offset0:36 offset1:44
	ds_read2_b32 v[62:63], v52 offset0:101 offset1:109
	ds_read2_b32 v[64:65], v52 offset0:166 offset1:174
	ds_read2_b32 v[68:69], v52 offset0:231 offset1:239
	v_lshl_add_u64 v[38:39], v[66:67], 0, v[38:39]
	global_store_dwordx4 v[38:39], v[2:5], off nt
	v_or_b32_e32 v38, s3, v46
	v_lshlrev_b32_e32 v38, 10, v38
	v_mov_b32_e32 v39, v7
	v_lshl_add_u64 v[38:39], v[66:67], 0, v[38:39]
	s_waitcnt lgkmcnt(6)
	v_cvt_pk_bf16_f32 v2, v40, v54
	s_waitcnt lgkmcnt(4)
	v_cvt_pk_bf16_f32 v3, v56, v58
	s_waitcnt lgkmcnt(2)
	v_cvt_pk_bf16_f32 v4, v60, v62
	s_waitcnt lgkmcnt(0)
	v_cvt_pk_bf16_f32 v5, v64, v68
	global_store_dwordx4 v[38:39], v[2:5], off nt
	v_or_b32_e32 v38, s3, v47
	v_lshlrev_b32_e32 v38, 10, v38
	v_cvt_pk_bf16_f32 v2, v41, v55
	v_cvt_pk_bf16_f32 v3, v57, v59
	v_cvt_pk_bf16_f32 v4, v61, v63
	v_cvt_pk_bf16_f32 v5, v65, v69
	v_mov_b32_e32 v39, v7
	ds_read2_b32 v[40:41], v19 offset0:48 offset1:56
	ds_read2_b32 v[54:55], v19 offset0:113 offset1:121
	ds_read2_b32 v[56:57], v19 offset0:178 offset1:186
	ds_read2_b32 v[58:59], v19 offset0:243 offset1:251
	ds_read2_b32 v[60:61], v52 offset0:52 offset1:60
	ds_read2_b32 v[62:63], v52 offset0:117 offset1:125
	ds_read2_b32 v[64:65], v52 offset0:182 offset1:190
	ds_read2_b32 v[68:69], v52 offset0:247 offset1:255
	v_lshl_add_u64 v[38:39], v[66:67], 0, v[38:39]
	global_store_dwordx4 v[38:39], v[2:5], off nt
	v_or_b32_e32 v38, s3, v48
	v_lshlrev_b32_e32 v38, 10, v38
	v_mov_b32_e32 v39, v7
	v_lshl_add_u64 v[38:39], v[66:67], 0, v[38:39]
	s_waitcnt lgkmcnt(6)
	v_cvt_pk_bf16_f32 v2, v40, v54
	s_waitcnt lgkmcnt(4)
	v_cvt_pk_bf16_f32 v3, v56, v58
	s_waitcnt lgkmcnt(2)
	v_cvt_pk_bf16_f32 v4, v60, v62
	s_waitcnt lgkmcnt(0)
	v_cvt_pk_bf16_f32 v5, v64, v68
	global_store_dwordx4 v[38:39], v[2:5], off nt
	v_or_b32_e32 v38, s3, v49
	v_lshlrev_b32_e32 v38, 10, v38
	v_mov_b32_e32 v39, v7
	v_lshl_add_u64 v[38:39], v[66:67], 0, v[38:39]
	v_cvt_pk_bf16_f32 v2, v41, v55
	v_cvt_pk_bf16_f32 v3, v57, v59
	v_cvt_pk_bf16_f32 v4, v61, v63
	v_cvt_pk_bf16_f32 v5, v65, v69
	global_store_dwordx4 v[38:39], v[2:5], off nt
	s_waitcnt lgkmcnt(0)

.LBB0_46:
	v_lshl_add_u64 v[38:39], v[2:3], 0, s[4:5]
	v_add_co_u32_e32 v40, vcc, 0x5000, v38
	global_load_dword v100, v[38:39], off nt
	s_nop 0
	v_addc_co_u32_e32 v41, vcc, 0, v39, vcc
	v_add_co_u32_e32 v54, vcc, 0xa000, v38
	global_load_dword v101, v[40:41], off offset:32 nt
	s_nop 0
	v_addc_co_u32_e32 v55, vcc, 0, v39, vcc
	v_add_co_u32_e32 v40, vcc, 0xf000, v38
	s_add_u32 s4, s4, 0x50200
	s_nop 0
	v_addc_co_u32_e32 v41, vcc, 0, v39, vcc
	v_add_co_u32_e32 v56, vcc, 0x14000, v38
	global_load_dword v102, v[54:55], off offset:64 nt
	global_load_dword v103, v[40:41], off offset:96 nt
	v_addc_co_u32_e32 v57, vcc, 0, v39, vcc
	v_add_co_u32_e32 v40, vcc, 0x19000, v38
	s_addc_u32 s5, s5, 0
	s_nop 0
	v_addc_co_u32_e32 v41, vcc, 0, v39, vcc
	v_add_co_u32_e32 v54, vcc, 0x1e000, v38
	global_load_dword v104, v[56:57], off offset:128 nt
	global_load_dword v105, v[40:41], off offset:160 nt
	v_addc_co_u32_e32 v55, vcc, 0, v39, vcc
	v_add_co_u32_e32 v40, vcc, 0x23000, v38
	s_nop 0
	v_addc_co_u32_e32 v41, vcc, 0, v39, vcc
	v_add_co_u32_e32 v56, vcc, 0x28000, v38
	global_load_dword v106, v[54:55], off offset:192 nt
	global_load_dword v107, v[40:41], off offset:224 nt
	v_addc_co_u32_e32 v57, vcc, 0, v39, vcc
	v_add_co_u32_e32 v40, vcc, 0x2d000, v38
	s_nop 1
	v_addc_co_u32_e32 v41, vcc, 0, v39, vcc
	v_add_co_u32_e32 v54, vcc, 0x32000, v38
	global_load_dword v108, v[56:57], off offset:256 nt
	global_load_dword v109, v[40:41], off offset:288 nt
	v_addc_co_u32_e32 v55, vcc, 0, v39, vcc
	v_add_co_u32_e32 v40, vcc, 0x37000, v38
	s_nop 1
	v_addc_co_u32_e32 v41, vcc, 0, v39, vcc
	v_add_co_u32_e32 v56, vcc, 0x3c000, v38
	global_load_dword v110, v[54:55], off offset:320 nt
	global_load_dword v111, v[40:41], off offset:352 nt
	v_addc_co_u32_e32 v57, vcc, 0, v39, vcc
	v_add_co_u32_e32 v40, vcc, 0x41000, v38
	s_nop 1
	v_addc_co_u32_e32 v41, vcc, 0, v39, vcc
	v_add_co_u32_e32 v54, vcc, 0x46000, v38
	global_load_dword v112, v[56:57], off offset:384 nt
	s_nop 0
	global_load_dword v113, v[40:41], off offset:416 nt
	v_addc_co_u32_e32 v55, vcc, 0, v39, vcc
	v_add_co_u32_e32 v38, vcc, 0x4b000, v38
	s_nop 1
	v_addc_co_u32_e32 v39, vcc, 0, v39, vcc
	global_load_dword v114, v[54:55], off offset:448 nt
	s_nop 0
	global_load_dword v115, v[38:39], off offset:480 nt
	v_lshl_add_u64 v[38:39], v[2:3], 0, s[4:5]
	v_add_co_u32_e32 v40, vcc, 0x5000, v38
	global_load_dword v116, v[38:39], off nt
	s_nop 0
	v_addc_co_u32_e32 v41, vcc, 0, v39, vcc
	v_add_co_u32_e32 v54, vcc, 0xa000, v38
	global_load_dword v117, v[40:41], off offset:32 nt
	s_nop 0
	v_addc_co_u32_e32 v55, vcc, 0, v39, vcc
	v_add_co_u32_e32 v40, vcc, 0xf000, v38
	s_add_u32 s4, s4, 0x50200
	s_nop 0
	v_addc_co_u32_e32 v41, vcc, 0, v39, vcc
	v_add_co_u32_e32 v56, vcc, 0x14000, v38
	global_load_dword v118, v[54:55], off offset:64 nt
	global_load_dword v119, v[40:41], off offset:96 nt
	v_addc_co_u32_e32 v57, vcc, 0, v39, vcc
	v_add_co_u32_e32 v40, vcc, 0x19000, v38
	s_addc_u32 s5, s5, 0
	s_nop 0
	v_addc_co_u32_e32 v41, vcc, 0, v39, vcc
	v_add_co_u32_e32 v54, vcc, 0x1e000, v38
	global_load_dword v120, v[56:57], off offset:128 nt
	global_load_dword v121, v[40:41], off offset:160 nt
	v_addc_co_u32_e32 v55, vcc, 0, v39, vcc
	v_add_co_u32_e32 v40, vcc, 0x23000, v38
	s_nop 0
	v_addc_co_u32_e32 v41, vcc, 0, v39, vcc
	v_add_co_u32_e32 v56, vcc, 0x28000, v38
	global_load_dword v122, v[54:55], off offset:192 nt
	global_load_dword v123, v[40:41], off offset:224 nt
	v_addc_co_u32_e32 v57, vcc, 0, v39, vcc
	v_add_co_u32_e32 v40, vcc, 0x2d000, v38
	s_nop 1
	v_addc_co_u32_e32 v41, vcc, 0, v39, vcc
	v_add_co_u32_e32 v54, vcc, 0x32000, v38
	global_load_dword v124, v[56:57], off offset:256 nt
	global_load_dword v125, v[40:41], off offset:288 nt
	v_addc_co_u32_e32 v55, vcc, 0, v39, vcc
	v_add_co_u32_e32 v40, vcc, 0x37000, v38
	s_nop 1
	v_addc_co_u32_e32 v41, vcc, 0, v39, vcc
	v_add_co_u32_e32 v56, vcc, 0x3c000, v38
	global_load_dword v126, v[54:55], off offset:320 nt
	global_load_dword v127, v[40:41], off offset:352 nt
	v_addc_co_u32_e32 v57, vcc, 0, v39, vcc
	v_add_co_u32_e32 v40, vcc, 0x41000, v38
	s_nop 1
	v_addc_co_u32_e32 v41, vcc, 0, v39, vcc
	v_add_co_u32_e32 v54, vcc, 0x46000, v38
	global_load_dword v128, v[56:57], off offset:384 nt
	s_nop 0
	global_load_dword v129, v[40:41], off offset:416 nt
	v_addc_co_u32_e32 v55, vcc, 0, v39, vcc
	v_add_co_u32_e32 v38, vcc, 0x4b000, v38
	s_nop 1
	v_addc_co_u32_e32 v39, vcc, 0, v39, vcc
	global_load_dword v130, v[54:55], off offset:448 nt
	s_nop 0
	global_load_dword v131, v[38:39], off offset:480 nt
	v_add_u32_e32 v39, 0x400, v4
	v_add_u32_e32 v54, 0x800, v4
	v_add_u32_e32 v55, 0xc00, v4
	s_waitcnt vmcnt(30)
	ds_write2_b32 v4, v100, v101 offset1:65
	s_waitcnt vmcnt(28)
	ds_write2_b32 v4, v102, v103 offset0:130 offset1:195
	v_add_u32_e32 v4, 0x1040, v4
	s_waitcnt vmcnt(26)
	ds_write2_b32 v39, v104, v105 offset0:4 offset1:69
	s_waitcnt vmcnt(24)
	ds_write2_b32 v39, v106, v107 offset0:134 offset1:199
	s_waitcnt vmcnt(22)
	ds_write2_b32 v54, v108, v109 offset0:8 offset1:73
	s_waitcnt vmcnt(20)
	ds_write2_b32 v54, v110, v111 offset0:138 offset1:203
	s_waitcnt vmcnt(18)
	ds_write2_b32 v55, v112, v113 offset0:12 offset1:77
	s_waitcnt vmcnt(16)
	ds_write2_b32 v55, v114, v115 offset0:142 offset1:207
	v_lshl_add_u64 v[38:39], v[2:3], 0, s[4:5]
	v_add_co_u32_e32 v40, vcc, 0x5000, v38
	global_load_dword v100, v[38:39], off nt
	s_nop 0
	v_addc_co_u32_e32 v41, vcc, 0, v39, vcc
	v_add_co_u32_e32 v54, vcc, 0xa000, v38
	global_load_dword v101, v[40:41], off offset:32 nt
	s_nop 0
	v_addc_co_u32_e32 v55, vcc, 0, v39, vcc
	v_add_co_u32_e32 v40, vcc, 0xf000, v38
	s_add_u32 s4, s4, 0x50200
	s_nop 0
	v_addc_co_u32_e32 v41, vcc, 0, v39, vcc
	v_add_co_u32_e32 v56, vcc, 0x14000, v38
	global_load_dword v102, v[54:55], off offset:64 nt
	global_load_dword v103, v[40:41], off offset:96 nt
	v_addc_co_u32_e32 v57, vcc, 0, v39, vcc
	v_add_co_u32_e32 v40, vcc, 0x19000, v38
	s_addc_u32 s5, s5, 0
	s_nop 0
	v_addc_co_u32_e32 v41, vcc, 0, v39, vcc
	v_add_co_u32_e32 v54, vcc, 0x1e000, v38
	global_load_dword v104, v[56:57], off offset:128 nt
	global_load_dword v105, v[40:41], off offset:160 nt
	v_addc_co_u32_e32 v55, vcc, 0, v39, vcc
	v_add_co_u32_e32 v40, vcc, 0x23000, v38
	s_nop 0
	v_addc_co_u32_e32 v41, vcc, 0, v39, vcc
	v_add_co_u32_e32 v56, vcc, 0x28000, v38
	global_load_dword v106, v[54:55], off offset:192 nt
	global_load_dword v107, v[40:41], off offset:224 nt
	v_addc_co_u32_e32 v57, vcc, 0, v39, vcc
	v_add_co_u32_e32 v40, vcc, 0x2d000, v38
	s_nop 1
	v_addc_co_u32_e32 v41, vcc, 0, v39, vcc
	v_add_co_u32_e32 v54, vcc, 0x32000, v38
	global_load_dword v108, v[56:57], off offset:256 nt
	global_load_dword v109, v[40:41], off offset:288 nt
	v_addc_co_u32_e32 v55, vcc, 0, v39, vcc
	v_add_co_u32_e32 v40, vcc, 0x37000, v38
	s_nop 1
	v_addc_co_u32_e32 v41, vcc, 0, v39, vcc
	v_add_co_u32_e32 v56, vcc, 0x3c000, v38
	global_load_dword v110, v[54:55], off offset:320 nt
	global_load_dword v111, v[40:41], off offset:352 nt
	v_addc_co_u32_e32 v57, vcc, 0, v39, vcc
	v_add_co_u32_e32 v40, vcc, 0x41000, v38
	s_nop 1
	v_addc_co_u32_e32 v41, vcc, 0, v39, vcc
	v_add_co_u32_e32 v54, vcc, 0x46000, v38
	global_load_dword v112, v[56:57], off offset:384 nt
	s_nop 0
	global_load_dword v113, v[40:41], off offset:416 nt
	v_addc_co_u32_e32 v55, vcc, 0, v39, vcc
	v_add_co_u32_e32 v38, vcc, 0x4b000, v38
	s_nop 1
	v_addc_co_u32_e32 v39, vcc, 0, v39, vcc
	global_load_dword v114, v[54:55], off offset:448 nt
	s_nop 0
	global_load_dword v115, v[38:39], off offset:480 nt
	v_add_u32_e32 v39, 0x400, v4
	v_add_u32_e32 v54, 0x800, v4
	v_add_u32_e32 v55, 0xc00, v4
	s_waitcnt vmcnt(30)
	ds_write2_b32 v4, v116, v117 offset1:65
	s_waitcnt vmcnt(28)
	ds_write2_b32 v4, v118, v119 offset0:130 offset1:195
	v_add_u32_e32 v4, 0x1040, v4
	s_waitcnt vmcnt(26)
	ds_write2_b32 v39, v120, v121 offset0:4 offset1:69
	s_waitcnt vmcnt(24)
	ds_write2_b32 v39, v122, v123 offset0:134 offset1:199
	s_waitcnt vmcnt(22)
	ds_write2_b32 v54, v124, v125 offset0:8 offset1:73
	s_waitcnt vmcnt(20)
	ds_write2_b32 v54, v126, v127 offset0:138 offset1:203
	s_waitcnt vmcnt(18)
	ds_write2_b32 v55, v128, v129 offset0:12 offset1:77
	s_waitcnt vmcnt(16)
	ds_write2_b32 v55, v130, v131 offset0:142 offset1:207
	v_lshl_add_u64 v[38:39], v[2:3], 0, s[4:5]
	v_add_co_u32_e32 v40, vcc, 0x5000, v38
	global_load_dword v116, v[38:39], off nt
	s_nop 0
	v_addc_co_u32_e32 v41, vcc, 0, v39, vcc
	v_add_co_u32_e32 v54, vcc, 0xa000, v38
	global_load_dword v117, v[40:41], off offset:32 nt
	s_nop 0
	v_addc_co_u32_e32 v55, vcc, 0, v39, vcc
	v_add_co_u32_e32 v40, vcc, 0xf000, v38
	s_add_u32 s4, s4, 0x50200
	s_nop 0
	v_addc_co_u32_e32 v41, vcc, 0, v39, vcc
	v_add_co_u32_e32 v56, vcc, 0x14000, v38
	global_load_dword v118, v[54:55], off offset:64 nt
	global_load_dword v119, v[40:41], off offset:96 nt
	v_addc_co_u32_e32 v57, vcc, 0, v39, vcc
	v_add_co_u32_e32 v40, vcc, 0x19000, v38
	s_addc_u32 s5, s5, 0
	s_nop 0
	v_addc_co_u32_e32 v41, vcc, 0, v39, vcc
	v_add_co_u32_e32 v54, vcc, 0x1e000, v38
	global_load_dword v120, v[56:57], off offset:128 nt
	global_load_dword v121, v[40:41], off offset:160 nt
	v_addc_co_u32_e32 v55, vcc, 0, v39, vcc
	v_add_co_u32_e32 v40, vcc, 0x23000, v38
	s_nop 0
	v_addc_co_u32_e32 v41, vcc, 0, v39, vcc
	v_add_co_u32_e32 v56, vcc, 0x28000, v38
	global_load_dword v122, v[54:55], off offset:192 nt
	global_load_dword v123, v[40:41], off offset:224 nt
	v_addc_co_u32_e32 v57, vcc, 0, v39, vcc
	v_add_co_u32_e32 v40, vcc, 0x2d000, v38
	s_nop 1
	v_addc_co_u32_e32 v41, vcc, 0, v39, vcc
	v_add_co_u32_e32 v54, vcc, 0x32000, v38
	global_load_dword v124, v[56:57], off offset:256 nt
	global_load_dword v125, v[40:41], off offset:288 nt
	v_addc_co_u32_e32 v55, vcc, 0, v39, vcc
	v_add_co_u32_e32 v40, vcc, 0x37000, v38
	s_nop 1
	v_addc_co_u32_e32 v41, vcc, 0, v39, vcc
	v_add_co_u32_e32 v56, vcc, 0x3c000, v38
	global_load_dword v126, v[54:55], off offset:320 nt
	global_load_dword v127, v[40:41], off offset:352 nt
	v_addc_co_u32_e32 v57, vcc, 0, v39, vcc
	v_add_co_u32_e32 v40, vcc, 0x41000, v38
	s_nop 1
	v_addc_co_u32_e32 v41, vcc, 0, v39, vcc
	v_add_co_u32_e32 v54, vcc, 0x46000, v38
	global_load_dword v128, v[56:57], off offset:384 nt
	s_nop 0
	global_load_dword v129, v[40:41], off offset:416 nt
	v_addc_co_u32_e32 v55, vcc, 0, v39, vcc
	v_add_co_u32_e32 v38, vcc, 0x4b000, v38
	s_nop 1
	v_addc_co_u32_e32 v39, vcc, 0, v39, vcc
	global_load_dword v130, v[54:55], off offset:448 nt
	s_nop 0
	global_load_dword v131, v[38:39], off offset:480 nt
	v_add_u32_e32 v39, 0x400, v4
	v_add_u32_e32 v54, 0x800, v4
	v_add_u32_e32 v55, 0xc00, v4
	s_waitcnt vmcnt(30)
	ds_write2_b32 v4, v100, v101 offset1:65
	s_waitcnt vmcnt(28)
	ds_write2_b32 v4, v102, v103 offset0:130 offset1:195
	v_add_u32_e32 v4, 0x1040, v4
	s_waitcnt vmcnt(26)
	ds_write2_b32 v39, v104, v105 offset0:4 offset1:69
	s_waitcnt vmcnt(24)
	ds_write2_b32 v39, v106, v107 offset0:134 offset1:199
	s_waitcnt vmcnt(22)
	ds_write2_b32 v54, v108, v109 offset0:8 offset1:73
	s_waitcnt vmcnt(20)
	ds_write2_b32 v54, v110, v111 offset0:138 offset1:203
	s_waitcnt vmcnt(18)
	ds_write2_b32 v55, v112, v113 offset0:12 offset1:77
	s_waitcnt vmcnt(16)
	ds_write2_b32 v55, v114, v115 offset0:142 offset1:207
	v_add_u32_e32 v39, 0x400, v4
	v_add_u32_e32 v54, 0x800, v4
	v_add_u32_e32 v55, 0xc00, v4
	s_waitcnt vmcnt(14)
	ds_write2_b32 v4, v116, v117 offset1:65
	s_waitcnt vmcnt(12)
	ds_write2_b32 v4, v118, v119 offset0:130 offset1:195
	v_add_u32_e32 v4, 0x1040, v4
	s_waitcnt vmcnt(10)
	ds_write2_b32 v39, v120, v121 offset0:4 offset1:69
	s_waitcnt vmcnt(8)
	ds_write2_b32 v39, v122, v123 offset0:134 offset1:199
	s_waitcnt vmcnt(6)
	ds_write2_b32 v54, v124, v125 offset0:8 offset1:73
	s_waitcnt vmcnt(4)
	ds_write2_b32 v54, v126, v127 offset0:138 offset1:203
	s_waitcnt vmcnt(2)
	ds_write2_b32 v55, v128, v129 offset0:12 offset1:77
	s_waitcnt vmcnt(0)
	ds_write2_b32 v55, v130, v131 offset0:142 offset1:207
	s_mul_i32 s7, s7, 0xa00000
	s_add_u32 s4, s47, s7
	s_addc_u32 s5, s48, 0
	s_lshl_b32 s7, s36, 1
	s_add_u32 s4, s4, s7
	s_addc_u32 s5, s5, 0
	s_cmpk_lt_u32 s3, 0x1408
	v_lshl_add_u64 v[38:39], s[4:5], 0, v[6:7]
	s_cselect_b64 s[4:5], -1, 0
	s_and_b32 s6, 0xffff, s6
	s_cmpk_lt_u32 s6, 0x180
	v_or_b32_e32 v2, s3, v42
	s_cselect_b64 vcc, -1, 0
	s_cmpk_gt_u32 s3, 0x607
	v_add_u32_e32 v3, -8, v2
	s_cselect_b64 s[6:7], -1, 0
	s_waitcnt lgkmcnt(0)
	v_cndmask_b32_e64 v3, -1, v3, s[6:7]
	v_cndmask_b32_e32 v4, v3, v2, vcc
	ds_read2_b32 v[2:3], v19 offset1:65
	v_cndmask_b32_e64 v40, -1, v4, s[4:5]
	ds_read2_b32 v[4:5], v19 offset0:130 offset1:195
	ds_read2_b32 v[54:55], v52 offset0:4 offset1:69
	v_cmp_lt_i32_e64 s[4:5], s68, v40
	ds_read2_b32 v[56:57], v52 offset0:134 offset1:199
	s_nop 0
	v_cndmask_b32_e64 v41, 1.0, v53, s[4:5]
	s_waitcnt lgkmcnt(3)
	v_mul_f32_e32 v2, v41, v2
	v_mul_f32_e32 v3, v41, v3
	v_cvt_pk_bf16_f32 v2, v2, v3
	s_waitcnt lgkmcnt(2)
	v_mul_f32_e32 v3, v41, v4
	v_mul_f32_e32 v4, v41, v5
	v_cvt_pk_bf16_f32 v3, v3, v4
	s_waitcnt lgkmcnt(1)
	v_mul_f32_e32 v4, v41, v54
	v_mul_f32_e32 v5, v41, v55
	v_cvt_pk_bf16_f32 v4, v4, v5
	s_waitcnt lgkmcnt(0)
	v_mul_f32_e32 v5, v41, v56
	v_cmp_lt_i32_e64 s[4:5], -1, v40
	v_mul_f32_e32 v41, v41, v57
	v_cvt_pk_bf16_f32 v5, v5, v41
	s_and_saveexec_b64 s[6:7], s[4:5]
	s_cbranch_execz .LBB0_49
	v_mov_b32_e32 v41, v7
	v_lshlrev_b64 v[40:41], 11, v[40:41]
	v_lshl_add_u64 v[40:41], v[38:39], 0, v[40:41]
	global_store_dwordx4 v[40:41], v[2:5], off nt

.LBB0_67:
	v_lshl_add_u64 v[38:39], v[2:3], 0, s[4:5]
	v_add_co_u32_e32 v40, vcc, 0x1000, v38
	global_load_dword v100, v[38:39], off nt
	s_nop 0
	v_addc_co_u32_e32 v41, vcc, 0, v39, vcc
	v_add_co_u32_e32 v54, vcc, 0x2000, v38
	global_load_dword v101, v[40:41], off nt
	s_nop 0
	v_addc_co_u32_e32 v55, vcc, 0, v39, vcc
	v_add_co_u32_e32 v40, vcc, 0x3000, v38
	s_add_u32 s4, s4, 0x10000
	s_nop 0
	v_addc_co_u32_e32 v41, vcc, 0, v39, vcc
	v_add_co_u32_e32 v56, vcc, 0x4000, v38
	global_load_dword v102, v[54:55], off nt
	global_load_dword v103, v[40:41], off nt
	v_addc_co_u32_e32 v57, vcc, 0, v39, vcc
	v_add_co_u32_e32 v40, vcc, 0x5000, v38
	s_addc_u32 s5, s5, 0
	s_nop 0
	v_addc_co_u32_e32 v41, vcc, 0, v39, vcc
	v_add_co_u32_e32 v54, vcc, 0x6000, v38
	global_load_dword v104, v[56:57], off nt
	global_load_dword v105, v[40:41], off nt
	v_addc_co_u32_e32 v55, vcc, 0, v39, vcc
	v_add_co_u32_e32 v40, vcc, 0x7000, v38
	s_nop 0
	v_addc_co_u32_e32 v41, vcc, 0, v39, vcc
	v_add_co_u32_e32 v56, vcc, 0x8000, v38
	global_load_dword v106, v[54:55], off nt
	global_load_dword v107, v[40:41], off nt
	v_addc_co_u32_e32 v57, vcc, 0, v39, vcc
	v_add_co_u32_e32 v40, vcc, 0x9000, v38
	s_nop 1
	v_addc_co_u32_e32 v41, vcc, 0, v39, vcc
	v_add_co_u32_e32 v54, vcc, 0xa000, v38
	global_load_dword v108, v[56:57], off nt
	global_load_dword v109, v[40:41], off nt
	v_addc_co_u32_e32 v55, vcc, 0, v39, vcc
	v_add_co_u32_e32 v40, vcc, 0xb000, v38
	s_nop 1
	v_addc_co_u32_e32 v41, vcc, 0, v39, vcc
	v_add_co_u32_e32 v56, vcc, 0xc000, v38
	global_load_dword v110, v[54:55], off nt
	global_load_dword v111, v[40:41], off nt
	v_addc_co_u32_e32 v57, vcc, 0, v39, vcc
	v_add_co_u32_e32 v40, vcc, 0xd000, v38
	s_nop 1
	v_addc_co_u32_e32 v41, vcc, 0, v39, vcc
	v_add_co_u32_e32 v54, vcc, 0xe000, v38
	global_load_dword v112, v[56:57], off nt
	s_nop 0
	global_load_dword v113, v[40:41], off nt
	v_addc_co_u32_e32 v55, vcc, 0, v39, vcc
	v_add_co_u32_e32 v38, vcc, 0xf000, v38
	s_nop 1
	v_addc_co_u32_e32 v39, vcc, 0, v39, vcc
	global_load_dword v114, v[54:55], off nt
	s_nop 0
	global_load_dword v115, v[38:39], off nt
	v_lshl_add_u64 v[38:39], v[2:3], 0, s[4:5]
	v_add_co_u32_e32 v40, vcc, 0x1000, v38
	global_load_dword v116, v[38:39], off nt
	s_nop 0
	v_addc_co_u32_e32 v41, vcc, 0, v39, vcc
	v_add_co_u32_e32 v54, vcc, 0x2000, v38
	global_load_dword v117, v[40:41], off nt
	s_nop 0
	v_addc_co_u32_e32 v55, vcc, 0, v39, vcc
	v_add_co_u32_e32 v40, vcc, 0x3000, v38
	s_add_u32 s4, s4, 0x10000
	s_nop 0
	v_addc_co_u32_e32 v41, vcc, 0, v39, vcc
	v_add_co_u32_e32 v56, vcc, 0x4000, v38
	global_load_dword v118, v[54:55], off nt
	global_load_dword v119, v[40:41], off nt
	v_addc_co_u32_e32 v57, vcc, 0, v39, vcc
	v_add_co_u32_e32 v40, vcc, 0x5000, v38
	s_addc_u32 s5, s5, 0
	s_nop 0
	v_addc_co_u32_e32 v41, vcc, 0, v39, vcc
	v_add_co_u32_e32 v54, vcc, 0x6000, v38
	global_load_dword v120, v[56:57], off nt
	global_load_dword v121, v[40:41], off nt
	v_addc_co_u32_e32 v55, vcc, 0, v39, vcc
	v_add_co_u32_e32 v40, vcc, 0x7000, v38
	s_nop 0
	v_addc_co_u32_e32 v41, vcc, 0, v39, vcc
	v_add_co_u32_e32 v56, vcc, 0x8000, v38
	global_load_dword v122, v[54:55], off nt
	global_load_dword v123, v[40:41], off nt
	v_addc_co_u32_e32 v57, vcc, 0, v39, vcc
	v_add_co_u32_e32 v40, vcc, 0x9000, v38
	s_nop 1
	v_addc_co_u32_e32 v41, vcc, 0, v39, vcc
	v_add_co_u32_e32 v54, vcc, 0xa000, v38
	global_load_dword v124, v[56:57], off nt
	global_load_dword v125, v[40:41], off nt
	v_addc_co_u32_e32 v55, vcc, 0, v39, vcc
	v_add_co_u32_e32 v40, vcc, 0xb000, v38
	s_nop 1
	v_addc_co_u32_e32 v41, vcc, 0, v39, vcc
	v_add_co_u32_e32 v56, vcc, 0xc000, v38
	global_load_dword v126, v[54:55], off nt
	global_load_dword v127, v[40:41], off nt
	v_addc_co_u32_e32 v57, vcc, 0, v39, vcc
	v_add_co_u32_e32 v40, vcc, 0xd000, v38
	s_nop 1
	v_addc_co_u32_e32 v41, vcc, 0, v39, vcc
	v_add_co_u32_e32 v54, vcc, 0xe000, v38
	global_load_dword v128, v[56:57], off nt
	s_nop 0
	global_load_dword v129, v[40:41], off nt
	v_addc_co_u32_e32 v55, vcc, 0, v39, vcc
	v_add_co_u32_e32 v38, vcc, 0xf000, v38
	s_nop 1
	v_addc_co_u32_e32 v39, vcc, 0, v39, vcc
	global_load_dword v130, v[54:55], off nt
	s_nop 0
	global_load_dword v131, v[38:39], off nt
	v_add_u32_e32 v39, 0x400, v4
	v_add_u32_e32 v54, 0x800, v4
	v_add_u32_e32 v55, 0xc00, v4
	s_waitcnt vmcnt(30)
	ds_write2_b32 v4, v100, v101 offset1:65
	s_waitcnt vmcnt(28)
	ds_write2_b32 v4, v102, v103 offset0:130 offset1:195
	v_add_u32_e32 v4, 0x1040, v4
	s_waitcnt vmcnt(26)
	ds_write2_b32 v39, v104, v105 offset0:4 offset1:69
	s_waitcnt vmcnt(24)
	ds_write2_b32 v39, v106, v107 offset0:134 offset1:199
	s_waitcnt vmcnt(22)
	ds_write2_b32 v54, v108, v109 offset0:8 offset1:73
	s_waitcnt vmcnt(20)
	ds_write2_b32 v54, v110, v111 offset0:138 offset1:203
	s_waitcnt vmcnt(18)
	ds_write2_b32 v55, v112, v113 offset0:12 offset1:77
	s_waitcnt vmcnt(16)
	ds_write2_b32 v55, v114, v115 offset0:142 offset1:207
	v_lshl_add_u64 v[38:39], v[2:3], 0, s[4:5]
	v_add_co_u32_e32 v40, vcc, 0x1000, v38
	global_load_dword v100, v[38:39], off nt
	s_nop 0
	v_addc_co_u32_e32 v41, vcc, 0, v39, vcc
	v_add_co_u32_e32 v54, vcc, 0x2000, v38
	global_load_dword v101, v[40:41], off nt
	s_nop 0
	v_addc_co_u32_e32 v55, vcc, 0, v39, vcc
	v_add_co_u32_e32 v40, vcc, 0x3000, v38
	s_add_u32 s4, s4, 0x10000
	s_nop 0
	v_addc_co_u32_e32 v41, vcc, 0, v39, vcc
	v_add_co_u32_e32 v56, vcc, 0x4000, v38
	global_load_dword v102, v[54:55], off nt
	global_load_dword v103, v[40:41], off nt
	v_addc_co_u32_e32 v57, vcc, 0, v39, vcc
	v_add_co_u32_e32 v40, vcc, 0x5000, v38
	s_addc_u32 s5, s5, 0
	s_nop 0
	v_addc_co_u32_e32 v41, vcc, 0, v39, vcc
	v_add_co_u32_e32 v54, vcc, 0x6000, v38
	global_load_dword v104, v[56:57], off nt
	global_load_dword v105, v[40:41], off nt
	v_addc_co_u32_e32 v55, vcc, 0, v39, vcc
	v_add_co_u32_e32 v40, vcc, 0x7000, v38
	s_nop 0
	v_addc_co_u32_e32 v41, vcc, 0, v39, vcc
	v_add_co_u32_e32 v56, vcc, 0x8000, v38
	global_load_dword v106, v[54:55], off nt
	global_load_dword v107, v[40:41], off nt
	v_addc_co_u32_e32 v57, vcc, 0, v39, vcc
	v_add_co_u32_e32 v40, vcc, 0x9000, v38
	s_nop 1
	v_addc_co_u32_e32 v41, vcc, 0, v39, vcc
	v_add_co_u32_e32 v54, vcc, 0xa000, v38
	global_load_dword v108, v[56:57], off nt
	global_load_dword v109, v[40:41], off nt
	v_addc_co_u32_e32 v55, vcc, 0, v39, vcc
	v_add_co_u32_e32 v40, vcc, 0xb000, v38
	s_nop 1
	v_addc_co_u32_e32 v41, vcc, 0, v39, vcc
	v_add_co_u32_e32 v56, vcc, 0xc000, v38
	global_load_dword v110, v[54:55], off nt
	global_load_dword v111, v[40:41], off nt
	v_addc_co_u32_e32 v57, vcc, 0, v39, vcc
	v_add_co_u32_e32 v40, vcc, 0xd000, v38
	s_nop 1
	v_addc_co_u32_e32 v41, vcc, 0, v39, vcc
	v_add_co_u32_e32 v54, vcc, 0xe000, v38
	global_load_dword v112, v[56:57], off nt
	s_nop 0
	global_load_dword v113, v[40:41], off nt
	v_addc_co_u32_e32 v55, vcc, 0, v39, vcc
	v_add_co_u32_e32 v38, vcc, 0xf000, v38
	s_nop 1
	v_addc_co_u32_e32 v39, vcc, 0, v39, vcc
	global_load_dword v114, v[54:55], off nt
	s_nop 0
	global_load_dword v115, v[38:39], off nt
	v_add_u32_e32 v39, 0x400, v4
	v_add_u32_e32 v54, 0x800, v4
	v_add_u32_e32 v55, 0xc00, v4
	s_waitcnt vmcnt(30)
	ds_write2_b32 v4, v116, v117 offset1:65
	s_waitcnt vmcnt(28)
	ds_write2_b32 v4, v118, v119 offset0:130 offset1:195
	v_add_u32_e32 v4, 0x1040, v4
	s_waitcnt vmcnt(26)
	ds_write2_b32 v39, v120, v121 offset0:4 offset1:69
	s_waitcnt vmcnt(24)
	ds_write2_b32 v39, v122, v123 offset0:134 offset1:199
	s_waitcnt vmcnt(22)
	ds_write2_b32 v54, v124, v125 offset0:8 offset1:73
	s_waitcnt vmcnt(20)
	ds_write2_b32 v54, v126, v127 offset0:138 offset1:203
	s_waitcnt vmcnt(18)
	ds_write2_b32 v55, v128, v129 offset0:12 offset1:77
	s_waitcnt vmcnt(16)
	ds_write2_b32 v55, v130, v131 offset0:142 offset1:207
	v_lshl_add_u64 v[38:39], v[2:3], 0, s[4:5]
	v_add_co_u32_e32 v40, vcc, 0x1000, v38
	global_load_dword v116, v[38:39], off nt
	s_nop 0
	v_addc_co_u32_e32 v41, vcc, 0, v39, vcc
	v_add_co_u32_e32 v54, vcc, 0x2000, v38
	global_load_dword v117, v[40:41], off nt
	s_nop 0
	v_addc_co_u32_e32 v55, vcc, 0, v39, vcc
	v_add_co_u32_e32 v40, vcc, 0x3000, v38
	s_add_u32 s4, s4, 0x10000
	s_nop 0
	v_addc_co_u32_e32 v41, vcc, 0, v39, vcc
	v_add_co_u32_e32 v56, vcc, 0x4000, v38
	global_load_dword v118, v[54:55], off nt
	global_load_dword v119, v[40:41], off nt
	v_addc_co_u32_e32 v57, vcc, 0, v39, vcc
	v_add_co_u32_e32 v40, vcc, 0x5000, v38
	s_addc_u32 s5, s5, 0
	s_nop 0
	v_addc_co_u32_e32 v41, vcc, 0, v39, vcc
	v_add_co_u32_e32 v54, vcc, 0x6000, v38
	global_load_dword v120, v[56:57], off nt
	global_load_dword v121, v[40:41], off nt
	v_addc_co_u32_e32 v55, vcc, 0, v39, vcc
	v_add_co_u32_e32 v40, vcc, 0x7000, v38
	s_nop 0
	v_addc_co_u32_e32 v41, vcc, 0, v39, vcc
	v_add_co_u32_e32 v56, vcc, 0x8000, v38
	global_load_dword v122, v[54:55], off nt
	global_load_dword v123, v[40:41], off nt
	v_addc_co_u32_e32 v57, vcc, 0, v39, vcc
	v_add_co_u32_e32 v40, vcc, 0x9000, v38
	s_nop 1
	v_addc_co_u32_e32 v41, vcc, 0, v39, vcc
	v_add_co_u32_e32 v54, vcc, 0xa000, v38
	global_load_dword v124, v[56:57], off nt
	global_load_dword v125, v[40:41], off nt
	v_addc_co_u32_e32 v55, vcc, 0, v39, vcc
	v_add_co_u32_e32 v40, vcc, 0xb000, v38
	s_nop 1
	v_addc_co_u32_e32 v41, vcc, 0, v39, vcc
	v_add_co_u32_e32 v56, vcc, 0xc000, v38
	global_load_dword v126, v[54:55], off nt
	global_load_dword v127, v[40:41], off nt
	v_addc_co_u32_e32 v57, vcc, 0, v39, vcc
	v_add_co_u32_e32 v40, vcc, 0xd000, v38
	s_nop 1
	v_addc_co_u32_e32 v41, vcc, 0, v39, vcc
	v_add_co_u32_e32 v54, vcc, 0xe000, v38
	global_load_dword v128, v[56:57], off nt
	s_nop 0
	global_load_dword v129, v[40:41], off nt
	v_addc_co_u32_e32 v55, vcc, 0, v39, vcc
	v_add_co_u32_e32 v38, vcc, 0xf000, v38
	s_nop 1
	v_addc_co_u32_e32 v39, vcc, 0, v39, vcc
	global_load_dword v130, v[54:55], off nt
	s_nop 0
	global_load_dword v131, v[38:39], off nt
	v_add_u32_e32 v39, 0x400, v4
	v_add_u32_e32 v54, 0x800, v4
	v_add_u32_e32 v55, 0xc00, v4
	s_waitcnt vmcnt(30)
	ds_write2_b32 v4, v100, v101 offset1:65
	s_waitcnt vmcnt(28)
	ds_write2_b32 v4, v102, v103 offset0:130 offset1:195
	v_add_u32_e32 v4, 0x1040, v4
	s_waitcnt vmcnt(26)
	ds_write2_b32 v39, v104, v105 offset0:4 offset1:69
	s_waitcnt vmcnt(24)
	ds_write2_b32 v39, v106, v107 offset0:134 offset1:199
	s_waitcnt vmcnt(22)
	ds_write2_b32 v54, v108, v109 offset0:8 offset1:73
	s_waitcnt vmcnt(20)
	ds_write2_b32 v54, v110, v111 offset0:138 offset1:203
	s_waitcnt vmcnt(18)
	ds_write2_b32 v55, v112, v113 offset0:12 offset1:77
	s_waitcnt vmcnt(16)
	ds_write2_b32 v55, v114, v115 offset0:142 offset1:207
	v_add_u32_e32 v39, 0x400, v4
	v_add_u32_e32 v54, 0x800, v4
	v_add_u32_e32 v55, 0xc00, v4
	s_waitcnt vmcnt(14)
	ds_write2_b32 v4, v116, v117 offset1:65
	s_waitcnt vmcnt(12)
	ds_write2_b32 v4, v118, v119 offset0:130 offset1:195
	v_add_u32_e32 v4, 0x1040, v4
	s_waitcnt vmcnt(10)
	ds_write2_b32 v39, v120, v121 offset0:4 offset1:69
	s_waitcnt vmcnt(8)
	ds_write2_b32 v39, v122, v123 offset0:134 offset1:199
	s_waitcnt vmcnt(6)
	ds_write2_b32 v54, v124, v125 offset0:8 offset1:73
	s_waitcnt vmcnt(4)
	ds_write2_b32 v54, v126, v127 offset0:138 offset1:203
	s_waitcnt vmcnt(2)
	ds_write2_b32 v55, v128, v129 offset0:12 offset1:77
	s_waitcnt vmcnt(0)
	ds_write2_b32 v55, v130, v131 offset0:142 offset1:207
	s_lshl_b64 s[4:5], s[34:35], 12
	s_add_u32 s3, s4, 0xf0000000
	s_addc_u32 s4, s5, 0xfffff
	s_and_b32 s5, s4, 0xfffff
	s_and_b32 s4, s3, 0xfff00000
	s_lshl_b32 s3, s34, 2
	s_and_b32 s3, s3, 0x3c0
	s_lshl_b64 s[4:5], s[4:5], 1
	s_add_u32 s4, s49, s4
	s_addc_u32 s5, s50, s5
	s_waitcnt lgkmcnt(0)
	s_lshl_b32 s6, s34, 7
	s_and_b32 s6, s6, 0x780
	ds_read2_b32 v[38:39], v19 offset0:65 offset1:73
	ds_read2_b32 v[40:41], v19 offset1:8
	ds_read2_b32 v[54:55], v19 offset0:130 offset1:138
	ds_read2_b32 v[56:57], v19 offset0:195 offset1:203
	ds_read2_b32 v[58:59], v52 offset0:4 offset1:12
	ds_read2_b32 v[60:61], v52 offset0:69 offset1:77
	ds_read2_b32 v[62:63], v52 offset0:134 offset1:142
	ds_read2_b32 v[64:65], v52 offset0:199 offset1:207
	s_add_u32 s4, s4, s6
	s_addc_u32 s5, s5, 0
	s_waitcnt lgkmcnt(6)
	v_cvt_pk_bf16_f32 v2, v40, v38
	v_or_b32_e32 v38, s3, v42
	v_lshl_add_u64 v[66:67], s[4:5], 0, v[6:7]
	v_lshlrev_b32_e32 v68, 11, v38
	v_mov_b32_e32 v69, v7
	v_lshl_add_u64 v[68:69], v[66:67], 0, v[68:69]
	s_waitcnt lgkmcnt(4)
	v_cvt_pk_bf16_f32 v3, v54, v56
	s_waitcnt lgkmcnt(2)
	v_cvt_pk_bf16_f32 v4, v58, v60
	s_waitcnt lgkmcnt(0)
	v_cvt_pk_bf16_f32 v5, v62, v64
	global_store_dwordx4 v[68:69], v[2:5], off nt
	v_or_b32_e32 v38, s3, v43
	v_lshlrev_b32_e32 v38, 11, v38
	v_cvt_pk_bf16_f32 v2, v41, v39
	v_cvt_pk_bf16_f32 v3, v55, v57
	v_cvt_pk_bf16_f32 v4, v59, v61
	v_cvt_pk_bf16_f32 v5, v63, v65
	v_mov_b32_e32 v39, v7
	ds_read2_b32 v[40:41], v19 offset0:16 offset1:24
	ds_read2_b32 v[54:55], v19 offset0:81 offset1:89
	ds_read2_b32 v[56:57], v19 offset0:146 offset1:154
	ds_read2_b32 v[58:59], v19 offset0:211 offset1:219
	ds_read2_b32 v[60:61], v52 offset0:20 offset1:28
	ds_read2_b32 v[62:63], v52 offset0:85 offset1:93
	ds_read2_b32 v[64:65], v52 offset0:150 offset1:158
	ds_read2_b32 v[68:69], v52 offset0:215 offset1:223
	v_lshl_add_u64 v[38:39], v[66:67], 0, v[38:39]
	global_store_dwordx4 v[38:39], v[2:5], off nt
	v_or_b32_e32 v38, s3, v44
	v_lshlrev_b32_e32 v38, 11, v38
	v_mov_b32_e32 v39, v7
	v_lshl_add_u64 v[38:39], v[66:67], 0, v[38:39]
	s_waitcnt lgkmcnt(6)
	v_cvt_pk_bf16_f32 v2, v40, v54
	s_waitcnt lgkmcnt(4)
	v_cvt_pk_bf16_f32 v3, v56, v58
	s_waitcnt lgkmcnt(2)
	v_cvt_pk_bf16_f32 v4, v60, v62
	s_waitcnt lgkmcnt(0)
	v_cvt_pk_bf16_f32 v5, v64, v68
	global_store_dwordx4 v[38:39], v[2:5], off nt
	v_or_b32_e32 v38, s3, v45
	v_lshlrev_b32_e32 v38, 11, v38
	v_cvt_pk_bf16_f32 v2, v41, v55
	v_cvt_pk_bf16_f32 v3, v57, v59
	v_cvt_pk_bf16_f32 v4, v61, v63
	v_cvt_pk_bf16_f32 v5, v65, v69
	v_mov_b32_e32 v39, v7
	ds_read2_b32 v[40:41], v19 offset0:32 offset1:40
	ds_read2_b32 v[54:55], v19 offset0:97 offset1:105
	ds_read2_b32 v[56:57], v19 offset0:162 offset1:170
	ds_read2_b32 v[58:59], v19 offset0:227 offset1:235
	ds_read2_b32 v[60:61], v52 offset0:36 offset1:44
	ds_read2_b32 v[62:63], v52 offset0:101 offset1:109
	ds_read2_b32 v[64:65], v52 offset0:166 offset1:174
	ds_read2_b32 v[68:69], v52 offset0:231 offset1:239
	v_lshl_add_u64 v[38:39], v[66:67], 0, v[38:39]
	global_store_dwordx4 v[38:39], v[2:5], off nt
	v_or_b32_e32 v38, s3, v46
	v_lshlrev_b32_e32 v38, 11, v38
	v_mov_b32_e32 v39, v7
	v_lshl_add_u64 v[38:39], v[66:67], 0, v[38:39]
	s_waitcnt lgkmcnt(6)
	v_cvt_pk_bf16_f32 v2, v40, v54
	s_waitcnt lgkmcnt(4)
	v_cvt_pk_bf16_f32 v3, v56, v58
	s_waitcnt lgkmcnt(2)
	v_cvt_pk_bf16_f32 v4, v60, v62
	s_waitcnt lgkmcnt(0)
	v_cvt_pk_bf16_f32 v5, v64, v68
	global_store_dwordx4 v[38:39], v[2:5], off nt
	v_or_b32_e32 v38, s3, v47
	v_lshlrev_b32_e32 v38, 11, v38
	v_cvt_pk_bf16_f32 v2, v41, v55
	v_cvt_pk_bf16_f32 v3, v57, v59
	v_cvt_pk_bf16_f32 v4, v61, v63
	v_cvt_pk_bf16_f32 v5, v65, v69
	v_mov_b32_e32 v39, v7
	ds_read2_b32 v[40:41], v19 offset0:48 offset1:56
	ds_read2_b32 v[54:55], v19 offset0:113 offset1:121
	ds_read2_b32 v[56:57], v19 offset0:178 offset1:186
	ds_read2_b32 v[58:59], v19 offset0:243 offset1:251
	ds_read2_b32 v[60:61], v52 offset0:52 offset1:60
	ds_read2_b32 v[62:63], v52 offset0:117 offset1:125
	ds_read2_b32 v[64:65], v52 offset0:182 offset1:190
	ds_read2_b32 v[68:69], v52 offset0:247 offset1:255
	v_lshl_add_u64 v[38:39], v[66:67], 0, v[38:39]
	global_store_dwordx4 v[38:39], v[2:5], off nt
	v_or_b32_e32 v38, s3, v48
	v_lshlrev_b32_e32 v38, 11, v38
	v_mov_b32_e32 v39, v7
	v_lshl_add_u64 v[38:39], v[66:67], 0, v[38:39]
	s_waitcnt lgkmcnt(6)
	v_cvt_pk_bf16_f32 v2, v40, v54
	s_waitcnt lgkmcnt(4)
	v_cvt_pk_bf16_f32 v3, v56, v58
	s_waitcnt lgkmcnt(2)
	v_cvt_pk_bf16_f32 v4, v60, v62
	s_waitcnt lgkmcnt(0)
	v_cvt_pk_bf16_f32 v5, v64, v68
	global_store_dwordx4 v[38:39], v[2:5], off nt
	v_or_b32_e32 v38, s3, v49
	v_lshlrev_b32_e32 v38, 11, v38
	v_mov_b32_e32 v39, v7
	v_lshl_add_u64 v[38:39], v[66:67], 0, v[38:39]
	v_cvt_pk_bf16_f32 v2, v41, v55
	v_cvt_pk_bf16_f32 v3, v57, v59
	v_cvt_pk_bf16_f32 v4, v61, v63
	v_cvt_pk_bf16_f32 v5, v65, v69
	global_store_dwordx4 v[38:39], v[2:5], off nt
	s_waitcnt lgkmcnt(0)

.LBB0_72:
	v_lshl_add_u64 v[38:39], v[2:3], 0, s[38:39]
	v_add_co_u32_e32 v40, vcc, 0x2000, v38
	global_load_dword v100, v[38:39], off nt
	s_nop 0
	v_addc_co_u32_e32 v41, vcc, 0, v39, vcc
	v_add_co_u32_e32 v54, vcc, 0x4000, v38
	global_load_dword v101, v[40:41], off nt
	s_nop 0
	v_addc_co_u32_e32 v55, vcc, 0, v39, vcc
	v_add_co_u32_e32 v40, vcc, 0x6000, v38
	s_add_u32 s38, s38, 0x20000
	s_nop 0
	v_addc_co_u32_e32 v41, vcc, 0, v39, vcc
	v_add_co_u32_e32 v56, vcc, 0x8000, v38
	global_load_dword v102, v[54:55], off nt
	global_load_dword v103, v[40:41], off nt
	v_addc_co_u32_e32 v57, vcc, 0, v39, vcc
	v_add_co_u32_e32 v40, vcc, 0xa000, v38
	s_addc_u32 s39, s39, 0
	s_nop 0
	v_addc_co_u32_e32 v41, vcc, 0, v39, vcc
	v_add_co_u32_e32 v54, vcc, 0xc000, v38
	global_load_dword v104, v[56:57], off nt
	global_load_dword v105, v[40:41], off nt
	v_addc_co_u32_e32 v55, vcc, 0, v39, vcc
	v_add_co_u32_e32 v40, vcc, 0xe000, v38
	s_nop 0
	v_addc_co_u32_e32 v41, vcc, 0, v39, vcc
	v_add_co_u32_e32 v56, vcc, s62, v38
	global_load_dword v106, v[54:55], off nt
	global_load_dword v107, v[40:41], off nt
	v_addc_co_u32_e32 v57, vcc, 0, v39, vcc
	v_add_co_u32_e32 v40, vcc, 0x12000, v38
	s_nop 1
	v_addc_co_u32_e32 v41, vcc, 0, v39, vcc
	v_add_co_u32_e32 v54, vcc, 0x14000, v38
	global_load_dword v108, v[56:57], off nt
	global_load_dword v109, v[40:41], off nt
	v_addc_co_u32_e32 v55, vcc, 0, v39, vcc
	v_add_co_u32_e32 v40, vcc, 0x16000, v38
	s_nop 1
	v_addc_co_u32_e32 v41, vcc, 0, v39, vcc
	v_add_co_u32_e32 v56, vcc, 0x18000, v38
	global_load_dword v110, v[54:55], off nt
	global_load_dword v111, v[40:41], off nt
	v_addc_co_u32_e32 v57, vcc, 0, v39, vcc
	v_add_co_u32_e32 v40, vcc, 0x1a000, v38
	s_nop 1
	v_addc_co_u32_e32 v41, vcc, 0, v39, vcc
	v_add_co_u32_e32 v54, vcc, 0x1c000, v38
	global_load_dword v112, v[56:57], off nt
	s_nop 0
	global_load_dword v113, v[40:41], off nt
	v_addc_co_u32_e32 v55, vcc, 0, v39, vcc
	v_add_co_u32_e32 v38, vcc, s64, v38
	s_nop 1
	v_addc_co_u32_e32 v39, vcc, 0, v39, vcc
	global_load_dword v114, v[54:55], off nt
	s_nop 0
	global_load_dword v115, v[38:39], off nt
	v_lshl_add_u64 v[38:39], v[2:3], 0, s[38:39]
	v_add_co_u32_e32 v40, vcc, 0x2000, v38
	global_load_dword v116, v[38:39], off nt
	s_nop 0
	v_addc_co_u32_e32 v41, vcc, 0, v39, vcc
	v_add_co_u32_e32 v54, vcc, 0x4000, v38
	global_load_dword v117, v[40:41], off nt
	s_nop 0
	v_addc_co_u32_e32 v55, vcc, 0, v39, vcc
	v_add_co_u32_e32 v40, vcc, 0x6000, v38
	s_add_u32 s38, s38, 0x20000
	s_nop 0
	v_addc_co_u32_e32 v41, vcc, 0, v39, vcc
	v_add_co_u32_e32 v56, vcc, 0x8000, v38
	global_load_dword v118, v[54:55], off nt
	global_load_dword v119, v[40:41], off nt
	v_addc_co_u32_e32 v57, vcc, 0, v39, vcc
	v_add_co_u32_e32 v40, vcc, 0xa000, v38
	s_addc_u32 s39, s39, 0
	s_nop 0
	v_addc_co_u32_e32 v41, vcc, 0, v39, vcc
	v_add_co_u32_e32 v54, vcc, 0xc000, v38
	global_load_dword v120, v[56:57], off nt
	global_load_dword v121, v[40:41], off nt
	v_addc_co_u32_e32 v55, vcc, 0, v39, vcc
	v_add_co_u32_e32 v40, vcc, 0xe000, v38
	s_nop 0
	v_addc_co_u32_e32 v41, vcc, 0, v39, vcc
	v_add_co_u32_e32 v56, vcc, s62, v38
	global_load_dword v122, v[54:55], off nt
	global_load_dword v123, v[40:41], off nt
	v_addc_co_u32_e32 v57, vcc, 0, v39, vcc
	v_add_co_u32_e32 v40, vcc, 0x12000, v38
	s_nop 1
	v_addc_co_u32_e32 v41, vcc, 0, v39, vcc
	v_add_co_u32_e32 v54, vcc, 0x14000, v38
	global_load_dword v124, v[56:57], off nt
	global_load_dword v125, v[40:41], off nt
	v_addc_co_u32_e32 v55, vcc, 0, v39, vcc
	v_add_co_u32_e32 v40, vcc, 0x16000, v38
	s_nop 1
	v_addc_co_u32_e32 v41, vcc, 0, v39, vcc
	v_add_co_u32_e32 v56, vcc, 0x18000, v38
	global_load_dword v126, v[54:55], off nt
	global_load_dword v127, v[40:41], off nt
	v_addc_co_u32_e32 v57, vcc, 0, v39, vcc
	v_add_co_u32_e32 v40, vcc, 0x1a000, v38
	s_nop 1
	v_addc_co_u32_e32 v41, vcc, 0, v39, vcc
	v_add_co_u32_e32 v54, vcc, 0x1c000, v38
	global_load_dword v128, v[56:57], off nt
	s_nop 0
	global_load_dword v129, v[40:41], off nt
	v_addc_co_u32_e32 v55, vcc, 0, v39, vcc
	v_add_co_u32_e32 v38, vcc, s64, v38
	s_nop 1
	v_addc_co_u32_e32 v39, vcc, 0, v39, vcc
	global_load_dword v130, v[54:55], off nt
	s_nop 0
	global_load_dword v131, v[38:39], off nt
	v_add_u32_e32 v39, 0x400, v4
	v_add_u32_e32 v54, 0x800, v4
	v_add_u32_e32 v55, 0xc00, v4
	s_waitcnt vmcnt(30)
	ds_write2_b32 v4, v100, v101 offset1:65
	s_waitcnt vmcnt(28)
	ds_write2_b32 v4, v102, v103 offset0:130 offset1:195
	v_add_u32_e32 v4, 0x1040, v4
	s_waitcnt vmcnt(26)
	ds_write2_b32 v39, v104, v105 offset0:4 offset1:69
	s_waitcnt vmcnt(24)
	ds_write2_b32 v39, v106, v107 offset0:134 offset1:199
	s_waitcnt vmcnt(22)
	ds_write2_b32 v54, v108, v109 offset0:8 offset1:73
	s_waitcnt vmcnt(20)
	ds_write2_b32 v54, v110, v111 offset0:138 offset1:203
	s_waitcnt vmcnt(18)
	ds_write2_b32 v55, v112, v113 offset0:12 offset1:77
	s_waitcnt vmcnt(16)
	ds_write2_b32 v55, v114, v115 offset0:142 offset1:207
	v_lshl_add_u64 v[38:39], v[2:3], 0, s[38:39]
	v_add_co_u32_e32 v40, vcc, 0x2000, v38
	global_load_dword v100, v[38:39], off nt
	s_nop 0
	v_addc_co_u32_e32 v41, vcc, 0, v39, vcc
	v_add_co_u32_e32 v54, vcc, 0x4000, v38
	global_load_dword v101, v[40:41], off nt
	s_nop 0
	v_addc_co_u32_e32 v55, vcc, 0, v39, vcc
	v_add_co_u32_e32 v40, vcc, 0x6000, v38
	s_add_u32 s38, s38, 0x20000
	s_nop 0
	v_addc_co_u32_e32 v41, vcc, 0, v39, vcc
	v_add_co_u32_e32 v56, vcc, 0x8000, v38
	global_load_dword v102, v[54:55], off nt
	global_load_dword v103, v[40:41], off nt
	v_addc_co_u32_e32 v57, vcc, 0, v39, vcc
	v_add_co_u32_e32 v40, vcc, 0xa000, v38
	s_addc_u32 s39, s39, 0
	s_nop 0
	v_addc_co_u32_e32 v41, vcc, 0, v39, vcc
	v_add_co_u32_e32 v54, vcc, 0xc000, v38
	global_load_dword v104, v[56:57], off nt
	global_load_dword v105, v[40:41], off nt
	v_addc_co_u32_e32 v55, vcc, 0, v39, vcc
	v_add_co_u32_e32 v40, vcc, 0xe000, v38
	s_nop 0
	v_addc_co_u32_e32 v41, vcc, 0, v39, vcc
	v_add_co_u32_e32 v56, vcc, s62, v38
	global_load_dword v106, v[54:55], off nt
	global_load_dword v107, v[40:41], off nt
	v_addc_co_u32_e32 v57, vcc, 0, v39, vcc
	v_add_co_u32_e32 v40, vcc, 0x12000, v38
	s_nop 1
	v_addc_co_u32_e32 v41, vcc, 0, v39, vcc
	v_add_co_u32_e32 v54, vcc, 0x14000, v38
	global_load_dword v108, v[56:57], off nt
	global_load_dword v109, v[40:41], off nt
	v_addc_co_u32_e32 v55, vcc, 0, v39, vcc
	v_add_co_u32_e32 v40, vcc, 0x16000, v38
	s_nop 1
	v_addc_co_u32_e32 v41, vcc, 0, v39, vcc
	v_add_co_u32_e32 v56, vcc, 0x18000, v38
	global_load_dword v110, v[54:55], off nt
	global_load_dword v111, v[40:41], off nt
	v_addc_co_u32_e32 v57, vcc, 0, v39, vcc
	v_add_co_u32_e32 v40, vcc, 0x1a000, v38
	s_nop 1
	v_addc_co_u32_e32 v41, vcc, 0, v39, vcc
	v_add_co_u32_e32 v54, vcc, 0x1c000, v38
	global_load_dword v112, v[56:57], off nt
	s_nop 0
	global_load_dword v113, v[40:41], off nt
	v_addc_co_u32_e32 v55, vcc, 0, v39, vcc
	v_add_co_u32_e32 v38, vcc, s64, v38
	s_nop 1
	v_addc_co_u32_e32 v39, vcc, 0, v39, vcc
	global_load_dword v114, v[54:55], off nt
	s_nop 0
	global_load_dword v115, v[38:39], off nt
	v_add_u32_e32 v39, 0x400, v4
	v_add_u32_e32 v54, 0x800, v4
	v_add_u32_e32 v55, 0xc00, v4
	s_waitcnt vmcnt(30)
	ds_write2_b32 v4, v116, v117 offset1:65
	s_waitcnt vmcnt(28)
	ds_write2_b32 v4, v118, v119 offset0:130 offset1:195
	v_add_u32_e32 v4, 0x1040, v4
	s_waitcnt vmcnt(26)
	ds_write2_b32 v39, v120, v121 offset0:4 offset1:69
	s_waitcnt vmcnt(24)
	ds_write2_b32 v39, v122, v123 offset0:134 offset1:199
	s_waitcnt vmcnt(22)
	ds_write2_b32 v54, v124, v125 offset0:8 offset1:73
	s_waitcnt vmcnt(20)
	ds_write2_b32 v54, v126, v127 offset0:138 offset1:203
	s_waitcnt vmcnt(18)
	ds_write2_b32 v55, v128, v129 offset0:12 offset1:77
	s_waitcnt vmcnt(16)
	ds_write2_b32 v55, v130, v131 offset0:142 offset1:207
	v_lshl_add_u64 v[38:39], v[2:3], 0, s[38:39]
	v_add_co_u32_e32 v40, vcc, 0x2000, v38
	global_load_dword v116, v[38:39], off nt
	s_nop 0
	v_addc_co_u32_e32 v41, vcc, 0, v39, vcc
	v_add_co_u32_e32 v54, vcc, 0x4000, v38
	global_load_dword v117, v[40:41], off nt
	s_nop 0
	v_addc_co_u32_e32 v55, vcc, 0, v39, vcc
	v_add_co_u32_e32 v40, vcc, 0x6000, v38
	s_add_u32 s38, s38, 0x20000
	s_nop 0
	v_addc_co_u32_e32 v41, vcc, 0, v39, vcc
	v_add_co_u32_e32 v56, vcc, 0x8000, v38
	global_load_dword v118, v[54:55], off nt
	global_load_dword v119, v[40:41], off nt
	v_addc_co_u32_e32 v57, vcc, 0, v39, vcc
	v_add_co_u32_e32 v40, vcc, 0xa000, v38
	s_addc_u32 s39, s39, 0
	s_nop 0
	v_addc_co_u32_e32 v41, vcc, 0, v39, vcc
	v_add_co_u32_e32 v54, vcc, 0xc000, v38
	global_load_dword v120, v[56:57], off nt
	global_load_dword v121, v[40:41], off nt
	v_addc_co_u32_e32 v55, vcc, 0, v39, vcc
	v_add_co_u32_e32 v40, vcc, 0xe000, v38
	s_nop 0
	v_addc_co_u32_e32 v41, vcc, 0, v39, vcc
	v_add_co_u32_e32 v56, vcc, s62, v38
	global_load_dword v122, v[54:55], off nt
	global_load_dword v123, v[40:41], off nt
	v_addc_co_u32_e32 v57, vcc, 0, v39, vcc
	v_add_co_u32_e32 v40, vcc, 0x12000, v38
	s_nop 1
	v_addc_co_u32_e32 v41, vcc, 0, v39, vcc
	v_add_co_u32_e32 v54, vcc, 0x14000, v38
	global_load_dword v124, v[56:57], off nt
	global_load_dword v125, v[40:41], off nt
	v_addc_co_u32_e32 v55, vcc, 0, v39, vcc
	v_add_co_u32_e32 v40, vcc, 0x16000, v38
	s_nop 1
	v_addc_co_u32_e32 v41, vcc, 0, v39, vcc
	v_add_co_u32_e32 v56, vcc, 0x18000, v38
	global_load_dword v126, v[54:55], off nt
	global_load_dword v127, v[40:41], off nt
	v_addc_co_u32_e32 v57, vcc, 0, v39, vcc
	v_add_co_u32_e32 v40, vcc, 0x1a000, v38
	s_nop 1
	v_addc_co_u32_e32 v41, vcc, 0, v39, vcc
	v_add_co_u32_e32 v54, vcc, 0x1c000, v38
	global_load_dword v128, v[56:57], off nt
	s_nop 0
	global_load_dword v129, v[40:41], off nt
	v_addc_co_u32_e32 v55, vcc, 0, v39, vcc
	v_add_co_u32_e32 v38, vcc, s64, v38
	s_nop 1
	v_addc_co_u32_e32 v39, vcc, 0, v39, vcc
	global_load_dword v130, v[54:55], off nt
	s_nop 0
	global_load_dword v131, v[38:39], off nt
	v_add_u32_e32 v39, 0x400, v4
	v_add_u32_e32 v54, 0x800, v4
	v_add_u32_e32 v55, 0xc00, v4
	s_waitcnt vmcnt(30)
	ds_write2_b32 v4, v100, v101 offset1:65
	s_waitcnt vmcnt(28)
	ds_write2_b32 v4, v102, v103 offset0:130 offset1:195
	v_add_u32_e32 v4, 0x1040, v4
	s_waitcnt vmcnt(26)
	ds_write2_b32 v39, v104, v105 offset0:4 offset1:69
	s_waitcnt vmcnt(24)
	ds_write2_b32 v39, v106, v107 offset0:134 offset1:199
	s_waitcnt vmcnt(22)
	ds_write2_b32 v54, v108, v109 offset0:8 offset1:73
	s_waitcnt vmcnt(20)
	ds_write2_b32 v54, v110, v111 offset0:138 offset1:203
	s_waitcnt vmcnt(18)
	ds_write2_b32 v55, v112, v113 offset0:12 offset1:77
	s_waitcnt vmcnt(16)
	ds_write2_b32 v55, v114, v115 offset0:142 offset1:207
	v_add_u32_e32 v39, 0x400, v4
	v_add_u32_e32 v54, 0x800, v4
	v_add_u32_e32 v55, 0xc00, v4
	s_waitcnt vmcnt(14)
	ds_write2_b32 v4, v116, v117 offset1:65
	s_waitcnt vmcnt(12)
	ds_write2_b32 v4, v118, v119 offset0:130 offset1:195
	v_add_u32_e32 v4, 0x1040, v4
	s_waitcnt vmcnt(10)
	ds_write2_b32 v39, v120, v121 offset0:4 offset1:69
	s_waitcnt vmcnt(8)
	ds_write2_b32 v39, v122, v123 offset0:134 offset1:199
	s_waitcnt vmcnt(6)
	ds_write2_b32 v54, v124, v125 offset0:8 offset1:73
	s_waitcnt vmcnt(4)
	ds_write2_b32 v54, v126, v127 offset0:138 offset1:203
	s_waitcnt vmcnt(2)
	ds_write2_b32 v55, v128, v129 offset0:12 offset1:77
	s_waitcnt vmcnt(0)
	ds_write2_b32 v55, v130, v131 offset0:142 offset1:207
	s_ashr_i64 s[6:7], s[6:7], 10
	s_add_u32 s3, s51, s6
	s_addc_u32 s5, s54, s7
	s_lshl_b64 s[6:7], s[36:37], 1
	s_add_u32 s6, s3, s6
	s_addc_u32 s7, s5, s7
	s_and_b32 s3, s4, 0xffffff00
	v_or_b32_e32 v40, s4, v42
	s_waitcnt lgkmcnt(0)
	v_or_b32_e32 v54, s3, v50
	v_lshrrev_b32_e32 v2, 1, v40
	v_and_or_b32 v41, v2, s70, v54
	ds_read2_b32 v[2:3], v19 offset1:65
	ds_read2_b32 v[4:5], v19 offset0:130 offset1:195
	ds_read2_b32 v[56:57], v52 offset0:4 offset1:69
	ds_read2_b32 v[58:59], v52 offset0:134 offset1:199
	v_cmp_gt_i32_e32 vcc, s69, v40
	v_lshl_add_u64 v[38:39], s[6:7], 0, v[6:7]
	s_waitcnt lgkmcnt(3)
	v_cvt_pk_bf16_f32 v2, v2, v3
	s_waitcnt lgkmcnt(2)
	v_cvt_pk_bf16_f32 v3, v4, v5
	s_waitcnt lgkmcnt(1)
	v_cvt_pk_bf16_f32 v4, v56, v57
	s_waitcnt lgkmcnt(0)
	v_cvt_pk_bf16_f32 v5, v58, v59
	v_cndmask_b32_e32 v40, -1, v41, vcc
	v_cmp_lt_i32_e32 vcc, -1, v40
	s_and_saveexec_b64 s[6:7], vcc
	s_cbranch_execz .LBB0_75
	v_mov_b32_e32 v41, v7
	v_lshlrev_b64 v[40:41], 11, v[40:41]
	v_lshl_add_u64 v[40:41], v[38:39], 0, v[40:41]
	global_store_dwordx4 v[40:41], v[2:5], off nt

.LBB0_390:
	s_add_u32 s1, s42, 0x100
	v_lshl_add_u64 v[142:143], s[40:41], 0, v[130:131]
	s_addc_u32 s24, s43, 0
	s_mov_b32 s25, -2
	s_mov_b64 s[42:43], 0
	s_add_u32 s14, s40, s42
	s_addc_u32 s15, s41, s43
	s_add_u32 s34, s14, 0x100
	s_addc_u32 s35, s15, 0
	s_add_u32 s44, s1, s42
	s_addc_u32 s45, s24, s43
	s_cmpk_eq_i32 s42, 0x700
	s_cselect_b64 vcc, -1, 0
	s_and_b64 s[14:15], vcc, exec
	s_cselect_b32 s15, s55, s35
	s_cselect_b32 s14, s54, s34
	s_cselect_b32 s35, s69, s45
	s_cselect_b32 s34, s68, s44
	s_add_i32 s44, 0, 0x11000
	v_add_u32_e32 v145, s44, v1
	s_add_i32 s45, 0, 0x15000
	ds_read_b128 v[146:149], v145
	ds_read_b128 v[150:153], v145 offset:1024
	ds_read_b128 v[154:157], v145 offset:2048
	ds_read_b128 v[158:161], v145 offset:3072
	v_add_u32_e32 v145, s45, v1
	ds_read_b128 v[162:165], v145
	ds_read_b128 v[166:169], v145 offset:1024
	ds_read_b128 v[170:173], v145 offset:2048
	ds_read_b128 v[174:177], v145 offset:3072
	v_cndmask_b32_e32 v193, v131, v141, vcc
	v_cndmask_b32_e32 v192, v130, v140, vcc
	v_lshl_add_u64 v[220:221], v[142:143], 0, s[42:43]
	v_lshl_add_u64 v[222:223], v[220:221], 0, s[6:7]
	s_add_i32 m0, s28, 0xd000
	ds_read_b128 v[178:181], v144 offset:4096
	ds_read_b128 v[182:185], v144 offset:5120
	ds_read_b128 v[196:199], v144 offset:6144
	ds_read_b128 v[200:203], v144 offset:7168
	ds_read_b128 v[204:207], v144 offset:8192
	ds_read_b128 v[208:211], v144 offset:9216
	ds_read_b128 v[212:215], v144 offset:10240
	ds_read_b128 v[216:219], v144 offset:11264
	global_load_lds_dwordx4 v[222:223], off
	v_lshl_add_u64 v[220:221], v[220:221], 0, s[8:9]
	s_add_i32 m0, s28, 0xf000
	s_nop 0
	global_load_lds_dwordx4 v[220:221], off
	s_waitcnt vmcnt(8)
	s_waitcnt lgkmcnt(0)
	s_barrier
	s_setprio 1
	s_waitcnt lgkmcnt(0)
	v_mfma_f32_16x16x32_bf16 v[126:129], v[146:149], v[178:181], 0
	v_mfma_f32_16x16x32_bf16 v[122:125], v[154:157], v[178:181], 0
	v_mfma_f32_16x16x32_bf16 v[110:113], v[146:149], v[196:199], 0
	v_mfma_f32_16x16x32_bf16 v[106:109], v[154:157], v[196:199], 0
	v_mfma_f32_16x16x32_bf16 v[94:97], v[146:149], v[204:207], 0
	v_mfma_f32_16x16x32_bf16 v[90:93], v[154:157], v[204:207], 0
	v_mfma_f32_16x16x32_bf16 v[78:81], v[146:149], v[212:215], 0
	v_mfma_f32_16x16x32_bf16 v[74:77], v[154:157], v[212:215], 0
	v_mfma_f32_16x16x32_bf16 v[126:129], v[150:153], v[182:185], v[126:129]
	v_mfma_f32_16x16x32_bf16 v[122:125], v[158:161], v[182:185], v[122:125]
	v_mfma_f32_16x16x32_bf16 v[110:113], v[150:153], v[200:203], v[110:113]
	v_mfma_f32_16x16x32_bf16 v[106:109], v[158:161], v[200:203], v[106:109]
	v_mfma_f32_16x16x32_bf16 v[94:97], v[150:153], v[208:211], v[94:97]
	v_mfma_f32_16x16x32_bf16 v[90:93], v[158:161], v[208:211], v[90:93]
	v_mfma_f32_16x16x32_bf16 v[78:81], v[150:153], v[216:219], v[78:81]
	v_mfma_f32_16x16x32_bf16 v[74:77], v[158:161], v[216:219], v[74:77]
	s_setprio 0
	s_setprio 1
	v_mfma_f32_16x16x32_bf16 v[118:121], v[162:165], v[178:181], 0
	v_mfma_f32_16x16x32_bf16 v[114:117], v[170:173], v[178:181], 0
	v_mfma_f32_16x16x32_bf16 v[102:105], v[162:165], v[196:199], 0
	v_mfma_f32_16x16x32_bf16 v[98:101], v[170:173], v[196:199], 0
	v_mfma_f32_16x16x32_bf16 v[86:89], v[162:165], v[204:207], 0
	v_mfma_f32_16x16x32_bf16 v[82:85], v[170:173], v[204:207], 0
	v_mfma_f32_16x16x32_bf16 v[70:73], v[162:165], v[212:215], 0
	v_mfma_f32_16x16x32_bf16 v[66:69], v[170:173], v[212:215], 0
	v_mfma_f32_16x16x32_bf16 v[118:121], v[166:169], v[182:185], v[118:121]
	v_mfma_f32_16x16x32_bf16 v[114:117], v[174:177], v[182:185], v[114:117]
	v_mfma_f32_16x16x32_bf16 v[102:105], v[166:169], v[200:203], v[102:105]
	v_mfma_f32_16x16x32_bf16 v[98:101], v[174:177], v[200:203], v[98:101]
	v_mfma_f32_16x16x32_bf16 v[86:89], v[166:169], v[208:211], v[86:89]
	v_mfma_f32_16x16x32_bf16 v[82:85], v[174:177], v[208:211], v[82:85]
	v_mfma_f32_16x16x32_bf16 v[70:73], v[166:169], v[216:219], v[70:73]
	v_mfma_f32_16x16x32_bf16 v[66:69], v[174:177], v[216:219], v[66:69]
	s_setprio 0
	s_barrier
	s_add_i32 s44, s44, s12
	v_lshl_add_u64 v[220:221], s[34:35], 0, v[186:187]
	s_mov_b32 m0, s44
	ds_read_b128 v[178:181], v144 offset:20480
	ds_read_b128 v[182:185], v144 offset:21504
	ds_read_b128 v[196:199], v144 offset:22528
	ds_read_b128 v[200:203], v144 offset:23552
	ds_read_b128 v[204:207], v144 offset:24576
	ds_read_b128 v[208:211], v144 offset:25600
	ds_read_b128 v[212:215], v144 offset:26624
	ds_read_b128 v[216:219], v144 offset:27648
	global_load_lds_dwordx4 v186, s[34:35]
	v_lshl_add_u64 v[222:223], v[220:221], 0, s[82:83]
	s_add_i32 m0, s44, 0x2000
	s_add_i32 s34, s45, s12
	global_load_lds_dwordx4 v[222:223], off
	v_lshl_add_u64 v[222:223], v[220:221], 0, s[64:65]
	s_mov_b32 m0, s34
	v_lshl_add_u64 v[192:193], s[14:15], 0, v[192:193]
	global_load_lds_dwordx4 v[222:223], off
	v_lshl_add_u64 v[222:223], v[220:221], 0, s[86:87]
	s_add_i32 m0, s34, 0x2000
	s_nop 0
	global_load_lds_dwordx4 v[222:223], off
	s_mov_b32 m0, s29
	v_lshl_add_u64 v[222:223], v[192:193], 0, s[82:83]
	global_load_lds_dwordx4 v[192:193], off
	s_mov_b32 m0, s47
	s_nop 0
	global_load_lds_dwordx4 v[222:223], off
	s_waitcnt vmcnt(8)
	s_waitcnt lgkmcnt(0)
	s_barrier
	s_setprio 1
	s_waitcnt lgkmcnt(0)
	v_mfma_f32_16x16x32_bf16 v[62:65], v[146:149], v[178:181], 0
	v_mfma_f32_16x16x32_bf16 v[58:61], v[154:157], v[178:181], 0
	v_mfma_f32_16x16x32_bf16 v[46:49], v[146:149], v[196:199], 0
	v_mfma_f32_16x16x32_bf16 v[42:45], v[154:157], v[196:199], 0
	v_mfma_f32_16x16x32_bf16 v[30:33], v[146:149], v[204:207], 0
	v_mfma_f32_16x16x32_bf16 v[26:29], v[154:157], v[204:207], 0
	v_mfma_f32_16x16x32_bf16 v[14:17], v[146:149], v[212:215], 0
	v_mfma_f32_16x16x32_bf16 v[10:13], v[154:157], v[212:215], 0
	v_mfma_f32_16x16x32_bf16 v[62:65], v[150:153], v[182:185], v[62:65]
	v_mfma_f32_16x16x32_bf16 v[58:61], v[158:161], v[182:185], v[58:61]
	v_mfma_f32_16x16x32_bf16 v[46:49], v[150:153], v[200:203], v[46:49]
	v_mfma_f32_16x16x32_bf16 v[42:45], v[158:161], v[200:203], v[42:45]
	v_mfma_f32_16x16x32_bf16 v[30:33], v[150:153], v[208:211], v[30:33]
	v_mfma_f32_16x16x32_bf16 v[26:29], v[158:161], v[208:211], v[26:29]
	v_mfma_f32_16x16x32_bf16 v[14:17], v[150:153], v[216:219], v[14:17]
	v_mfma_f32_16x16x32_bf16 v[10:13], v[158:161], v[216:219], v[10:13]
	s_setprio 0
	s_setprio 1
	v_mfma_f32_16x16x32_bf16 v[54:57], v[162:165], v[178:181], 0
	v_mfma_f32_16x16x32_bf16 v[50:53], v[170:173], v[178:181], 0
	v_mfma_f32_16x16x32_bf16 v[38:41], v[162:165], v[196:199], 0
	v_mfma_f32_16x16x32_bf16 v[34:37], v[170:173], v[196:199], 0
	v_mfma_f32_16x16x32_bf16 v[22:25], v[162:165], v[204:207], 0
	v_mfma_f32_16x16x32_bf16 v[18:21], v[170:173], v[204:207], 0
	v_mfma_f32_16x16x32_bf16 v[6:9], v[162:165], v[212:215], 0
	v_mfma_f32_16x16x32_bf16 v[2:5], v[170:173], v[212:215], 0
	v_mfma_f32_16x16x32_bf16 v[54:57], v[166:169], v[182:185], v[54:57]
	v_mfma_f32_16x16x32_bf16 v[50:53], v[174:177], v[182:185], v[50:53]
	v_mfma_f32_16x16x32_bf16 v[38:41], v[166:169], v[200:203], v[38:41]
	v_mfma_f32_16x16x32_bf16 v[34:37], v[174:177], v[200:203], v[34:37]
	v_mfma_f32_16x16x32_bf16 v[22:25], v[166:169], v[208:211], v[22:25]
	v_mfma_f32_16x16x32_bf16 v[18:21], v[174:177], v[208:211], v[18:21]
	v_mfma_f32_16x16x32_bf16 v[6:9], v[166:169], v[216:219], v[6:9]
	v_mfma_f32_16x16x32_bf16 v[2:5], v[174:177], v[216:219], v[2:5]
	s_setprio 0
	s_barrier
	s_add_i32 s14, 0, 0x19000
	v_add_u32_e32 v145, s14, v1
	s_add_i32 s15, 0, 0x1d000
	ds_read_b128 v[146:149], v145
	ds_read_b128 v[150:153], v145 offset:1024
	ds_read_b128 v[154:157], v145 offset:2048
	ds_read_b128 v[158:161], v145 offset:3072
	v_add_u32_e32 v145, s15, v1
	ds_read_b128 v[162:165], v145
	ds_read_b128 v[166:169], v145 offset:1024
	ds_read_b128 v[170:173], v145 offset:2048
	ds_read_b128 v[174:177], v145 offset:3072
	s_mov_b32 m0, s60
	v_lshl_add_u64 v[222:223], v[192:193], 0, s[64:65]
	ds_read_b128 v[178:181], v144 offset:36864
	ds_read_b128 v[182:185], v144 offset:37888
	ds_read_b128 v[196:199], v144 offset:38912
	ds_read_b128 v[200:203], v144 offset:39936
	ds_read_b128 v[204:207], v144 offset:40960
	ds_read_b128 v[208:211], v144 offset:41984
	ds_read_b128 v[212:215], v144 offset:43008
	ds_read_b128 v[216:219], v144 offset:44032
	global_load_lds_dwordx4 v[222:223], off
	v_lshl_add_u64 v[222:223], v[192:193], 0, s[86:87]
	s_mov_b32 m0, s61
	s_nop 0
	global_load_lds_dwordx4 v[222:223], off
	s_waitcnt vmcnt(8)
	s_waitcnt lgkmcnt(0)
	s_barrier
	s_setprio 1
	s_waitcnt lgkmcnt(0)
	v_mfma_f32_16x16x32_bf16 v[126:129], v[146:149], v[178:181], v[126:129]
	v_mfma_f32_16x16x32_bf16 v[122:125], v[154:157], v[178:181], v[122:125]
	v_mfma_f32_16x16x32_bf16 v[110:113], v[146:149], v[196:199], v[110:113]
	v_mfma_f32_16x16x32_bf16 v[106:109], v[154:157], v[196:199], v[106:109]
	v_mfma_f32_16x16x32_bf16 v[94:97], v[146:149], v[204:207], v[94:97]
	v_mfma_f32_16x16x32_bf16 v[90:93], v[154:157], v[204:207], v[90:93]
	v_mfma_f32_16x16x32_bf16 v[78:81], v[146:149], v[212:215], v[78:81]
	v_mfma_f32_16x16x32_bf16 v[74:77], v[154:157], v[212:215], v[74:77]
	v_mfma_f32_16x16x32_bf16 v[126:129], v[150:153], v[182:185], v[126:129]
	v_mfma_f32_16x16x32_bf16 v[122:125], v[158:161], v[182:185], v[122:125]
	v_mfma_f32_16x16x32_bf16 v[110:113], v[150:153], v[200:203], v[110:113]
	v_mfma_f32_16x16x32_bf16 v[106:109], v[158:161], v[200:203], v[106:109]
	v_mfma_f32_16x16x32_bf16 v[94:97], v[150:153], v[208:211], v[94:97]
	v_mfma_f32_16x16x32_bf16 v[90:93], v[158:161], v[208:211], v[90:93]
	v_mfma_f32_16x16x32_bf16 v[78:81], v[150:153], v[216:219], v[78:81]
	v_mfma_f32_16x16x32_bf16 v[74:77], v[158:161], v[216:219], v[74:77]
	s_setprio 0
	s_setprio 1
	v_mfma_f32_16x16x32_bf16 v[118:121], v[162:165], v[178:181], v[118:121]
	v_mfma_f32_16x16x32_bf16 v[114:117], v[170:173], v[178:181], v[114:117]
	v_mfma_f32_16x16x32_bf16 v[102:105], v[162:165], v[196:199], v[102:105]
	v_mfma_f32_16x16x32_bf16 v[98:101], v[170:173], v[196:199], v[98:101]
	v_mfma_f32_16x16x32_bf16 v[86:89], v[162:165], v[204:207], v[86:89]
	v_mfma_f32_16x16x32_bf16 v[82:85], v[170:173], v[204:207], v[82:85]
	v_mfma_f32_16x16x32_bf16 v[70:73], v[162:165], v[212:215], v[70:73]
	v_mfma_f32_16x16x32_bf16 v[66:69], v[170:173], v[212:215], v[66:69]
	v_mfma_f32_16x16x32_bf16 v[118:121], v[166:169], v[182:185], v[118:121]
	v_mfma_f32_16x16x32_bf16 v[114:117], v[174:177], v[182:185], v[114:117]
	v_mfma_f32_16x16x32_bf16 v[102:105], v[166:169], v[200:203], v[102:105]
	v_mfma_f32_16x16x32_bf16 v[98:101], v[174:177], v[200:203], v[98:101]
	v_mfma_f32_16x16x32_bf16 v[86:89], v[166:169], v[208:211], v[86:89]
	v_mfma_f32_16x16x32_bf16 v[82:85], v[174:177], v[208:211], v[82:85]
	v_mfma_f32_16x16x32_bf16 v[70:73], v[166:169], v[216:219], v[70:73]
	v_mfma_f32_16x16x32_bf16 v[66:69], v[174:177], v[216:219], v[66:69]
	s_setprio 0
	s_barrier
	s_add_i32 s14, s14, s12
	v_lshl_add_u64 v[222:223], v[220:221], 0, s[92:93]
	s_mov_b32 m0, s14
	ds_read_b128 v[178:181], v144 offset:53248
	ds_read_b128 v[182:185], v144 offset:54272
	ds_read_b128 v[196:199], v144 offset:55296
	ds_read_b128 v[200:203], v144 offset:56320
	ds_read_b128 v[204:207], v144 offset:57344
	ds_read_b128 v[208:211], v144 offset:58368
	ds_read_b128 v[212:215], v144 offset:59392
	ds_read_b128 v[216:219], v144 offset:60416
	global_load_lds_dwordx4 v[222:223], off
	v_lshl_add_u64 v[222:223], v[220:221], 0, s[4:5]
	s_add_i32 m0, s14, 0x2000
	s_add_i32 s14, s15, s12
	global_load_lds_dwordx4 v[222:223], off
	v_lshl_add_u64 v[222:223], v[220:221], 0, s[6:7]
	s_mov_b32 m0, s14
	v_lshl_add_u64 v[220:221], v[220:221], 0, s[8:9]
	global_load_lds_dwordx4 v[222:223], off
	s_add_i32 m0, s14, 0x2000
	s_nop 0
	global_load_lds_dwordx4 v[220:221], off
	v_lshl_add_u64 v[220:221], v[192:193], 0, s[92:93]
	s_mov_b32 m0, s76
	v_lshl_add_u64 v[192:193], v[192:193], 0, s[4:5]
	global_load_lds_dwordx4 v[220:221], off
	s_mov_b32 m0, s77
	s_nop 0
	global_load_lds_dwordx4 v[192:193], off
	s_waitcnt vmcnt(8)
	s_waitcnt lgkmcnt(0)
	s_barrier
	s_setprio 1
	s_waitcnt lgkmcnt(0)
	v_mfma_f32_16x16x32_bf16 v[62:65], v[146:149], v[178:181], v[62:65]
	v_mfma_f32_16x16x32_bf16 v[58:61], v[154:157], v[178:181], v[58:61]
	v_mfma_f32_16x16x32_bf16 v[46:49], v[146:149], v[196:199], v[46:49]
	v_mfma_f32_16x16x32_bf16 v[42:45], v[154:157], v[196:199], v[42:45]
	v_mfma_f32_16x16x32_bf16 v[30:33], v[146:149], v[204:207], v[30:33]
	v_mfma_f32_16x16x32_bf16 v[26:29], v[154:157], v[204:207], v[26:29]
	v_mfma_f32_16x16x32_bf16 v[14:17], v[146:149], v[212:215], v[14:17]
	v_mfma_f32_16x16x32_bf16 v[10:13], v[154:157], v[212:215], v[10:13]
	v_mfma_f32_16x16x32_bf16 v[62:65], v[150:153], v[182:185], v[62:65]
	v_mfma_f32_16x16x32_bf16 v[58:61], v[158:161], v[182:185], v[58:61]
	v_mfma_f32_16x16x32_bf16 v[46:49], v[150:153], v[200:203], v[46:49]
	v_mfma_f32_16x16x32_bf16 v[42:45], v[158:161], v[200:203], v[42:45]
	v_mfma_f32_16x16x32_bf16 v[30:33], v[150:153], v[208:211], v[30:33]
	v_mfma_f32_16x16x32_bf16 v[26:29], v[158:161], v[208:211], v[26:29]
	v_mfma_f32_16x16x32_bf16 v[14:17], v[150:153], v[216:219], v[14:17]
	v_mfma_f32_16x16x32_bf16 v[10:13], v[158:161], v[216:219], v[10:13]
	s_setprio 0
	s_setprio 1
	v_mfma_f32_16x16x32_bf16 v[54:57], v[162:165], v[178:181], v[54:57]
	v_mfma_f32_16x16x32_bf16 v[50:53], v[170:173], v[178:181], v[50:53]
	v_mfma_f32_16x16x32_bf16 v[38:41], v[162:165], v[196:199], v[38:41]
	v_mfma_f32_16x16x32_bf16 v[34:37], v[170:173], v[196:199], v[34:37]
	v_mfma_f32_16x16x32_bf16 v[22:25], v[162:165], v[204:207], v[22:25]
	v_mfma_f32_16x16x32_bf16 v[18:21], v[170:173], v[204:207], v[18:21]
	v_mfma_f32_16x16x32_bf16 v[6:9], v[162:165], v[212:215], v[6:9]
	v_mfma_f32_16x16x32_bf16 v[2:5], v[170:173], v[212:215], v[2:5]
	v_mfma_f32_16x16x32_bf16 v[54:57], v[166:169], v[182:185], v[54:57]
	v_mfma_f32_16x16x32_bf16 v[50:53], v[174:177], v[182:185], v[50:53]
	v_mfma_f32_16x16x32_bf16 v[38:41], v[166:169], v[200:203], v[38:41]
	v_mfma_f32_16x16x32_bf16 v[34:37], v[174:177], v[200:203], v[34:37]
	v_mfma_f32_16x16x32_bf16 v[22:25], v[166:169], v[208:211], v[22:25]
	v_mfma_f32_16x16x32_bf16 v[18:21], v[174:177], v[208:211], v[18:21]
	v_mfma_f32_16x16x32_bf16 v[6:9], v[166:169], v[216:219], v[6:9]
	v_mfma_f32_16x16x32_bf16 v[2:5], v[174:177], v[216:219], v[2:5]
	s_setprio 0
	s_barrier
	s_add_i32 s25, s25, 2
	s_add_u32 s42, s42, 0x100
	s_addc_u32 s43, s43, 0

.LBB0_1110:
	s_add_u32 s24, s54, 0x100
	v_lshl_add_u64 v[140:141], s[52:53], 0, v[138:139]
	s_addc_u32 s25, s55, 0
	s_mov_b32 s43, -2
	s_mov_b64 s[54:55], 0
	s_add_u32 s14, s52, s54
	s_addc_u32 s15, s53, s55
	s_add_u32 s45, s14, 0x100
	s_addc_u32 s73, s15, 0
	s_add_u32 s74, s24, s54
	s_addc_u32 s75, s25, s55
	s_cmpk_eq_i32 s54, 0x700
	s_cselect_b64 vcc, -1, 0
	s_and_b64 s[14:15], vcc, exec
	s_cselect_b32 s15, s47, s73
	s_cselect_b32 s14, s46, s45
	s_cselect_b32 s75, s49, s75
	s_cselect_b32 s74, s48, s74
	s_add_i32 s45, 0, 0x11000
	v_add_u32_e32 v131, s45, v1
	s_add_i32 s73, 0, 0x15000
	ds_read_b128 v[144:147], v131
	ds_read_b128 v[148:151], v131 offset:1024
	ds_read_b128 v[152:155], v131 offset:2048
	ds_read_b128 v[156:159], v131 offset:3072
	v_add_u32_e32 v131, s73, v1
	ds_read_b128 v[160:163], v131
	ds_read_b128 v[164:167], v131 offset:1024
	ds_read_b128 v[168:171], v131 offset:2048
	ds_read_b128 v[172:175], v131 offset:3072
	v_cndmask_b32_e32 v185, v139, v137, vcc
	v_cndmask_b32_e32 v184, v138, v136, vcc
	v_lshl_add_u64 v[192:193], v[140:141], 0, s[54:55]
	v_lshl_add_u64 v[220:221], v[192:193], 0, s[6:7]
	s_add_i32 m0, s29, 0xd000
	ds_read_b128 v[176:179], v142 offset:4096
	ds_read_b128 v[180:183], v142 offset:5120
	ds_read_b128 v[196:199], v142 offset:6144
	ds_read_b128 v[200:203], v142 offset:7168
	ds_read_b128 v[204:207], v142 offset:8192
	ds_read_b128 v[208:211], v142 offset:9216
	ds_read_b128 v[212:215], v142 offset:10240
	ds_read_b128 v[216:219], v142 offset:11264
	global_load_lds_dwordx4 v[220:221], off
	v_lshl_add_u64 v[192:193], v[192:193], 0, s[8:9]
	s_add_i32 m0, s29, 0xf000
	s_nop 0
	global_load_lds_dwordx4 v[192:193], off
	s_waitcnt vmcnt(8)
	s_waitcnt lgkmcnt(0)
	s_barrier
	s_setprio 1
	s_waitcnt lgkmcnt(0)
	v_mfma_f32_16x16x32_bf16 v[126:129], v[144:147], v[176:179], 0
	v_mfma_f32_16x16x32_bf16 v[122:125], v[152:155], v[176:179], 0
	v_mfma_f32_16x16x32_bf16 v[110:113], v[144:147], v[196:199], 0
	v_mfma_f32_16x16x32_bf16 v[106:109], v[152:155], v[196:199], 0
	v_mfma_f32_16x16x32_bf16 v[94:97], v[144:147], v[204:207], 0
	v_mfma_f32_16x16x32_bf16 v[90:93], v[152:155], v[204:207], 0
	v_mfma_f32_16x16x32_bf16 v[78:81], v[144:147], v[212:215], 0
	v_mfma_f32_16x16x32_bf16 v[74:77], v[152:155], v[212:215], 0
	v_mfma_f32_16x16x32_bf16 v[126:129], v[148:151], v[180:183], v[126:129]
	v_mfma_f32_16x16x32_bf16 v[122:125], v[156:159], v[180:183], v[122:125]
	v_mfma_f32_16x16x32_bf16 v[110:113], v[148:151], v[200:203], v[110:113]
	v_mfma_f32_16x16x32_bf16 v[106:109], v[156:159], v[200:203], v[106:109]
	v_mfma_f32_16x16x32_bf16 v[94:97], v[148:151], v[208:211], v[94:97]
	v_mfma_f32_16x16x32_bf16 v[90:93], v[156:159], v[208:211], v[90:93]
	v_mfma_f32_16x16x32_bf16 v[78:81], v[148:151], v[216:219], v[78:81]
	v_mfma_f32_16x16x32_bf16 v[74:77], v[156:159], v[216:219], v[74:77]
	s_setprio 0
	s_setprio 1
	v_mfma_f32_16x16x32_bf16 v[118:121], v[160:163], v[176:179], 0
	v_mfma_f32_16x16x32_bf16 v[114:117], v[168:171], v[176:179], 0
	v_mfma_f32_16x16x32_bf16 v[102:105], v[160:163], v[196:199], 0
	v_mfma_f32_16x16x32_bf16 v[98:101], v[168:171], v[196:199], 0
	v_mfma_f32_16x16x32_bf16 v[86:89], v[160:163], v[204:207], 0
	v_mfma_f32_16x16x32_bf16 v[82:85], v[168:171], v[204:207], 0
	v_mfma_f32_16x16x32_bf16 v[70:73], v[160:163], v[212:215], 0
	v_mfma_f32_16x16x32_bf16 v[66:69], v[168:171], v[212:215], 0
	v_mfma_f32_16x16x32_bf16 v[118:121], v[164:167], v[180:183], v[118:121]
	v_mfma_f32_16x16x32_bf16 v[114:117], v[172:175], v[180:183], v[114:117]
	v_mfma_f32_16x16x32_bf16 v[102:105], v[164:167], v[200:203], v[102:105]
	v_mfma_f32_16x16x32_bf16 v[98:101], v[172:175], v[200:203], v[98:101]
	v_mfma_f32_16x16x32_bf16 v[86:89], v[164:167], v[208:211], v[86:89]
	v_mfma_f32_16x16x32_bf16 v[82:85], v[172:175], v[208:211], v[82:85]
	v_mfma_f32_16x16x32_bf16 v[70:73], v[164:167], v[216:219], v[70:73]
	v_mfma_f32_16x16x32_bf16 v[66:69], v[172:175], v[216:219], v[66:69]
	s_setprio 0
	s_barrier
	s_add_i32 s45, s45, s2
	v_lshl_add_u64 v[192:193], s[74:75], 0, v[186:187]
	s_mov_b32 m0, s45
	ds_read_b128 v[176:179], v142 offset:20480
	ds_read_b128 v[180:183], v142 offset:21504
	ds_read_b128 v[196:199], v142 offset:22528
	ds_read_b128 v[200:203], v142 offset:23552
	ds_read_b128 v[204:207], v142 offset:24576
	ds_read_b128 v[208:211], v142 offset:25600
	ds_read_b128 v[212:215], v142 offset:26624
	ds_read_b128 v[216:219], v142 offset:27648
	global_load_lds_dwordx4 v186, s[74:75]
	v_lshl_add_u64 v[220:221], v[192:193], 0, s[82:83]
	s_add_i32 m0, s45, 0x2000
	s_add_i32 s45, s73, s2
	global_load_lds_dwordx4 v[220:221], off
	v_lshl_add_u64 v[220:221], v[192:193], 0, s[64:65]
	s_mov_b32 m0, s45
	v_lshl_add_u64 v[184:185], s[14:15], 0, v[184:185]
	global_load_lds_dwordx4 v[220:221], off
	v_lshl_add_u64 v[220:221], v[192:193], 0, s[86:87]
	s_add_i32 m0, s45, 0x2000
	s_nop 0
	global_load_lds_dwordx4 v[220:221], off
	s_mov_b32 m0, s33
	v_lshl_add_u64 v[220:221], v[184:185], 0, s[82:83]
	global_load_lds_dwordx4 v[184:185], off
	s_mov_b32 m0, s34
	s_nop 0
	global_load_lds_dwordx4 v[220:221], off
	s_waitcnt vmcnt(8)
	s_waitcnt lgkmcnt(0)
	s_barrier
	s_setprio 1
	s_waitcnt lgkmcnt(0)
	v_mfma_f32_16x16x32_bf16 v[62:65], v[144:147], v[176:179], 0
	v_mfma_f32_16x16x32_bf16 v[58:61], v[152:155], v[176:179], 0
	v_mfma_f32_16x16x32_bf16 v[46:49], v[144:147], v[196:199], 0
	v_mfma_f32_16x16x32_bf16 v[42:45], v[152:155], v[196:199], 0
	v_mfma_f32_16x16x32_bf16 v[30:33], v[144:147], v[204:207], 0
	v_mfma_f32_16x16x32_bf16 v[26:29], v[152:155], v[204:207], 0
	v_mfma_f32_16x16x32_bf16 v[14:17], v[144:147], v[212:215], 0
	v_mfma_f32_16x16x32_bf16 v[10:13], v[152:155], v[212:215], 0
	v_mfma_f32_16x16x32_bf16 v[62:65], v[148:151], v[180:183], v[62:65]
	v_mfma_f32_16x16x32_bf16 v[58:61], v[156:159], v[180:183], v[58:61]
	v_mfma_f32_16x16x32_bf16 v[46:49], v[148:151], v[200:203], v[46:49]
	v_mfma_f32_16x16x32_bf16 v[42:45], v[156:159], v[200:203], v[42:45]
	v_mfma_f32_16x16x32_bf16 v[30:33], v[148:151], v[208:211], v[30:33]
	v_mfma_f32_16x16x32_bf16 v[26:29], v[156:159], v[208:211], v[26:29]
	v_mfma_f32_16x16x32_bf16 v[14:17], v[148:151], v[216:219], v[14:17]
	v_mfma_f32_16x16x32_bf16 v[10:13], v[156:159], v[216:219], v[10:13]
	s_setprio 0
	s_setprio 1
	v_mfma_f32_16x16x32_bf16 v[54:57], v[160:163], v[176:179], 0
	v_mfma_f32_16x16x32_bf16 v[50:53], v[168:171], v[176:179], 0
	v_mfma_f32_16x16x32_bf16 v[38:41], v[160:163], v[196:199], 0
	v_mfma_f32_16x16x32_bf16 v[34:37], v[168:171], v[196:199], 0
	v_mfma_f32_16x16x32_bf16 v[22:25], v[160:163], v[204:207], 0
	v_mfma_f32_16x16x32_bf16 v[18:21], v[168:171], v[204:207], 0
	v_mfma_f32_16x16x32_bf16 v[6:9], v[160:163], v[212:215], 0
	v_mfma_f32_16x16x32_bf16 v[2:5], v[168:171], v[212:215], 0
	v_mfma_f32_16x16x32_bf16 v[54:57], v[164:167], v[180:183], v[54:57]
	v_mfma_f32_16x16x32_bf16 v[50:53], v[172:175], v[180:183], v[50:53]
	v_mfma_f32_16x16x32_bf16 v[38:41], v[164:167], v[200:203], v[38:41]
	v_mfma_f32_16x16x32_bf16 v[34:37], v[172:175], v[200:203], v[34:37]
	v_mfma_f32_16x16x32_bf16 v[22:25], v[164:167], v[208:211], v[22:25]
	v_mfma_f32_16x16x32_bf16 v[18:21], v[172:175], v[208:211], v[18:21]
	v_mfma_f32_16x16x32_bf16 v[6:9], v[164:167], v[216:219], v[6:9]
	v_mfma_f32_16x16x32_bf16 v[2:5], v[172:175], v[216:219], v[2:5]
	s_setprio 0
	s_barrier
	s_add_i32 s14, 0, 0x19000
	v_add_u32_e32 v131, s14, v1
	s_add_i32 s15, 0, 0x1d000
	ds_read_b128 v[144:147], v131
	ds_read_b128 v[148:151], v131 offset:1024
	ds_read_b128 v[152:155], v131 offset:2048
	ds_read_b128 v[156:159], v131 offset:3072
	v_add_u32_e32 v131, s15, v1
	ds_read_b128 v[160:163], v131
	ds_read_b128 v[164:167], v131 offset:1024
	ds_read_b128 v[168:171], v131 offset:2048
	ds_read_b128 v[172:175], v131 offset:3072
	s_mov_b32 m0, s35
	v_lshl_add_u64 v[220:221], v[184:185], 0, s[64:65]
	ds_read_b128 v[176:179], v142 offset:36864
	ds_read_b128 v[180:183], v142 offset:37888
	ds_read_b128 v[196:199], v142 offset:38912
	ds_read_b128 v[200:203], v142 offset:39936
	ds_read_b128 v[204:207], v142 offset:40960
	ds_read_b128 v[208:211], v142 offset:41984
	ds_read_b128 v[212:215], v142 offset:43008
	ds_read_b128 v[216:219], v142 offset:44032
	global_load_lds_dwordx4 v[220:221], off
	v_lshl_add_u64 v[220:221], v[184:185], 0, s[86:87]
	s_mov_b32 m0, s56
	s_nop 0
	global_load_lds_dwordx4 v[220:221], off
	s_waitcnt vmcnt(8)
	s_waitcnt lgkmcnt(0)
	s_barrier
	s_setprio 1
	s_waitcnt lgkmcnt(0)
	v_mfma_f32_16x16x32_bf16 v[126:129], v[144:147], v[176:179], v[126:129]
	v_mfma_f32_16x16x32_bf16 v[122:125], v[152:155], v[176:179], v[122:125]
	v_mfma_f32_16x16x32_bf16 v[110:113], v[144:147], v[196:199], v[110:113]
	v_mfma_f32_16x16x32_bf16 v[106:109], v[152:155], v[196:199], v[106:109]
	v_mfma_f32_16x16x32_bf16 v[94:97], v[144:147], v[204:207], v[94:97]
	v_mfma_f32_16x16x32_bf16 v[90:93], v[152:155], v[204:207], v[90:93]
	v_mfma_f32_16x16x32_bf16 v[78:81], v[144:147], v[212:215], v[78:81]
	v_mfma_f32_16x16x32_bf16 v[74:77], v[152:155], v[212:215], v[74:77]
	v_mfma_f32_16x16x32_bf16 v[126:129], v[148:151], v[180:183], v[126:129]
	v_mfma_f32_16x16x32_bf16 v[122:125], v[156:159], v[180:183], v[122:125]
	v_mfma_f32_16x16x32_bf16 v[110:113], v[148:151], v[200:203], v[110:113]
	v_mfma_f32_16x16x32_bf16 v[106:109], v[156:159], v[200:203], v[106:109]
	v_mfma_f32_16x16x32_bf16 v[94:97], v[148:151], v[208:211], v[94:97]
	v_mfma_f32_16x16x32_bf16 v[90:93], v[156:159], v[208:211], v[90:93]
	v_mfma_f32_16x16x32_bf16 v[78:81], v[148:151], v[216:219], v[78:81]
	v_mfma_f32_16x16x32_bf16 v[74:77], v[156:159], v[216:219], v[74:77]
	s_setprio 0
	s_setprio 1
	v_mfma_f32_16x16x32_bf16 v[118:121], v[160:163], v[176:179], v[118:121]
	v_mfma_f32_16x16x32_bf16 v[114:117], v[168:171], v[176:179], v[114:117]
	v_mfma_f32_16x16x32_bf16 v[102:105], v[160:163], v[196:199], v[102:105]
	v_mfma_f32_16x16x32_bf16 v[98:101], v[168:171], v[196:199], v[98:101]
	v_mfma_f32_16x16x32_bf16 v[86:89], v[160:163], v[204:207], v[86:89]
	v_mfma_f32_16x16x32_bf16 v[82:85], v[168:171], v[204:207], v[82:85]
	v_mfma_f32_16x16x32_bf16 v[70:73], v[160:163], v[212:215], v[70:73]
	v_mfma_f32_16x16x32_bf16 v[66:69], v[168:171], v[212:215], v[66:69]
	v_mfma_f32_16x16x32_bf16 v[118:121], v[164:167], v[180:183], v[118:121]
	v_mfma_f32_16x16x32_bf16 v[114:117], v[172:175], v[180:183], v[114:117]
	v_mfma_f32_16x16x32_bf16 v[102:105], v[164:167], v[200:203], v[102:105]
	v_mfma_f32_16x16x32_bf16 v[98:101], v[172:175], v[200:203], v[98:101]
	v_mfma_f32_16x16x32_bf16 v[86:89], v[164:167], v[208:211], v[86:89]
	v_mfma_f32_16x16x32_bf16 v[82:85], v[172:175], v[208:211], v[82:85]
	v_mfma_f32_16x16x32_bf16 v[70:73], v[164:167], v[216:219], v[70:73]
	v_mfma_f32_16x16x32_bf16 v[66:69], v[172:175], v[216:219], v[66:69]
	s_setprio 0
	s_barrier
	s_add_i32 s14, s14, s2
	v_lshl_add_u64 v[220:221], v[192:193], 0, s[92:93]
	s_mov_b32 m0, s14
	ds_read_b128 v[176:179], v142 offset:53248
	ds_read_b128 v[180:183], v142 offset:54272
	ds_read_b128 v[196:199], v142 offset:55296
	ds_read_b128 v[200:203], v142 offset:56320
	ds_read_b128 v[204:207], v142 offset:57344
	ds_read_b128 v[208:211], v142 offset:58368
	ds_read_b128 v[212:215], v142 offset:59392
	ds_read_b128 v[216:219], v142 offset:60416
	global_load_lds_dwordx4 v[220:221], off
	v_lshl_add_u64 v[220:221], v[192:193], 0, s[4:5]
	s_add_i32 m0, s14, 0x2000
	s_add_i32 s14, s15, s2
	global_load_lds_dwordx4 v[220:221], off
	v_lshl_add_u64 v[220:221], v[192:193], 0, s[6:7]
	s_mov_b32 m0, s14
	v_lshl_add_u64 v[192:193], v[192:193], 0, s[8:9]
	global_load_lds_dwordx4 v[220:221], off
	s_add_i32 m0, s14, 0x2000
	s_nop 0
	global_load_lds_dwordx4 v[192:193], off
	v_lshl_add_u64 v[192:193], v[184:185], 0, s[92:93]
	s_mov_b32 m0, s59
	v_lshl_add_u64 v[184:185], v[184:185], 0, s[4:5]
	global_load_lds_dwordx4 v[192:193], off
	s_mov_b32 m0, s60
	s_nop 0
	global_load_lds_dwordx4 v[184:185], off
	s_waitcnt vmcnt(8)
	s_waitcnt lgkmcnt(0)
	s_barrier
	s_setprio 1
	s_waitcnt lgkmcnt(0)
	v_mfma_f32_16x16x32_bf16 v[62:65], v[144:147], v[176:179], v[62:65]
	v_mfma_f32_16x16x32_bf16 v[58:61], v[152:155], v[176:179], v[58:61]
	v_mfma_f32_16x16x32_bf16 v[46:49], v[144:147], v[196:199], v[46:49]
	v_mfma_f32_16x16x32_bf16 v[42:45], v[152:155], v[196:199], v[42:45]
	v_mfma_f32_16x16x32_bf16 v[30:33], v[144:147], v[204:207], v[30:33]
	v_mfma_f32_16x16x32_bf16 v[26:29], v[152:155], v[204:207], v[26:29]
	v_mfma_f32_16x16x32_bf16 v[14:17], v[144:147], v[212:215], v[14:17]
	v_mfma_f32_16x16x32_bf16 v[10:13], v[152:155], v[212:215], v[10:13]
	v_mfma_f32_16x16x32_bf16 v[62:65], v[148:151], v[180:183], v[62:65]
	v_mfma_f32_16x16x32_bf16 v[58:61], v[156:159], v[180:183], v[58:61]
	v_mfma_f32_16x16x32_bf16 v[46:49], v[148:151], v[200:203], v[46:49]
	v_mfma_f32_16x16x32_bf16 v[42:45], v[156:159], v[200:203], v[42:45]
	v_mfma_f32_16x16x32_bf16 v[30:33], v[148:151], v[208:211], v[30:33]
	v_mfma_f32_16x16x32_bf16 v[26:29], v[156:159], v[208:211], v[26:29]
	v_mfma_f32_16x16x32_bf16 v[14:17], v[148:151], v[216:219], v[14:17]
	v_mfma_f32_16x16x32_bf16 v[10:13], v[156:159], v[216:219], v[10:13]
	s_setprio 0
	s_setprio 1
	v_mfma_f32_16x16x32_bf16 v[54:57], v[160:163], v[176:179], v[54:57]
	v_mfma_f32_16x16x32_bf16 v[50:53], v[168:171], v[176:179], v[50:53]
	v_mfma_f32_16x16x32_bf16 v[38:41], v[160:163], v[196:199], v[38:41]
	v_mfma_f32_16x16x32_bf16 v[34:37], v[168:171], v[196:199], v[34:37]
	v_mfma_f32_16x16x32_bf16 v[22:25], v[160:163], v[204:207], v[22:25]
	v_mfma_f32_16x16x32_bf16 v[18:21], v[168:171], v[204:207], v[18:21]
	v_mfma_f32_16x16x32_bf16 v[6:9], v[160:163], v[212:215], v[6:9]
	v_mfma_f32_16x16x32_bf16 v[2:5], v[168:171], v[212:215], v[2:5]
	v_mfma_f32_16x16x32_bf16 v[54:57], v[164:167], v[180:183], v[54:57]
	v_mfma_f32_16x16x32_bf16 v[50:53], v[172:175], v[180:183], v[50:53]
	v_mfma_f32_16x16x32_bf16 v[38:41], v[164:167], v[200:203], v[38:41]
	v_mfma_f32_16x16x32_bf16 v[34:37], v[172:175], v[200:203], v[34:37]
	v_mfma_f32_16x16x32_bf16 v[22:25], v[164:167], v[208:211], v[22:25]
	v_mfma_f32_16x16x32_bf16 v[18:21], v[172:175], v[208:211], v[18:21]
	v_mfma_f32_16x16x32_bf16 v[6:9], v[164:167], v[216:219], v[6:9]
	v_mfma_f32_16x16x32_bf16 v[2:5], v[172:175], v[216:219], v[2:5]
	s_setprio 0
	s_barrier
	s_add_i32 s43, s43, 2
	s_add_u32 s54, s54, 0x100
	s_addc_u32 s55, s55, 0

.LBB0_1462:
	s_add_u32 s2, s56, 0x100
	s_addc_u32 s24, s57, 0
	s_add_u32 s56, s58, 0x40080
	s_waitcnt lgkmcnt(0)
	s_addc_u32 s57, s59, 0
	s_mov_b32 s25, -2
	s_add_u32 s14, s56, 0xfffc0080
	s_addc_u32 s15, s57, -1
	s_add_i32 s49, 0, 0x11000
	s_cmp_eq_u32 s25, 12
	s_cselect_b32 s15, s53, s15
	s_cselect_b32 s14, s52, s14
	v_add_u32_e32 v155, s49, v1
	s_cselect_b32 s35, s51, s24
	s_cselect_b32 s34, s50, s2
	s_add_i32 s55, 0, 0x15000
	ds_read_b128 v[156:159], v155
	ds_read_b128 v[160:163], v155 offset:1024
	ds_read_b128 v[164:167], v155 offset:2048
	ds_read_b128 v[168:171], v155 offset:3072
	v_add_u32_e32 v155, s55, v1
	ds_read_b128 v[172:175], v155
	ds_read_b128 v[176:179], v155 offset:1024
	ds_read_b128 v[180:183], v155 offset:2048
	ds_read_b128 v[196:199], v155 offset:3072
	v_lshl_add_u64 v[184:185], s[56:57], 0, v[152:153]
	s_add_i32 m0, s61, 0xd000
	ds_read_b128 v[200:203], v154 offset:4096
	ds_read_b128 v[204:207], v154 offset:5120
	ds_read_b128 v[208:211], v154 offset:6144
	ds_read_b128 v[212:215], v154 offset:7168
	ds_read_b128 v[216:219], v154 offset:8192
	ds_read_b128 v[220:223], v154 offset:9216
	ds_read_b128 v[240:243], v154 offset:10240
	ds_read_b128 v[244:247], v154 offset:11264
	global_load_lds_dwordx4 v[184:185], off
	v_lshl_add_u64 v[184:185], v[184:185], 0, s[82:83]
	s_add_i32 m0, s61, 0xf000
	s_nop 0
	global_load_lds_dwordx4 v[184:185], off
	s_waitcnt vmcnt(8)
	s_waitcnt lgkmcnt(0)
	s_barrier
	s_setprio 1
	s_waitcnt lgkmcnt(0)
	v_mfma_f32_16x16x32_bf16 v[142:145], v[156:159], v[200:203], 0
	v_mfma_f32_16x16x32_bf16 v[138:141], v[164:167], v[200:203], 0
	v_mfma_f32_16x16x32_bf16 v[126:129], v[156:159], v[208:211], 0
	v_mfma_f32_16x16x32_bf16 v[122:125], v[164:167], v[208:211], 0
	v_mfma_f32_16x16x32_bf16 v[110:113], v[156:159], v[216:219], 0
	v_mfma_f32_16x16x32_bf16 v[106:109], v[164:167], v[216:219], 0
	v_mfma_f32_16x16x32_bf16 v[94:97], v[156:159], v[240:243], 0
	v_mfma_f32_16x16x32_bf16 v[90:93], v[164:167], v[240:243], 0
	v_mfma_f32_16x16x32_bf16 v[142:145], v[160:163], v[204:207], v[142:145]
	v_mfma_f32_16x16x32_bf16 v[138:141], v[168:171], v[204:207], v[138:141]
	v_mfma_f32_16x16x32_bf16 v[126:129], v[160:163], v[212:215], v[126:129]
	v_mfma_f32_16x16x32_bf16 v[122:125], v[168:171], v[212:215], v[122:125]
	v_mfma_f32_16x16x32_bf16 v[110:113], v[160:163], v[220:223], v[110:113]
	v_mfma_f32_16x16x32_bf16 v[106:109], v[168:171], v[220:223], v[106:109]
	v_mfma_f32_16x16x32_bf16 v[94:97], v[160:163], v[244:247], v[94:97]
	v_mfma_f32_16x16x32_bf16 v[90:93], v[168:171], v[244:247], v[90:93]
	s_setprio 0
	s_setprio 1
	v_mfma_f32_16x16x32_bf16 v[134:137], v[172:175], v[200:203], 0
	v_mfma_f32_16x16x32_bf16 v[130:133], v[180:183], v[200:203], 0
	v_mfma_f32_16x16x32_bf16 v[118:121], v[172:175], v[208:211], 0
	v_mfma_f32_16x16x32_bf16 v[114:117], v[180:183], v[208:211], 0
	v_mfma_f32_16x16x32_bf16 v[102:105], v[172:175], v[216:219], 0
	v_mfma_f32_16x16x32_bf16 v[98:101], v[180:183], v[216:219], 0
	v_mfma_f32_16x16x32_bf16 v[86:89], v[172:175], v[240:243], 0
	v_mfma_f32_16x16x32_bf16 v[82:85], v[180:183], v[240:243], 0
	v_mfma_f32_16x16x32_bf16 v[134:137], v[176:179], v[204:207], v[134:137]
	v_mfma_f32_16x16x32_bf16 v[130:133], v[196:199], v[204:207], v[130:133]
	v_mfma_f32_16x16x32_bf16 v[118:121], v[176:179], v[212:215], v[118:121]
	v_mfma_f32_16x16x32_bf16 v[114:117], v[196:199], v[212:215], v[114:117]
	v_mfma_f32_16x16x32_bf16 v[102:105], v[176:179], v[220:223], v[102:105]
	v_mfma_f32_16x16x32_bf16 v[98:101], v[196:199], v[220:223], v[98:101]
	v_mfma_f32_16x16x32_bf16 v[86:89], v[176:179], v[244:247], v[86:89]
	v_mfma_f32_16x16x32_bf16 v[82:85], v[196:199], v[244:247], v[82:85]
	s_setprio 0
	s_barrier
	v_lshl_add_u64 v[184:185], s[34:35], 0, v[186:187]
	s_add_i32 s34, s49, s28
	s_mov_b32 m0, s34
	ds_read_b128 v[200:203], v154 offset:20480
	ds_read_b128 v[204:207], v154 offset:21504
	ds_read_b128 v[208:211], v154 offset:22528
	ds_read_b128 v[212:215], v154 offset:23552
	ds_read_b128 v[216:219], v154 offset:24576
	ds_read_b128 v[220:223], v154 offset:25600
	ds_read_b128 v[240:243], v154 offset:26624
	ds_read_b128 v[244:247], v154 offset:27648
	global_load_lds_dwordx4 v[184:185], off
	v_lshl_add_u64 v[192:193], v[184:185], 0, s[82:83]
	s_add_i32 m0, s34, 0x2000
	s_add_i32 s34, s55, s28
	global_load_lds_dwordx4 v[192:193], off
	v_lshl_add_u64 v[192:193], v[184:185], 0, s[64:65]
	s_mov_b32 m0, s34
	s_nop 0
	global_load_lds_dwordx4 v[192:193], off
	v_lshl_add_u64 v[192:193], v[184:185], 0, s[86:87]
	s_add_i32 m0, s34, 0x2000
	s_nop 0
	global_load_lds_dwordx4 v[192:193], off
	v_lshl_add_u64 v[192:193], s[14:15], 0, v[146:147]
	s_mov_b32 m0, s68
	v_lshl_add_u64 v[224:225], v[192:193], 0, s[82:83]
	global_load_lds_dwordx4 v[192:193], off
	s_mov_b32 m0, s69
	s_nop 0
	global_load_lds_dwordx4 v[224:225], off
	s_waitcnt vmcnt(8)
	s_waitcnt lgkmcnt(0)
	s_barrier
	s_setprio 1
	s_waitcnt lgkmcnt(0)
	v_mfma_f32_16x16x32_bf16 v[78:81], v[156:159], v[200:203], 0
	v_mfma_f32_16x16x32_bf16 v[74:77], v[164:167], v[200:203], 0
	v_mfma_f32_16x16x32_bf16 v[62:65], v[156:159], v[208:211], 0
	v_mfma_f32_16x16x32_bf16 v[58:61], v[164:167], v[208:211], 0
	v_mfma_f32_16x16x32_bf16 v[46:49], v[156:159], v[216:219], 0
	v_mfma_f32_16x16x32_bf16 v[42:45], v[164:167], v[216:219], 0
	v_mfma_f32_16x16x32_bf16 v[30:33], v[156:159], v[240:243], 0
	v_mfma_f32_16x16x32_bf16 v[26:29], v[164:167], v[240:243], 0
	v_mfma_f32_16x16x32_bf16 v[78:81], v[160:163], v[204:207], v[78:81]
	v_mfma_f32_16x16x32_bf16 v[74:77], v[168:171], v[204:207], v[74:77]
	v_mfma_f32_16x16x32_bf16 v[62:65], v[160:163], v[212:215], v[62:65]
	v_mfma_f32_16x16x32_bf16 v[58:61], v[168:171], v[212:215], v[58:61]
	v_mfma_f32_16x16x32_bf16 v[46:49], v[160:163], v[220:223], v[46:49]
	v_mfma_f32_16x16x32_bf16 v[42:45], v[168:171], v[220:223], v[42:45]
	v_mfma_f32_16x16x32_bf16 v[30:33], v[160:163], v[244:247], v[30:33]
	v_mfma_f32_16x16x32_bf16 v[26:29], v[168:171], v[244:247], v[26:29]
	s_setprio 0
	s_setprio 1
	v_mfma_f32_16x16x32_bf16 v[70:73], v[172:175], v[200:203], 0
	v_mfma_f32_16x16x32_bf16 v[66:69], v[180:183], v[200:203], 0
	v_mfma_f32_16x16x32_bf16 v[54:57], v[172:175], v[208:211], 0
	v_mfma_f32_16x16x32_bf16 v[50:53], v[180:183], v[208:211], 0
	v_mfma_f32_16x16x32_bf16 v[38:41], v[172:175], v[216:219], 0
	v_mfma_f32_16x16x32_bf16 v[34:37], v[180:183], v[216:219], 0
	v_mfma_f32_16x16x32_bf16 v[22:25], v[172:175], v[240:243], 0
	v_mfma_f32_16x16x32_bf16 v[18:21], v[180:183], v[240:243], 0
	v_mfma_f32_16x16x32_bf16 v[70:73], v[176:179], v[204:207], v[70:73]
	v_mfma_f32_16x16x32_bf16 v[66:69], v[196:199], v[204:207], v[66:69]
	v_mfma_f32_16x16x32_bf16 v[54:57], v[176:179], v[212:215], v[54:57]
	v_mfma_f32_16x16x32_bf16 v[50:53], v[196:199], v[212:215], v[50:53]
	v_mfma_f32_16x16x32_bf16 v[38:41], v[176:179], v[220:223], v[38:41]
	v_mfma_f32_16x16x32_bf16 v[34:37], v[196:199], v[220:223], v[34:37]
	v_mfma_f32_16x16x32_bf16 v[22:25], v[176:179], v[244:247], v[22:25]
	v_mfma_f32_16x16x32_bf16 v[18:21], v[196:199], v[244:247], v[18:21]
	s_setprio 0
	s_barrier
	s_add_i32 s14, 0, 0x19000
	v_add_u32_e32 v155, s14, v1
	s_add_i32 s15, 0, 0x1d000
	ds_read_b128 v[156:159], v155
	ds_read_b128 v[160:163], v155 offset:1024
	ds_read_b128 v[164:167], v155 offset:2048
	ds_read_b128 v[168:171], v155 offset:3072
	v_add_u32_e32 v155, s15, v1
	ds_read_b128 v[172:175], v155
	ds_read_b128 v[176:179], v155 offset:1024
	ds_read_b128 v[180:183], v155 offset:2048
	ds_read_b128 v[196:199], v155 offset:3072
	s_mov_b32 m0, s70
	v_lshl_add_u64 v[224:225], v[192:193], 0, s[64:65]
	ds_read_b128 v[200:203], v154 offset:36864
	ds_read_b128 v[204:207], v154 offset:37888
	ds_read_b128 v[208:211], v154 offset:38912
	ds_read_b128 v[212:215], v154 offset:39936
	ds_read_b128 v[216:219], v154 offset:40960
	ds_read_b128 v[220:223], v154 offset:41984
	ds_read_b128 v[240:243], v154 offset:43008
	ds_read_b128 v[244:247], v154 offset:44032
	global_load_lds_dwordx4 v[224:225], off
	v_lshl_add_u64 v[224:225], v[192:193], 0, s[86:87]
	s_mov_b32 m0, s71
	s_nop 0
	global_load_lds_dwordx4 v[224:225], off
	s_waitcnt vmcnt(8)
	s_waitcnt lgkmcnt(0)
	s_barrier
	s_setprio 1
	s_waitcnt lgkmcnt(0)
	v_mfma_f32_16x16x32_bf16 v[142:145], v[156:159], v[200:203], v[142:145]
	v_mfma_f32_16x16x32_bf16 v[138:141], v[164:167], v[200:203], v[138:141]
	v_mfma_f32_16x16x32_bf16 v[126:129], v[156:159], v[208:211], v[126:129]
	v_mfma_f32_16x16x32_bf16 v[122:125], v[164:167], v[208:211], v[122:125]
	v_mfma_f32_16x16x32_bf16 v[110:113], v[156:159], v[216:219], v[110:113]
	v_mfma_f32_16x16x32_bf16 v[106:109], v[164:167], v[216:219], v[106:109]
	v_mfma_f32_16x16x32_bf16 v[94:97], v[156:159], v[240:243], v[94:97]
	v_mfma_f32_16x16x32_bf16 v[90:93], v[164:167], v[240:243], v[90:93]
	v_mfma_f32_16x16x32_bf16 v[142:145], v[160:163], v[204:207], v[142:145]
	v_mfma_f32_16x16x32_bf16 v[138:141], v[168:171], v[204:207], v[138:141]
	v_mfma_f32_16x16x32_bf16 v[126:129], v[160:163], v[212:215], v[126:129]
	v_mfma_f32_16x16x32_bf16 v[122:125], v[168:171], v[212:215], v[122:125]
	v_mfma_f32_16x16x32_bf16 v[110:113], v[160:163], v[220:223], v[110:113]
	v_mfma_f32_16x16x32_bf16 v[106:109], v[168:171], v[220:223], v[106:109]
	v_mfma_f32_16x16x32_bf16 v[94:97], v[160:163], v[244:247], v[94:97]
	v_mfma_f32_16x16x32_bf16 v[90:93], v[168:171], v[244:247], v[90:93]
	s_setprio 0
	s_setprio 1
	v_mfma_f32_16x16x32_bf16 v[134:137], v[172:175], v[200:203], v[134:137]
	v_mfma_f32_16x16x32_bf16 v[130:133], v[180:183], v[200:203], v[130:133]
	v_mfma_f32_16x16x32_bf16 v[118:121], v[172:175], v[208:211], v[118:121]
	v_mfma_f32_16x16x32_bf16 v[114:117], v[180:183], v[208:211], v[114:117]
	v_mfma_f32_16x16x32_bf16 v[102:105], v[172:175], v[216:219], v[102:105]
	v_mfma_f32_16x16x32_bf16 v[98:101], v[180:183], v[216:219], v[98:101]
	v_mfma_f32_16x16x32_bf16 v[86:89], v[172:175], v[240:243], v[86:89]
	v_mfma_f32_16x16x32_bf16 v[82:85], v[180:183], v[240:243], v[82:85]
	v_mfma_f32_16x16x32_bf16 v[134:137], v[176:179], v[204:207], v[134:137]
	v_mfma_f32_16x16x32_bf16 v[130:133], v[196:199], v[204:207], v[130:133]
	v_mfma_f32_16x16x32_bf16 v[118:121], v[176:179], v[212:215], v[118:121]
	v_mfma_f32_16x16x32_bf16 v[114:117], v[196:199], v[212:215], v[114:117]
	v_mfma_f32_16x16x32_bf16 v[102:105], v[176:179], v[220:223], v[102:105]
	v_mfma_f32_16x16x32_bf16 v[98:101], v[196:199], v[220:223], v[98:101]
	v_mfma_f32_16x16x32_bf16 v[86:89], v[176:179], v[244:247], v[86:89]
	v_mfma_f32_16x16x32_bf16 v[82:85], v[196:199], v[244:247], v[82:85]
	s_setprio 0
	s_barrier
	s_add_i32 s14, s14, s28
	v_lshl_add_u64 v[224:225], v[184:185], 0, s[92:93]
	s_mov_b32 m0, s14
	ds_read_b128 v[200:203], v154 offset:53248
	ds_read_b128 v[204:207], v154 offset:54272
	ds_read_b128 v[208:211], v154 offset:55296
	ds_read_b128 v[212:215], v154 offset:56320
	ds_read_b128 v[216:219], v154 offset:57344
	ds_read_b128 v[220:223], v154 offset:58368
	ds_read_b128 v[240:243], v154 offset:59392
	ds_read_b128 v[244:247], v154 offset:60416
	global_load_lds_dwordx4 v[224:225], off
	v_lshl_add_u64 v[224:225], v[184:185], 0, s[4:5]
	s_add_i32 m0, s14, 0x2000
	s_add_i32 s14, s15, s28
	global_load_lds_dwordx4 v[224:225], off
	v_lshl_add_u64 v[224:225], v[184:185], 0, s[6:7]
	s_mov_b32 m0, s14
	v_lshl_add_u64 v[184:185], v[184:185], 0, s[8:9]
	global_load_lds_dwordx4 v[224:225], off
	s_add_i32 m0, s14, 0x2000
	s_nop 0
	global_load_lds_dwordx4 v[184:185], off
	v_lshl_add_u64 v[184:185], v[192:193], 0, s[92:93]
	s_mov_b32 m0, s75
	s_nop 0
	global_load_lds_dwordx4 v[184:185], off
	v_lshl_add_u64 v[184:185], v[192:193], 0, s[4:5]
	s_mov_b32 m0, s76
	s_nop 0
	global_load_lds_dwordx4 v[184:185], off
	s_waitcnt vmcnt(8)
	s_waitcnt lgkmcnt(0)
	s_barrier
	s_setprio 1
	s_waitcnt lgkmcnt(0)
	v_mfma_f32_16x16x32_bf16 v[78:81], v[156:159], v[200:203], v[78:81]
	v_mfma_f32_16x16x32_bf16 v[74:77], v[164:167], v[200:203], v[74:77]
	v_mfma_f32_16x16x32_bf16 v[62:65], v[156:159], v[208:211], v[62:65]
	v_mfma_f32_16x16x32_bf16 v[58:61], v[164:167], v[208:211], v[58:61]
	v_mfma_f32_16x16x32_bf16 v[46:49], v[156:159], v[216:219], v[46:49]
	v_mfma_f32_16x16x32_bf16 v[42:45], v[164:167], v[216:219], v[42:45]
	v_mfma_f32_16x16x32_bf16 v[30:33], v[156:159], v[240:243], v[30:33]
	v_mfma_f32_16x16x32_bf16 v[26:29], v[164:167], v[240:243], v[26:29]
	v_mfma_f32_16x16x32_bf16 v[78:81], v[160:163], v[204:207], v[78:81]
	v_mfma_f32_16x16x32_bf16 v[74:77], v[168:171], v[204:207], v[74:77]
	v_mfma_f32_16x16x32_bf16 v[62:65], v[160:163], v[212:215], v[62:65]
	v_mfma_f32_16x16x32_bf16 v[58:61], v[168:171], v[212:215], v[58:61]
	v_mfma_f32_16x16x32_bf16 v[46:49], v[160:163], v[220:223], v[46:49]
	v_mfma_f32_16x16x32_bf16 v[42:45], v[168:171], v[220:223], v[42:45]
	v_mfma_f32_16x16x32_bf16 v[30:33], v[160:163], v[244:247], v[30:33]
	v_mfma_f32_16x16x32_bf16 v[26:29], v[168:171], v[244:247], v[26:29]
	s_setprio 0
	s_setprio 1
	v_mfma_f32_16x16x32_bf16 v[70:73], v[172:175], v[200:203], v[70:73]
	v_mfma_f32_16x16x32_bf16 v[66:69], v[180:183], v[200:203], v[66:69]
	v_mfma_f32_16x16x32_bf16 v[54:57], v[172:175], v[208:211], v[54:57]
	v_mfma_f32_16x16x32_bf16 v[50:53], v[180:183], v[208:211], v[50:53]
	v_mfma_f32_16x16x32_bf16 v[38:41], v[172:175], v[216:219], v[38:41]
	v_mfma_f32_16x16x32_bf16 v[34:37], v[180:183], v[216:219], v[34:37]
	v_mfma_f32_16x16x32_bf16 v[22:25], v[172:175], v[240:243], v[22:25]
	v_mfma_f32_16x16x32_bf16 v[18:21], v[180:183], v[240:243], v[18:21]
	v_mfma_f32_16x16x32_bf16 v[70:73], v[176:179], v[204:207], v[70:73]
	v_mfma_f32_16x16x32_bf16 v[66:69], v[196:199], v[204:207], v[66:69]
	v_mfma_f32_16x16x32_bf16 v[54:57], v[176:179], v[212:215], v[54:57]
	v_mfma_f32_16x16x32_bf16 v[50:53], v[196:199], v[212:215], v[50:53]
	v_mfma_f32_16x16x32_bf16 v[38:41], v[176:179], v[220:223], v[38:41]
	v_mfma_f32_16x16x32_bf16 v[34:37], v[196:199], v[220:223], v[34:37]
	v_mfma_f32_16x16x32_bf16 v[22:25], v[176:179], v[244:247], v[22:25]
	v_mfma_f32_16x16x32_bf16 v[18:21], v[196:199], v[244:247], v[18:21]
	s_setprio 0
	s_barrier
	s_add_i32 s25, s25, 2
	s_add_u32 s2, s2, 0x100
	s_addc_u32 s24, s24, 0
	s_add_u32 s56, s56, 0x100
	s_addc_u32 s57, s57, 0
